# speedup vs baseline: 1.1146x; 1.1146x over previous
.LBB8_27:
	ds_read_b128 v[72:75], v231
	ds_read_b128 v[80:83], v231 offset:1024
	ds_read_b128 v[88:91], v231 offset:2048
	ds_read_b128 v[92:95], v231 offset:3072
	s_add_u32 s40, s38, 0xfffd0080
	s_addc_u32 s41, s39, -1
	s_cmp_eq_u32 s87, 8
	s_cselect_b32 s43, s9, s41
	s_cselect_b32 s42, s8, s40
	s_cselect_b32 s41, s1, s86
	s_cselect_b32 s40, s0, s85
	v_lshl_add_u64 v[190:191], s[38:39], 0, v[184:185]
	s_add_i32 m0, s51, 0xc000
	ds_read_b128 v[136:139], v232
	ds_read_b128 v[148:151], v232 offset:1024
	ds_read_b128 v[152:155], v232 offset:2048
	ds_read_b128 v[156:159], v232 offset:3072
	ds_read_b128 v[160:163], v232 offset:4096
	ds_read_b128 v[164:167], v232 offset:5120
	ds_read_b128 v[168:171], v232 offset:6144
	ds_read_b128 v[172:175], v232 offset:7168
	global_load_lds_dwordx4 v[190:191], off
	v_lshl_add_u64 v[190:191], s[38:39], 0, v[186:187]
	s_add_i32 m0, s51, 0xe000
	s_nop 0
	global_load_lds_dwordx4 v[190:191], off
	s_waitcnt lgkmcnt(8)
	s_barrier
	s_waitcnt lgkmcnt(0)
	s_setprio 1
	s_waitcnt lgkmcnt(0)
	v_mfma_f32_16x16x32_f16 v[144:147], v[72:75], v[136:139], v[144:147]
	v_mfma_f32_16x16x32_f16 v[140:143], v[88:91], v[136:139], v[140:143]
	v_mfma_f32_16x16x32_f16 v[124:127], v[72:75], v[152:155], v[124:127]
	v_mfma_f32_16x16x32_f16 v[120:123], v[88:91], v[152:155], v[120:123]
	v_mfma_f32_16x16x32_f16 v[108:111], v[72:75], v[160:163], v[108:111]
	v_mfma_f32_16x16x32_f16 v[104:107], v[88:91], v[160:163], v[104:107]
	v_mfma_f32_16x16x32_f16 v[84:87], v[72:75], v[168:171], v[84:87]
	v_mfma_f32_16x16x32_f16 v[76:79], v[88:91], v[168:171], v[76:79]
	v_mfma_f32_16x16x32_f16 v[144:147], v[80:83], v[148:151], v[144:147]
	v_mfma_f32_16x16x32_f16 v[140:143], v[92:95], v[148:151], v[140:143]
	v_mfma_f32_16x16x32_f16 v[124:127], v[80:83], v[156:159], v[124:127]
	v_mfma_f32_16x16x32_f16 v[120:123], v[92:95], v[156:159], v[120:123]
	v_mfma_f32_16x16x32_f16 v[108:111], v[80:83], v[164:167], v[108:111]
	v_mfma_f32_16x16x32_f16 v[104:107], v[92:95], v[164:167], v[104:107]
	v_mfma_f32_16x16x32_f16 v[84:87], v[80:83], v[172:175], v[84:87]
	v_mfma_f32_16x16x32_f16 v[76:79], v[92:95], v[172:175], v[76:79]
	s_setprio 0
	s_barrier
	s_add_i32 s88, s70, s50
	v_lshl_add_u64 v[206:207], s[40:41], 0, v[178:179]
	s_mov_b32 m0, s88
	ds_read_b128 v[190:193], v233
	ds_read_b128 v[194:197], v233 offset:1024
	ds_read_b128 v[198:201], v233 offset:2048
	ds_read_b128 v[202:205], v233 offset:3072
	global_load_lds_dwordx4 v[206:207], off
	v_lshl_add_u64 v[208:209], s[40:41], 0, v[182:183]
	s_add_i32 m0, s88, 0x2000
	s_nop 0
	global_load_lds_dwordx4 v[208:209], off
	s_barrier
	s_waitcnt lgkmcnt(0)
	s_setprio 1
	s_waitcnt lgkmcnt(0)
	v_mfma_f32_16x16x32_f16 v[132:135], v[190:193], v[136:139], v[132:135]
	v_mfma_f32_16x16x32_f16 v[128:131], v[198:201], v[136:139], v[128:131]
	v_mfma_f32_16x16x32_f16 v[116:119], v[190:193], v[152:155], v[116:119]
	v_mfma_f32_16x16x32_f16 v[112:115], v[198:201], v[152:155], v[112:115]
	v_mfma_f32_16x16x32_f16 v[100:103], v[190:193], v[160:163], v[100:103]
	v_mfma_f32_16x16x32_f16 v[96:99], v[198:201], v[160:163], v[96:99]
	v_mfma_f32_16x16x32_f16 v[68:71], v[190:193], v[168:171], v[68:71]
	v_mfma_f32_16x16x32_f16 v[64:67], v[198:201], v[168:171], v[64:67]
	v_mfma_f32_16x16x32_f16 v[132:135], v[194:197], v[148:151], v[132:135]
	v_mfma_f32_16x16x32_f16 v[128:131], v[202:205], v[148:151], v[128:131]
	v_mfma_f32_16x16x32_f16 v[116:119], v[194:197], v[156:159], v[116:119]
	v_mfma_f32_16x16x32_f16 v[112:115], v[202:205], v[156:159], v[112:115]
	v_mfma_f32_16x16x32_f16 v[100:103], v[194:197], v[164:167], v[100:103]
	v_mfma_f32_16x16x32_f16 v[96:99], v[202:205], v[164:167], v[96:99]
	v_mfma_f32_16x16x32_f16 v[68:71], v[194:197], v[172:175], v[68:71]
	v_mfma_f32_16x16x32_f16 v[64:67], v[202:205], v[172:175], v[64:67]
	s_setprio 0
	s_mov_b32 m0, s51
	v_lshl_add_u64 v[210:211], s[42:43], 0, v[176:177]
	s_barrier
	ds_read_b128 v[136:139], v232 offset:16384
	ds_read_b128 v[148:151], v232 offset:17408
	ds_read_b128 v[152:155], v232 offset:18432
	ds_read_b128 v[156:159], v232 offset:19456
	ds_read_b128 v[160:163], v232 offset:20480
	ds_read_b128 v[164:167], v232 offset:21504
	ds_read_b128 v[168:171], v232 offset:22528
	ds_read_b128 v[172:175], v232 offset:23552
	global_load_lds_dwordx4 v[210:211], off
	v_lshl_add_u64 v[212:213], s[42:43], 0, v[180:181]
	s_mov_b32 m0, s52
	s_nop 0
	global_load_lds_dwordx4 v[212:213], off
	s_barrier
	s_waitcnt lgkmcnt(0)
	s_setprio 1
	s_waitcnt lgkmcnt(0)
	v_mfma_f32_16x16x32_f16 v[60:63], v[72:75], v[136:139], v[60:63]
	v_mfma_f32_16x16x32_f16 v[56:59], v[88:91], v[136:139], v[56:59]
	v_mfma_f32_16x16x32_f16 v[44:47], v[72:75], v[152:155], v[44:47]
	v_mfma_f32_16x16x32_f16 v[40:43], v[88:91], v[152:155], v[40:43]
	v_mfma_f32_16x16x32_f16 v[28:31], v[72:75], v[160:163], v[28:31]
	v_mfma_f32_16x16x32_f16 v[24:27], v[88:91], v[160:163], v[24:27]
	v_mfma_f32_16x16x32_f16 v[12:15], v[72:75], v[168:171], v[12:15]
	v_mfma_f32_16x16x32_f16 v[8:11], v[88:91], v[168:171], v[8:11]
	v_mfma_f32_16x16x32_f16 v[60:63], v[80:83], v[148:151], v[60:63]
	v_mfma_f32_16x16x32_f16 v[56:59], v[92:95], v[148:151], v[56:59]
	v_mfma_f32_16x16x32_f16 v[44:47], v[80:83], v[156:159], v[44:47]
	v_mfma_f32_16x16x32_f16 v[40:43], v[92:95], v[156:159], v[40:43]
	v_mfma_f32_16x16x32_f16 v[28:31], v[80:83], v[164:167], v[28:31]
	v_mfma_f32_16x16x32_f16 v[24:27], v[92:95], v[164:167], v[24:27]
	v_mfma_f32_16x16x32_f16 v[12:15], v[80:83], v[172:175], v[12:15]
	v_mfma_f32_16x16x32_f16 v[8:11], v[92:95], v[172:175], v[8:11]
	s_setprio 0
	s_barrier
	s_add_u32 s88, s40, 0xc000
	s_addc_u32 s89, s41, 0
	s_add_i32 s90, s71, s50
	v_lshl_add_u64 v[72:73], s[88:89], 0, v[178:179]
	s_mov_b32 m0, s90
	s_nop 0
	global_load_lds_dwordx4 v[72:73], off
	v_lshl_add_u64 v[72:73], s[88:89], 0, v[182:183]
	s_add_i32 m0, s90, 0x2000
	s_nop 0
	global_load_lds_dwordx4 v[72:73], off
	s_waitcnt vmcnt(6)
	s_barrier
	s_setprio 1
	v_mfma_f32_16x16x32_f16 v[52:55], v[190:193], v[136:139], v[52:55]
	v_mfma_f32_16x16x32_f16 v[48:51], v[198:201], v[136:139], v[48:51]
	v_mfma_f32_16x16x32_f16 v[36:39], v[190:193], v[152:155], v[36:39]
	v_mfma_f32_16x16x32_f16 v[32:35], v[198:201], v[152:155], v[32:35]
	v_mfma_f32_16x16x32_f16 v[20:23], v[190:193], v[160:163], v[20:23]
	v_mfma_f32_16x16x32_f16 v[16:19], v[198:201], v[160:163], v[16:19]
	v_mfma_f32_16x16x32_f16 v[4:7], v[190:193], v[168:171], v[4:7]
	v_mfma_f32_16x16x32_f16 v[0:3], v[198:201], v[168:171], v[0:3]
	v_mfma_f32_16x16x32_f16 v[52:55], v[194:197], v[148:151], v[52:55]
	v_mfma_f32_16x16x32_f16 v[48:51], v[202:205], v[148:151], v[48:51]
	v_mfma_f32_16x16x32_f16 v[36:39], v[194:197], v[156:159], v[36:39]
	v_mfma_f32_16x16x32_f16 v[32:35], v[202:205], v[156:159], v[32:35]
	v_mfma_f32_16x16x32_f16 v[20:23], v[194:197], v[164:167], v[20:23]
	v_mfma_f32_16x16x32_f16 v[16:19], v[202:205], v[164:167], v[16:19]
	v_mfma_f32_16x16x32_f16 v[4:7], v[194:197], v[172:175], v[4:7]
	v_mfma_f32_16x16x32_f16 v[0:3], v[202:205], v[172:175], v[0:3]
	s_setprio 0
	s_add_i32 s88, 0, 0x18000
	v_add_u32_e32 v92, s88, v228
	s_barrier
	ds_read_b128 v[72:75], v92
	ds_read_b128 v[80:83], v92 offset:1024
	ds_read_b128 v[88:91], v92 offset:2048
	ds_read_b128 v[92:95], v92 offset:3072
	s_add_u32 s42, s42, 0x30000
	s_addc_u32 s43, s43, 0
	s_mov_b32 m0, s53
	v_lshl_add_u64 v[190:191], s[42:43], 0, v[176:177]
	ds_read_b128 v[136:139], v232 offset:32768
	ds_read_b128 v[148:151], v232 offset:33792
	ds_read_b128 v[152:155], v232 offset:34816
	ds_read_b128 v[156:159], v232 offset:35840
	ds_read_b128 v[160:163], v232 offset:36864
	ds_read_b128 v[164:167], v232 offset:37888
	ds_read_b128 v[168:171], v232 offset:38912
	ds_read_b128 v[172:175], v232 offset:39936
	global_load_lds_dwordx4 v[190:191], off
	v_lshl_add_u64 v[190:191], s[42:43], 0, v[180:181]
	s_mov_b32 m0, s54
	s_nop 0
	global_load_lds_dwordx4 v[190:191], off
	s_waitcnt lgkmcnt(8)
	s_barrier
	s_waitcnt lgkmcnt(0)
	s_setprio 1
	s_waitcnt lgkmcnt(0)
	v_mfma_f32_16x16x32_f16 v[144:147], v[72:75], v[136:139], v[144:147]
	v_mfma_f32_16x16x32_f16 v[140:143], v[88:91], v[136:139], v[140:143]
	v_mfma_f32_16x16x32_f16 v[124:127], v[72:75], v[152:155], v[124:127]
	v_mfma_f32_16x16x32_f16 v[120:123], v[88:91], v[152:155], v[120:123]
	v_mfma_f32_16x16x32_f16 v[108:111], v[72:75], v[160:163], v[108:111]
	v_mfma_f32_16x16x32_f16 v[104:107], v[88:91], v[160:163], v[104:107]
	v_mfma_f32_16x16x32_f16 v[84:87], v[72:75], v[168:171], v[84:87]
	v_mfma_f32_16x16x32_f16 v[76:79], v[88:91], v[168:171], v[76:79]
	v_mfma_f32_16x16x32_f16 v[144:147], v[80:83], v[148:151], v[144:147]
	v_mfma_f32_16x16x32_f16 v[140:143], v[92:95], v[148:151], v[140:143]
	v_mfma_f32_16x16x32_f16 v[124:127], v[80:83], v[156:159], v[124:127]
	v_mfma_f32_16x16x32_f16 v[120:123], v[92:95], v[156:159], v[120:123]
	v_mfma_f32_16x16x32_f16 v[108:111], v[80:83], v[164:167], v[108:111]
	v_mfma_f32_16x16x32_f16 v[104:107], v[92:95], v[164:167], v[104:107]
	v_mfma_f32_16x16x32_f16 v[84:87], v[80:83], v[172:175], v[84:87]
	v_mfma_f32_16x16x32_f16 v[76:79], v[92:95], v[172:175], v[76:79]
	s_setprio 0
	s_barrier
	s_add_i32 s42, 0, 0x1c000
	s_add_i32 s43, s88, s50
	v_add_u32_e32 v202, s42, v228
	v_lshl_add_u64 v[206:207], v[206:207], 0, s[36:37]
	s_mov_b32 m0, s43
	ds_read_b128 v[190:193], v202
	ds_read_b128 v[194:197], v202 offset:1024
	ds_read_b128 v[198:201], v202 offset:2048
	ds_read_b128 v[202:205], v202 offset:3072
	global_load_lds_dwordx4 v[206:207], off
	v_lshl_add_u64 v[206:207], v[208:209], 0, s[36:37]
	s_add_i32 m0, s43, 0x2000
	s_nop 0
	global_load_lds_dwordx4 v[206:207], off
	s_barrier
	s_waitcnt lgkmcnt(0)
	s_setprio 1
	s_waitcnt lgkmcnt(0)
	v_mfma_f32_16x16x32_f16 v[132:135], v[190:193], v[136:139], v[132:135]
	v_mfma_f32_16x16x32_f16 v[128:131], v[198:201], v[136:139], v[128:131]
	v_mfma_f32_16x16x32_f16 v[116:119], v[190:193], v[152:155], v[116:119]
	v_mfma_f32_16x16x32_f16 v[112:115], v[198:201], v[152:155], v[112:115]
	v_mfma_f32_16x16x32_f16 v[100:103], v[190:193], v[160:163], v[100:103]
	v_mfma_f32_16x16x32_f16 v[96:99], v[198:201], v[160:163], v[96:99]
	v_mfma_f32_16x16x32_f16 v[68:71], v[190:193], v[168:171], v[68:71]
	v_mfma_f32_16x16x32_f16 v[64:67], v[198:201], v[168:171], v[64:67]
	v_mfma_f32_16x16x32_f16 v[132:135], v[194:197], v[148:151], v[132:135]
	v_mfma_f32_16x16x32_f16 v[128:131], v[202:205], v[148:151], v[128:131]
	v_mfma_f32_16x16x32_f16 v[116:119], v[194:197], v[156:159], v[116:119]
	v_mfma_f32_16x16x32_f16 v[112:115], v[202:205], v[156:159], v[112:115]
	v_mfma_f32_16x16x32_f16 v[100:103], v[194:197], v[164:167], v[100:103]
	v_mfma_f32_16x16x32_f16 v[96:99], v[202:205], v[164:167], v[96:99]
	v_mfma_f32_16x16x32_f16 v[68:71], v[194:197], v[172:175], v[68:71]
	v_mfma_f32_16x16x32_f16 v[64:67], v[202:205], v[172:175], v[64:67]
	s_setprio 0
	s_mov_b32 m0, s59
	v_lshl_add_u64 v[206:207], v[210:211], 0, s[36:37]
	s_barrier
	ds_read_b128 v[136:139], v232 offset:49152
	ds_read_b128 v[148:151], v232 offset:50176
	ds_read_b128 v[152:155], v232 offset:51200
	ds_read_b128 v[156:159], v232 offset:52224
	ds_read_b128 v[160:163], v232 offset:53248
	ds_read_b128 v[164:167], v232 offset:54272
	ds_read_b128 v[168:171], v232 offset:55296
	ds_read_b128 v[172:175], v232 offset:56320
	global_load_lds_dwordx4 v[206:207], off
	v_lshl_add_u64 v[206:207], v[212:213], 0, s[36:37]
	s_mov_b32 m0, s60
	s_nop 0
	global_load_lds_dwordx4 v[206:207], off
	s_barrier
	s_waitcnt lgkmcnt(0)
	s_setprio 1
	s_waitcnt lgkmcnt(0)
	v_mfma_f32_16x16x32_f16 v[60:63], v[72:75], v[136:139], v[60:63]
	v_mfma_f32_16x16x32_f16 v[56:59], v[88:91], v[136:139], v[56:59]
	v_mfma_f32_16x16x32_f16 v[44:47], v[72:75], v[152:155], v[44:47]
	v_mfma_f32_16x16x32_f16 v[40:43], v[88:91], v[152:155], v[40:43]
	v_mfma_f32_16x16x32_f16 v[28:31], v[72:75], v[160:163], v[28:31]
	v_mfma_f32_16x16x32_f16 v[24:27], v[88:91], v[160:163], v[24:27]
	v_mfma_f32_16x16x32_f16 v[12:15], v[72:75], v[168:171], v[12:15]
	v_mfma_f32_16x16x32_f16 v[8:11], v[88:91], v[168:171], v[8:11]
	v_mfma_f32_16x16x32_f16 v[60:63], v[80:83], v[148:151], v[60:63]
	v_mfma_f32_16x16x32_f16 v[56:59], v[92:95], v[148:151], v[56:59]
	v_mfma_f32_16x16x32_f16 v[44:47], v[80:83], v[156:159], v[44:47]
	v_mfma_f32_16x16x32_f16 v[40:43], v[92:95], v[156:159], v[40:43]
	v_mfma_f32_16x16x32_f16 v[28:31], v[80:83], v[164:167], v[28:31]
	v_mfma_f32_16x16x32_f16 v[24:27], v[92:95], v[164:167], v[24:27]
	v_mfma_f32_16x16x32_f16 v[12:15], v[80:83], v[172:175], v[12:15]
	v_mfma_f32_16x16x32_f16 v[8:11], v[92:95], v[172:175], v[8:11]
	s_setprio 0
	s_barrier
	s_add_u32 s40, s40, 0xc080
	s_addc_u32 s41, s41, 0
	s_add_i32 s42, s42, s50
	v_lshl_add_u64 v[72:73], s[40:41], 0, v[178:179]
	s_mov_b32 m0, s42
	s_nop 0
	global_load_lds_dwordx4 v[72:73], off
	v_lshl_add_u64 v[72:73], s[40:41], 0, v[182:183]
	s_add_i32 m0, s42, 0x2000
	s_nop 0
	global_load_lds_dwordx4 v[72:73], off
	s_waitcnt vmcnt(6)
	s_barrier
	s_setprio 1
	v_mfma_f32_16x16x32_f16 v[52:55], v[190:193], v[136:139], v[52:55]
	v_mfma_f32_16x16x32_f16 v[48:51], v[198:201], v[136:139], v[48:51]
	v_mfma_f32_16x16x32_f16 v[36:39], v[190:193], v[152:155], v[36:39]
	v_mfma_f32_16x16x32_f16 v[32:35], v[198:201], v[152:155], v[32:35]
	v_mfma_f32_16x16x32_f16 v[20:23], v[190:193], v[160:163], v[20:23]
	v_mfma_f32_16x16x32_f16 v[16:19], v[198:201], v[160:163], v[16:19]
	v_mfma_f32_16x16x32_f16 v[4:7], v[190:193], v[168:171], v[4:7]
	v_mfma_f32_16x16x32_f16 v[0:3], v[198:201], v[168:171], v[0:3]
	v_mfma_f32_16x16x32_f16 v[52:55], v[194:197], v[148:151], v[52:55]
	v_mfma_f32_16x16x32_f16 v[48:51], v[202:205], v[148:151], v[48:51]
	v_mfma_f32_16x16x32_f16 v[36:39], v[194:197], v[156:159], v[36:39]
	v_mfma_f32_16x16x32_f16 v[32:35], v[202:205], v[156:159], v[32:35]
	v_mfma_f32_16x16x32_f16 v[20:23], v[194:197], v[164:167], v[20:23]
	v_mfma_f32_16x16x32_f16 v[16:19], v[202:205], v[164:167], v[16:19]
	v_mfma_f32_16x16x32_f16 v[4:7], v[194:197], v[172:175], v[4:7]
	v_mfma_f32_16x16x32_f16 v[0:3], v[202:205], v[172:175], v[0:3]
	s_setprio 0
	s_add_i32 s87, s87, 2
	s_add_u32 s38, s38, 0x100
	s_addc_u32 s39, s39, 0
	s_add_u32 s85, s85, 0x100
	s_addc_u32 s86, s86, 0
	s_cmp_gt_u32 s87, 9
	s_barrier
	s_cbranch_scc0 .LBB8_27
	s_lshl_b32 s38, s84, 8
	s_lshl_b32 s39, s83, 8
	s_add_i32 s38, s38, s58
	s_or_b32 s39, s39, s61
	v_or_b32_e32 v72, s39, v226
	v_or_b32_e32 v220, s38, v227
	v_mov_b64_e32 v[74:75], s[10:11]
	v_mad_i64_i32 v[74:75], s[40:41], v220, s72, v[74:75]
	v_ashrrev_i32_e32 v73, 31, v72
	v_lshl_add_u64 v[214:215], v[72:73], 1, v[74:75]
	v_add_co_u32_e32 v74, vcc, 0x6000, v214
	global_load_dwordx4 v[172:175], v[214:215], off nt
	global_load_dwordx4 v[168:171], v[214:215], off offset:64 nt
	v_addc_co_u32_e32 v75, vcc, 0, v215, vcc
	global_load_dwordx4 v[164:167], v[74:75], off nt
	global_load_dwordx4 v[160:163], v[74:75], off offset:64 nt
	v_add_co_u32_e32 v74, vcc, 0xc000, v214
	v_ashrrev_i32_e32 v221, 31, v220
	s_nop 0
	v_addc_co_u32_e32 v75, vcc, 0, v215, vcc
	global_load_dwordx4 v[156:159], v[74:75], off nt
	global_load_dwordx4 v[152:155], v[74:75], off offset:64 nt
	v_add_co_u32_e32 v74, vcc, s57, v214
	v_lshlrev_b64 v[72:73], 2, v[72:73]
	s_nop 0
	v_addc_co_u32_e32 v75, vcc, 0, v215, vcc
	global_load_dwordx4 v[148:151], v[74:75], off nt
	global_load_dwordx4 v[136:139], v[74:75], off offset:64 nt
	v_lshl_add_u64 v[74:75], v[220:221], 3, s[12:13]
	v_lshl_add_u64 v[238:239], s[14:15], 0, v[72:73]
	global_load_dwordx2 v[224:225], v[74:75], off
	global_load_dwordx2 v[222:223], v[74:75], off offset:128
	global_load_dwordx2 v[218:219], v[74:75], off offset:256
	global_load_dwordx2 v[216:217], v[74:75], off offset:384
	global_load_dwordx2 v[212:213], v[74:75], off offset:1024
	global_load_dwordx2 v[210:211], v[74:75], off offset:1152
	global_load_dwordx2 v[196:197], v[74:75], off offset:1280
	global_load_dwordx2 v[190:191], v[74:75], off offset:1408
	v_lshl_add_u64 v[242:243], s[16:17], 0, v[72:73]
	v_lshl_add_u64 v[246:247], s[18:19], 0, v[72:73]
	global_load_dwordx4 v[88:91], v[238:239], off offset:16
	global_load_dwordx4 v[92:95], v[238:239], off
	global_load_dwordx4 v[72:75], v[242:243], off offset:16
	global_load_dwordx4 v[80:83], v[242:243], off
	global_load_dwordx4 v[192:195], v[246:247], off offset:16
	global_load_dwordx4 v[198:201], v[246:247], off
	v_or_b32_e32 v221, s38, v229
	v_mul_lo_u32 v221, v221, s56
	v_and_b32_e32 v237, 64, v234
	v_add_u32_e32 v237, 64, v237
	s_lshl_b32 s38, s83, 2
	s_mov_b32 s92, 0x30000
	s_mov_b32 s93, 0
	s_mov_b32 s94, 0x6000
	s_mov_b32 s95, 0
	v_lshl_add_u64 v[250:251], v[214:215], 0, s[92:93]
	global_load_dword v252, v[250:251], off
	v_lshl_add_u64 v[250:251], v[250:251], 0, s[94:95]
	global_load_dword v252, v[250:251], off
	v_lshl_add_u64 v[250:251], v[250:251], 0, s[94:95]
	global_load_dword v252, v[250:251], off
	v_lshl_add_u64 v[250:251], v[250:251], 0, s[94:95]
	global_load_dword v252, v[250:251], off
	s_waitcnt vmcnt(0)
	v_pk_add_f32 v[202:203], v[74:75], v[194:195]
	v_pk_add_f32 v[206:207], v[82:83], v[200:201]
	v_pk_add_f32 v[208:209], v[80:81], v[198:199]
	v_pk_add_f32 v[204:205], v[72:73], v[192:193]
	global_load_dwordx4 v[72:75], v[238:239], off offset:144
	global_load_dwordx4 v[80:83], v[238:239], off offset:128
	s_nop 0
	global_load_dwordx4 v[238:241], v[242:243], off offset:144
	global_load_dwordx4 v[192:195], v[242:243], off offset:128
	s_nop 0
	global_load_dwordx4 v[242:245], v[246:247], off offset:144
	s_nop 0
	global_load_dwordx4 v[246:249], v[246:247], off offset:128
	v_pk_add_f32 v[146:147], v[146:147], v[206:207]
	v_pk_add_f32 v[144:145], v[144:145], v[208:209]
	v_pk_add_f32 v[142:143], v[142:143], v[202:203]
	v_pk_add_f32 v[140:141], v[140:141], v[204:205]
	v_pk_add_f32 v[126:127], v[126:127], v[206:207]
	v_pk_add_f32 v[124:125], v[124:125], v[208:209]
	v_pk_add_f32 v[122:123], v[122:123], v[202:203]
	v_pk_add_f32 v[120:121], v[120:121], v[204:205]
	s_waitcnt vmcnt(0)
	v_pk_add_f32 v[198:199], v[194:195], v[248:249]
	v_pk_add_f32 v[194:195], v[238:239], v[242:243]
	v_add_u32_e32 v238, s39, v221
	v_xor_b32_e32 v221, 16, v234
	v_cmp_lt_i32_e32 vcc, v221, v237
	v_xor_b32_e32 v239, 32, v234
	v_pk_add_f32 v[200:201], v[192:193], v[246:247]
	v_cndmask_b32_e32 v221, v234, v221, vcc
	v_cmp_lt_i32_e32 vcc, v239, v237
	v_pk_add_f32 v[192:193], v[240:241], v[244:245]
	v_cvt_f32_f16_e32 v240, v172
	v_cndmask_b32_e32 v237, v234, v239, vcc
	v_cvt_f32_f16_sdwa v239, v172 dst_sel:DWORD dst_unused:UNUSED_PAD src0_sel:WORD_1
	v_cvt_f32_f16_sdwa v241, v173 dst_sel:DWORD dst_unused:UNUSED_PAD src0_sel:WORD_1
	v_cvt_f32_f16_e32 v172, v173
	v_cvt_f32_f16_sdwa v242, v174 dst_sel:DWORD dst_unused:UNUSED_PAD src0_sel:WORD_1
	v_cvt_f32_f16_e32 v243, v174
	v_cvt_f32_f16_sdwa v244, v175 dst_sel:DWORD dst_unused:UNUSED_PAD src0_sel:WORD_1
	v_cvt_f32_f16_e32 v245, v175
	v_sub_f32_e32 v172, v172, v224
	v_sub_f32_e32 v173, v241, v224
	v_sub_f32_e32 v174, v240, v224
	v_sub_f32_e32 v175, v239, v224
	v_pk_mul_f32 v[174:175], v[224:225], v[174:175] op_sel:[1,0]
	v_pk_mul_f32 v[172:173], v[224:225], v[172:173] op_sel:[1,0]
	v_pk_fma_f32 v[144:145], v[174:175], v[92:93], v[144:145]
	v_pk_fma_f32 v[146:147], v[172:173], v[94:95], v[146:147]
	v_sub_f32_e32 v172, v245, v224
	v_sub_f32_e32 v173, v244, v224
	v_sub_f32_e32 v174, v243, v224
	v_sub_f32_e32 v175, v242, v224
	v_pk_mul_f32 v[174:175], v[224:225], v[174:175] op_sel:[1,0]
	v_pk_mul_f32 v[172:173], v[224:225], v[172:173] op_sel:[1,0]
	v_pk_add_f32 v[134:135], v[134:135], v[198:199]
	v_pk_fma_f32 v[172:173], v[172:173], v[90:91], v[142:143]
	v_pk_fma_f32 v[142:143], v[174:175], v[88:89], v[140:141]
	v_cvt_f16_f32_e32 v174, v144
	v_cvt_f16_f32_e32 v175, v145
	v_cvt_pk_f16_f32 v140, v144, v145
	v_cvt_f16_f32_e32 v144, v146
	v_cvt_f16_f32_e32 v145, v147
	v_cvt_pk_f16_f32 v141, v146, v147
	v_cvt_f16_f32_e32 v146, v142
	v_cvt_f16_f32_e32 v147, v143
	v_cvt_f16_f32_e32 v239, v172
	v_cvt_f16_f32_e32 v240, v173
	v_cvt_pk_f16_f32 v142, v142, v143
	v_cvt_pk_f16_f32 v143, v172, v173
	ds_write_b128 v235, v[140:143]
	v_cvt_f32_f16_e32 v140, v174
	v_cvt_f32_f16_e32 v141, v175
	v_cvt_f32_f16_e32 v142, v144
	v_cvt_f32_f16_e32 v143, v145
	v_cvt_f32_f16_e32 v145, v146
	v_cvt_f32_f16_e32 v147, v147
	v_cvt_f32_f16_e32 v172, v239
	v_cvt_f32_f16_e32 v173, v240
	v_add_f32_e32 v140, v140, v141
	v_add_f32_e32 v142, v142, v143
	v_add_f32_e32 v140, v140, v142
	v_add_f32_e32 v142, v145, v147
	v_add_f32_e32 v145, v172, v173
	v_add_f32_e32 v142, v142, v145
	v_add_f32_e32 v140, v140, v142
	v_add_f32_e32 v145, 0, v140
	v_mul_f32_e32 v140, v141, v141
	v_mul_f32_e32 v141, v143, v143
	v_fma_mix_f32 v140, v174, v174, v140 op_sel_hi:[1,1,0]
	v_fma_mix_f32 v141, v144, v144, v141 op_sel_hi:[1,1,0]
	v_mul_f32_e32 v142, v173, v173
	v_add_f32_e32 v140, v140, v141
	v_mul_f32_e32 v141, v147, v147
	v_fma_mix_f32 v141, v146, v146, v141 op_sel_hi:[1,1,0]
	v_fma_mix_f32 v142, v239, v239, v142 op_sel_hi:[1,1,0]
	v_cvt_f32_f16_sdwa v143, v168 dst_sel:DWORD dst_unused:UNUSED_PAD src0_sel:WORD_1
	v_add_f32_e32 v141, v141, v142
	v_add_f32_e32 v144, v140, v141
	v_cvt_f32_f16_e32 v142, v168
	v_cvt_f32_f16_sdwa v141, v169 dst_sel:DWORD dst_unused:UNUSED_PAD src0_sel:WORD_1
	v_cvt_f32_f16_e32 v140, v169
	v_cvt_f32_f16_sdwa v146, v170 dst_sel:DWORD dst_unused:UNUSED_PAD src0_sel:WORD_1
	v_cvt_f32_f16_e32 v147, v170
	v_cvt_f32_f16_sdwa v168, v171 dst_sel:DWORD dst_unused:UNUSED_PAD src0_sel:WORD_1
	v_cvt_f32_f16_e32 v169, v171
	v_sub_f32_e32 v140, v140, v224
	v_sub_f32_e32 v141, v141, v224
	v_sub_f32_e32 v142, v142, v224
	v_sub_f32_e32 v143, v143, v224
	v_pk_add_f32 v[132:133], v[132:133], v[200:201]
	v_pk_mul_f32 v[142:143], v[224:225], v[142:143] op_sel:[1,0]
	v_pk_mul_f32 v[140:141], v[224:225], v[140:141] op_sel:[1,0]
	v_pk_fma_f32 v[132:133], v[142:143], v[80:81], v[132:133]
	v_pk_fma_f32 v[134:135], v[140:141], v[82:83], v[134:135]
	v_sub_f32_e32 v140, v169, v224
	v_sub_f32_e32 v141, v168, v224
	v_sub_f32_e32 v142, v147, v224
	v_sub_f32_e32 v143, v146, v224
	v_pk_add_f32 v[130:131], v[130:131], v[192:193]
	v_pk_add_f32 v[128:129], v[128:129], v[194:195]
	v_pk_mul_f32 v[142:143], v[224:225], v[142:143] op_sel:[1,0]
	v_pk_mul_f32 v[140:141], v[224:225], v[140:141] op_sel:[1,0]
	v_lshlrev_b32_e32 v221, 2, v221
	v_pk_fma_f32 v[140:141], v[140:141], v[74:75], v[130:131]
	v_pk_fma_f32 v[130:131], v[142:143], v[72:73], v[128:129]
	v_cvt_f16_f32_e32 v142, v132
	v_cvt_f16_f32_e32 v143, v133
	v_cvt_pk_f16_f32 v128, v132, v133
	v_cvt_f16_f32_e32 v132, v134
	v_cvt_f16_f32_e32 v133, v135
	v_cvt_pk_f16_f32 v129, v134, v135
	v_cvt_f16_f32_e32 v134, v130
	v_cvt_f16_f32_e32 v135, v131
	v_cvt_f16_f32_e32 v146, v140
	v_cvt_f16_f32_e32 v147, v141
	v_cvt_pk_f16_f32 v130, v130, v131
	v_cvt_pk_f16_f32 v131, v140, v141
	ds_write_b128 v235, v[128:131] offset:64
	v_cvt_f32_f16_e32 v128, v142
	v_cvt_f32_f16_e32 v129, v143
	v_cvt_f32_f16_e32 v130, v132
	v_cvt_f32_f16_e32 v131, v133
	v_cvt_f32_f16_e32 v133, v134
	v_cvt_f32_f16_e32 v135, v135
	v_cvt_f32_f16_e32 v140, v146
	v_cvt_f32_f16_e32 v141, v147
	v_add_f32_e32 v128, v128, v129
	v_add_f32_e32 v130, v130, v131
	v_add_f32_e32 v128, v128, v130
	v_add_f32_e32 v130, v133, v135
	v_add_f32_e32 v133, v140, v141
	v_add_f32_e32 v130, v130, v133
	v_add_f32_e32 v128, v128, v130
	v_add_f32_e32 v140, v145, v128
	v_mul_f32_e32 v128, v129, v129
	v_mul_f32_e32 v129, v131, v131
	v_fma_mix_f32 v128, v142, v142, v128 op_sel_hi:[1,1,0]
	v_fma_mix_f32 v129, v132, v132, v129 op_sel_hi:[1,1,0]
	v_mul_f32_e32 v130, v141, v141
	v_add_f32_e32 v128, v128, v129
	v_mul_f32_e32 v129, v135, v135
	ds_bpermute_b32 v142, v221, v140
	v_fma_mix_f32 v129, v134, v134, v129 op_sel_hi:[1,1,0]
	v_fma_mix_f32 v130, v146, v146, v130 op_sel_hi:[1,1,0]
	v_lshlrev_b32_e32 v237, 2, v237
	v_add_f32_e32 v129, v129, v130
	v_add_f32_e32 v128, v128, v129
	v_add_f32_e32 v141, v144, v128
	s_waitcnt lgkmcnt(0)
	v_add_f32_e32 v140, v140, v142
	ds_bpermute_b32 v142, v221, v141
	v_cvt_f32_f16_sdwa v145, v164 dst_sel:DWORD dst_unused:UNUSED_PAD src0_sel:WORD_1
	v_cvt_f32_f16_e32 v144, v164
	v_cvt_f32_f16_sdwa v146, v166 dst_sel:DWORD dst_unused:UNUSED_PAD src0_sel:WORD_1
	v_cvt_f32_f16_e32 v147, v166
	s_waitcnt lgkmcnt(0)
	v_add_f32_e32 v141, v141, v142
	ds_bpermute_b32 v142, v237, v140
	v_cvt_f32_f16_sdwa v164, v167 dst_sel:DWORD dst_unused:UNUSED_PAD src0_sel:WORD_1
	v_sub_f32_e32 v144, v144, v222
	v_sub_f32_e32 v145, v145, v222
	v_pk_mul_f32 v[144:145], v[222:223], v[144:145] op_sel:[1,0]
	s_waitcnt lgkmcnt(0)
	v_add_f32_e32 v142, v140, v142
	ds_bpermute_b32 v140, v237, v141
	v_pk_fma_f32 v[124:125], v[144:145], v[92:93], v[124:125]
	v_sub_f32_e32 v144, v147, v222
	v_sub_f32_e32 v145, v146, v222
	v_pk_mul_f32 v[144:145], v[222:223], v[144:145] op_sel:[1,0]
	s_waitcnt lgkmcnt(0)
	v_add_f32_e32 v143, v141, v140
	v_cvt_f32_f16_sdwa v141, v165 dst_sel:DWORD dst_unused:UNUSED_PAD src0_sel:WORD_1
	v_cvt_f32_f16_e32 v140, v165
	v_cvt_f32_f16_e32 v165, v167
	ds_read_b128 v[132:135], v236
	ds_read_b128 v[128:131], v236 offset:1152
	v_sub_f32_e32 v141, v141, v222
	v_sub_f32_e32 v140, v140, v222
	v_pk_mul_f32 v[140:141], v[222:223], v[140:141] op_sel:[1,0]
	v_pk_add_f32 v[118:119], v[118:119], v[198:199]
	v_pk_fma_f32 v[126:127], v[140:141], v[94:95], v[126:127]
	v_sub_f32_e32 v140, v165, v222
	v_sub_f32_e32 v141, v164, v222
	v_pk_mul_f32 v[140:141], v[222:223], v[140:141] op_sel:[1,0]
	v_pk_add_f32 v[116:117], v[116:117], v[200:201]
	v_pk_fma_f32 v[140:141], v[140:141], v[90:91], v[122:123]
	v_pk_fma_f32 v[122:123], v[144:145], v[88:89], v[120:121]
	v_cvt_f16_f32_e32 v144, v124
	v_cvt_f16_f32_e32 v145, v125
	v_cvt_pk_f16_f32 v120, v124, v125
	v_cvt_f16_f32_e32 v124, v126
	v_cvt_f16_f32_e32 v125, v127
	v_cvt_pk_f16_f32 v121, v126, v127
	v_cvt_f16_f32_e32 v126, v122
	v_cvt_f16_f32_e32 v127, v123
	v_cvt_f16_f32_e32 v146, v140
	v_cvt_f16_f32_e32 v147, v141
	v_cvt_pk_f16_f32 v122, v122, v123
	v_cvt_pk_f16_f32 v123, v140, v141
	ds_write_b128 v235, v[120:123]
	v_cvt_f32_f16_e32 v120, v144
	v_cvt_f32_f16_e32 v121, v145
	v_cvt_f32_f16_e32 v122, v124
	v_cvt_f32_f16_e32 v123, v125
	v_cvt_f32_f16_e32 v125, v126
	v_cvt_f32_f16_e32 v127, v127
	v_cvt_f32_f16_e32 v140, v146
	v_cvt_f32_f16_e32 v141, v147
	v_add_f32_e32 v120, v120, v121
	v_add_f32_e32 v122, v122, v123
	v_add_f32_e32 v120, v120, v122
	v_add_f32_e32 v122, v125, v127
	v_add_f32_e32 v125, v140, v141
	v_add_f32_e32 v122, v122, v125
	v_add_f32_e32 v120, v120, v122
	v_add_f32_e32 v125, 0, v120
	v_mul_f32_e32 v120, v121, v121
	v_mul_f32_e32 v121, v123, v123
	v_fma_mix_f32 v120, v144, v144, v120 op_sel_hi:[1,1,0]
	v_fma_mix_f32 v121, v124, v124, v121 op_sel_hi:[1,1,0]
	v_mul_f32_e32 v122, v141, v141
	v_add_f32_e32 v120, v120, v121
	v_mul_f32_e32 v121, v127, v127
	v_fma_mix_f32 v121, v126, v126, v121 op_sel_hi:[1,1,0]
	v_fma_mix_f32 v122, v146, v146, v122 op_sel_hi:[1,1,0]
	v_cvt_f32_f16_sdwa v123, v160 dst_sel:DWORD dst_unused:UNUSED_PAD src0_sel:WORD_1
	v_add_f32_e32 v121, v121, v122
	v_add_f32_e32 v124, v120, v121
	v_cvt_f32_f16_e32 v122, v160
	v_cvt_f32_f16_sdwa v121, v161 dst_sel:DWORD dst_unused:UNUSED_PAD src0_sel:WORD_1
	v_cvt_f32_f16_e32 v120, v161
	v_cvt_f32_f16_sdwa v126, v162 dst_sel:DWORD dst_unused:UNUSED_PAD src0_sel:WORD_1
	v_cvt_f32_f16_e32 v127, v162
	v_cvt_f32_f16_sdwa v140, v163 dst_sel:DWORD dst_unused:UNUSED_PAD src0_sel:WORD_1
	v_cvt_f32_f16_e32 v141, v163
	v_sub_f32_e32 v120, v120, v222
	v_sub_f32_e32 v121, v121, v222
	v_sub_f32_e32 v122, v122, v222
	v_sub_f32_e32 v123, v123, v222
	v_pk_mul_f32 v[122:123], v[222:223], v[122:123] op_sel:[1,0]
	v_pk_mul_f32 v[120:121], v[222:223], v[120:121] op_sel:[1,0]
	v_pk_fma_f32 v[116:117], v[122:123], v[80:81], v[116:117]
	v_pk_fma_f32 v[118:119], v[120:121], v[82:83], v[118:119]
	v_sub_f32_e32 v120, v141, v222
	v_sub_f32_e32 v121, v140, v222
	v_sub_f32_e32 v122, v127, v222
	v_sub_f32_e32 v123, v126, v222
	v_pk_add_f32 v[114:115], v[114:115], v[192:193]
	v_pk_add_f32 v[112:113], v[112:113], v[194:195]
	v_pk_mul_f32 v[122:123], v[222:223], v[122:123] op_sel:[1,0]
	v_pk_mul_f32 v[120:121], v[222:223], v[120:121] op_sel:[1,0]
	s_ashr_i32 s39, s38, 31
	v_pk_fma_f32 v[120:121], v[120:121], v[74:75], v[114:115]
	v_pk_fma_f32 v[114:115], v[122:123], v[72:73], v[112:113]
	v_cvt_f16_f32_e32 v122, v116
	v_cvt_f16_f32_e32 v123, v117
	v_cvt_pk_f16_f32 v112, v116, v117
	v_cvt_f16_f32_e32 v116, v118
	v_cvt_f16_f32_e32 v117, v119
	v_cvt_pk_f16_f32 v113, v118, v119
	v_cvt_f16_f32_e32 v118, v114
	v_cvt_f16_f32_e32 v119, v115
	v_cvt_f16_f32_e32 v126, v120
	v_cvt_f16_f32_e32 v127, v121
	v_cvt_pk_f16_f32 v114, v114, v115
	v_cvt_pk_f16_f32 v115, v120, v121
	ds_write_b128 v235, v[112:115] offset:64
	v_cvt_f32_f16_e32 v112, v122
	v_cvt_f32_f16_e32 v113, v123
	v_cvt_f32_f16_e32 v114, v116
	v_cvt_f32_f16_e32 v115, v117
	v_cvt_f32_f16_e32 v117, v118
	v_cvt_f32_f16_e32 v119, v119
	v_cvt_f32_f16_e32 v120, v126
	v_cvt_f32_f16_e32 v121, v127
	v_add_f32_e32 v112, v112, v113
	v_add_f32_e32 v114, v114, v115
	v_add_f32_e32 v112, v112, v114
	v_add_f32_e32 v114, v117, v119
	v_add_f32_e32 v117, v120, v121
	v_add_f32_e32 v114, v114, v117
	v_add_f32_e32 v112, v112, v114
	v_mul_f32_e32 v113, v113, v113
	v_mul_f32_e32 v114, v115, v115
	v_fma_mix_f32 v113, v122, v122, v113 op_sel_hi:[1,1,0]
	v_fma_mix_f32 v114, v116, v116, v114 op_sel_hi:[1,1,0]
	v_mul_f32_e32 v115, v121, v121
	v_add_f32_e32 v113, v113, v114
	v_mul_f32_e32 v114, v119, v119
	v_fma_mix_f32 v114, v118, v118, v114 op_sel_hi:[1,1,0]
	v_fma_mix_f32 v115, v126, v126, v115 op_sel_hi:[1,1,0]
	v_add_f32_e32 v112, v125, v112
	v_add_f32_e32 v114, v114, v115
	v_add_f32_e32 v113, v113, v114
	ds_bpermute_b32 v114, v221, v112
	v_add_f32_e32 v113, v124, v113
	ds_read_b128 v[160:163], v236
	ds_read_b128 v[164:167], v236 offset:1152
	s_waitcnt lgkmcnt(2)
	v_add_f32_e32 v112, v112, v114
	ds_bpermute_b32 v114, v221, v113
	s_waitcnt lgkmcnt(0)
	v_add_f32_e32 v113, v113, v114
	ds_bpermute_b32 v114, v237, v112
	s_waitcnt lgkmcnt(0)
	v_add_f32_e32 v146, v112, v114
	ds_bpermute_b32 v112, v237, v113
	s_waitcnt lgkmcnt(0)
	v_add_f32_e32 v147, v113, v112
	v_mov_b64_e32 v[112:113], s[28:29]
	v_mad_i64_i32 v[112:113], s[40:41], v220, s73, v[112:113]
	v_lshl_add_u64 v[140:141], s[38:39], 3, v[112:113]
	v_add_co_u32_e32 v112, vcc, s74, v214
	v_lshl_or_b32 v144, v238, 1, v230
	s_nop 0
	v_addc_co_u32_e32 v113, vcc, 0, v215, vcc
	global_load_dwordx4 v[124:127], v[112:113], off nt
	global_load_dwordx4 v[120:123], v[112:113], off offset:64 nt
	v_add_co_u32_e32 v112, vcc, s75, v214
	v_lshl_add_u64 v[140:141], v[140:141], 0, s[34:35]
	s_nop 0
	v_addc_co_u32_e32 v113, vcc, 0, v215, vcc
	global_load_dwordx4 v[116:119], v[112:113], off nt
	s_nop 0
	global_load_dwordx4 v[112:115], v[112:113], off offset:64 nt
	s_nop 0
	buffer_store_dwordx4 v[132:135], v144, s[24:27], 0 offen nt
	s_nop 1
	v_add_u32_e32 v132, 0x3000, v144
	buffer_store_dwordx4 v[128:131], v132, s[24:27], 0 offen nt
	global_store_dwordx2 v[140:141], v[142:143], off
	s_nop 0
	v_add_u32_e32 v128, 0x6000, v144
	buffer_store_dwordx4 v[160:163], v128, s[24:27], 0 offen nt
	v_add_u32_e32 v128, 0x9000, v144
	buffer_store_dwordx4 v[164:167], v128, s[24:27], 0 offen nt
	global_store_dwordx2 v[140:141], v[146:147], off offset:1536
	v_cvt_f32_f16_sdwa v131, v156 dst_sel:DWORD dst_unused:UNUSED_PAD src0_sel:WORD_1
	v_cvt_f32_f16_e32 v130, v156
	v_cvt_f32_f16_sdwa v129, v157 dst_sel:DWORD dst_unused:UNUSED_PAD src0_sel:WORD_1
	v_cvt_f32_f16_e32 v128, v157
	v_cvt_f32_f16_sdwa v132, v158 dst_sel:DWORD dst_unused:UNUSED_PAD src0_sel:WORD_1
	v_cvt_f32_f16_e32 v133, v158
	v_cvt_f32_f16_sdwa v134, v159 dst_sel:DWORD dst_unused:UNUSED_PAD src0_sel:WORD_1
	v_cvt_f32_f16_e32 v135, v159
	v_sub_f32_e32 v128, v128, v218
	v_sub_f32_e32 v129, v129, v218
	v_sub_f32_e32 v130, v130, v218
	v_sub_f32_e32 v131, v131, v218
	v_pk_add_f32 v[110:111], v[110:111], v[206:207]
	v_pk_add_f32 v[108:109], v[108:109], v[208:209]
	v_pk_mul_f32 v[130:131], v[218:219], v[130:131] op_sel:[1,0]
	v_pk_mul_f32 v[128:129], v[218:219], v[128:129] op_sel:[1,0]
	v_pk_fma_f32 v[108:109], v[130:131], v[92:93], v[108:109]
	v_pk_fma_f32 v[110:111], v[128:129], v[94:95], v[110:111]
	v_sub_f32_e32 v128, v135, v218
	v_sub_f32_e32 v129, v134, v218
	v_sub_f32_e32 v130, v133, v218
	v_sub_f32_e32 v131, v132, v218
	v_pk_add_f32 v[106:107], v[106:107], v[202:203]
	v_pk_add_f32 v[104:105], v[104:105], v[204:205]
	v_pk_mul_f32 v[130:131], v[218:219], v[130:131] op_sel:[1,0]
	v_pk_mul_f32 v[128:129], v[218:219], v[128:129] op_sel:[1,0]
	v_pk_add_f32 v[102:103], v[102:103], v[198:199]
	v_pk_fma_f32 v[128:129], v[128:129], v[90:91], v[106:107]
	v_pk_fma_f32 v[106:107], v[130:131], v[88:89], v[104:105]
	v_cvt_f16_f32_e32 v130, v108
	v_cvt_f16_f32_e32 v131, v109
	v_cvt_pk_f16_f32 v104, v108, v109
	v_cvt_f16_f32_e32 v108, v110
	v_cvt_f16_f32_e32 v109, v111
	v_cvt_pk_f16_f32 v105, v110, v111
	v_cvt_f16_f32_e32 v110, v106
	v_cvt_f16_f32_e32 v111, v107
	v_cvt_f16_f32_e32 v132, v128
	v_cvt_f16_f32_e32 v133, v129
	v_cvt_pk_f16_f32 v106, v106, v107
	v_cvt_pk_f16_f32 v107, v128, v129
	ds_write_b128 v235, v[104:107]
	v_cvt_f32_f16_e32 v104, v130
	v_cvt_f32_f16_e32 v105, v131
	v_cvt_f32_f16_e32 v106, v108
	v_cvt_f32_f16_e32 v107, v109
	v_cvt_f32_f16_e32 v109, v110
	v_cvt_f32_f16_e32 v111, v111
	v_cvt_f32_f16_e32 v128, v132
	v_cvt_f32_f16_e32 v129, v133
	v_add_f32_e32 v104, v104, v105
	v_add_f32_e32 v106, v106, v107
	v_add_f32_e32 v104, v104, v106
	v_add_f32_e32 v106, v109, v111
	v_add_f32_e32 v109, v128, v129
	v_add_f32_e32 v106, v106, v109
	v_add_f32_e32 v104, v104, v106
	v_add_f32_e32 v109, 0, v104
	v_mul_f32_e32 v104, v105, v105
	v_mul_f32_e32 v105, v107, v107
	v_fma_mix_f32 v104, v130, v130, v104 op_sel_hi:[1,1,0]
	v_fma_mix_f32 v105, v108, v108, v105 op_sel_hi:[1,1,0]
	v_mul_f32_e32 v106, v129, v129
	v_add_f32_e32 v104, v104, v105
	v_mul_f32_e32 v105, v111, v111
	v_fma_mix_f32 v105, v110, v110, v105 op_sel_hi:[1,1,0]
	v_fma_mix_f32 v106, v132, v132, v106 op_sel_hi:[1,1,0]
	v_cvt_f32_f16_sdwa v107, v152 dst_sel:DWORD dst_unused:UNUSED_PAD src0_sel:WORD_1
	v_add_f32_e32 v105, v105, v106
	v_add_f32_e32 v108, v104, v105
	v_cvt_f32_f16_e32 v106, v152
	v_cvt_f32_f16_sdwa v105, v153 dst_sel:DWORD dst_unused:UNUSED_PAD src0_sel:WORD_1
	v_cvt_f32_f16_e32 v104, v153
	v_cvt_f32_f16_sdwa v110, v154 dst_sel:DWORD dst_unused:UNUSED_PAD src0_sel:WORD_1
	v_cvt_f32_f16_e32 v111, v154
	v_cvt_f32_f16_sdwa v128, v155 dst_sel:DWORD dst_unused:UNUSED_PAD src0_sel:WORD_1
	v_cvt_f32_f16_e32 v129, v155
	v_sub_f32_e32 v104, v104, v218
	v_sub_f32_e32 v105, v105, v218
	v_sub_f32_e32 v106, v106, v218
	v_sub_f32_e32 v107, v107, v218
	v_pk_add_f32 v[100:101], v[100:101], v[200:201]
	v_pk_mul_f32 v[106:107], v[218:219], v[106:107] op_sel:[1,0]
	v_pk_mul_f32 v[104:105], v[218:219], v[104:105] op_sel:[1,0]
	v_pk_fma_f32 v[100:101], v[106:107], v[80:81], v[100:101]
	v_pk_fma_f32 v[102:103], v[104:105], v[82:83], v[102:103]
	v_sub_f32_e32 v104, v129, v218
	v_sub_f32_e32 v105, v128, v218
	v_sub_f32_e32 v106, v111, v218
	v_sub_f32_e32 v107, v110, v218
	v_pk_add_f32 v[98:99], v[98:99], v[192:193]
	v_pk_add_f32 v[96:97], v[96:97], v[194:195]
	v_pk_mul_f32 v[106:107], v[218:219], v[106:107] op_sel:[1,0]
	v_pk_mul_f32 v[104:105], v[218:219], v[104:105] op_sel:[1,0]
	v_pk_add_f32 v[86:87], v[86:87], v[206:207]
	v_pk_fma_f32 v[104:105], v[104:105], v[74:75], v[98:99]
	v_pk_fma_f32 v[98:99], v[106:107], v[72:73], v[96:97]
	v_cvt_f16_f32_e32 v106, v100
	v_cvt_f16_f32_e32 v107, v101
	v_cvt_pk_f16_f32 v96, v100, v101
	v_cvt_f16_f32_e32 v100, v102
	v_cvt_f16_f32_e32 v101, v103
	v_cvt_pk_f16_f32 v97, v102, v103
	v_cvt_f16_f32_e32 v103, v99
	v_cvt_f16_f32_e32 v111, v105
	v_cvt_f16_f32_e32 v102, v98
	v_cvt_f16_f32_e32 v110, v104
	v_cvt_pk_f16_f32 v98, v98, v99
	v_cvt_pk_f16_f32 v99, v104, v105
	v_cvt_f32_f16_e32 v105, v107
	v_cvt_f32_f16_e32 v107, v100
	v_cvt_f32_f16_e32 v101, v101
	v_cvt_f32_f16_e32 v103, v103
	v_cvt_f32_f16_e32 v104, v106
	v_cvt_f32_f16_e32 v111, v111
	v_cvt_f32_f16_e32 v128, v102
	v_cvt_f32_f16_e32 v129, v110
	v_add_f32_e32 v107, v107, v101
	v_mul_f32_e32 v101, v101, v101
	v_fma_mix_f32 v100, v100, v100, v101 op_sel_hi:[1,1,0]
	v_mul_f32_e32 v101, v103, v103
	v_add_f32_e32 v104, v104, v105
	v_mul_f32_e32 v105, v105, v105
	v_fma_mix_f32 v101, v102, v102, v101 op_sel_hi:[1,1,0]
	v_mul_f32_e32 v102, v111, v111
	v_add_f32_e32 v104, v104, v107
	v_add_f32_e32 v107, v128, v103
	v_add_f32_e32 v128, v129, v111
	v_fma_mix_f32 v105, v106, v106, v105 op_sel_hi:[1,1,0]
	v_fma_mix_f32 v102, v110, v110, v102 op_sel_hi:[1,1,0]
	v_add_f32_e32 v107, v107, v128
	v_add_f32_e32 v100, v105, v100
	v_add_f32_e32 v101, v101, v102
	v_add_f32_e32 v104, v104, v107
	v_add_f32_e32 v100, v100, v101
	v_add_f32_e32 v104, v109, v104
	v_add_f32_e32 v105, v108, v100
	ds_bpermute_b32 v106, v221, v104
	ds_bpermute_b32 v107, v221, v105
	v_cvt_f32_f16_sdwa v108, v150 dst_sel:DWORD dst_unused:UNUSED_PAD src0_sel:WORD_1
	v_cvt_f32_f16_e32 v109, v150
	v_cvt_f32_f16_sdwa v110, v151 dst_sel:DWORD dst_unused:UNUSED_PAD src0_sel:WORD_1
	s_waitcnt lgkmcnt(1)
	v_add_f32_e32 v128, v104, v106
	s_waitcnt lgkmcnt(0)
	v_add_f32_e32 v129, v105, v107
	v_cvt_f32_f16_sdwa v107, v148 dst_sel:DWORD dst_unused:UNUSED_PAD src0_sel:WORD_1
	v_cvt_f32_f16_e32 v106, v148
	v_cvt_f32_f16_sdwa v105, v149 dst_sel:DWORD dst_unused:UNUSED_PAD src0_sel:WORD_1
	v_cvt_f32_f16_e32 v104, v149
	v_cvt_f32_f16_e32 v111, v151
	v_sub_f32_e32 v106, v106, v216
	v_sub_f32_e32 v105, v105, v216
	v_sub_f32_e32 v104, v104, v216
	v_sub_f32_e32 v107, v107, v216
	v_pk_add_f32 v[84:85], v[84:85], v[208:209]
	v_pk_mul_f32 v[106:107], v[216:217], v[106:107] op_sel:[1,0]
	v_pk_mul_f32 v[104:105], v[216:217], v[104:105] op_sel:[1,0]
	v_pk_fma_f32 v[84:85], v[106:107], v[92:93], v[84:85]
	v_pk_fma_f32 v[86:87], v[104:105], v[94:95], v[86:87]
	v_sub_f32_e32 v104, v111, v216
	v_sub_f32_e32 v105, v110, v216
	v_sub_f32_e32 v106, v109, v216
	v_sub_f32_e32 v107, v108, v216
	v_pk_add_f32 v[78:79], v[78:79], v[202:203]
	v_pk_add_f32 v[76:77], v[76:77], v[204:205]
	v_pk_mul_f32 v[106:107], v[216:217], v[106:107] op_sel:[1,0]
	v_pk_mul_f32 v[104:105], v[216:217], v[104:105] op_sel:[1,0]
	ds_write_b128 v235, v[96:99] offset:64
	v_pk_fma_f32 v[104:105], v[104:105], v[90:91], v[78:79]
	v_pk_fma_f32 v[78:79], v[106:107], v[88:89], v[76:77]
	v_cvt_f16_f32_e32 v106, v84
	v_cvt_f16_f32_e32 v107, v85
	v_cvt_pk_f16_f32 v76, v84, v85
	v_cvt_f16_f32_e32 v84, v86
	v_cvt_f16_f32_e32 v85, v87
	v_cvt_pk_f16_f32 v77, v86, v87
	v_cvt_f16_f32_e32 v86, v78
	v_cvt_f16_f32_e32 v87, v79
	v_cvt_f16_f32_e32 v108, v104
	v_cvt_f16_f32_e32 v109, v105
	v_cvt_pk_f16_f32 v78, v78, v79
	v_cvt_pk_f16_f32 v79, v104, v105
	ds_read_b128 v[96:99], v236
	ds_read_b128 v[100:103], v236 offset:1152
	ds_write_b128 v235, v[76:79]
	v_cvt_f32_f16_e32 v76, v106
	v_cvt_f32_f16_e32 v77, v107
	v_cvt_f32_f16_e32 v78, v84
	v_cvt_f32_f16_e32 v79, v85
	v_cvt_f32_f16_e32 v85, v86
	v_cvt_f32_f16_e32 v87, v87
	v_cvt_f32_f16_e32 v104, v108
	v_cvt_f32_f16_e32 v105, v109
	v_add_f32_e32 v76, v76, v77
	v_add_f32_e32 v78, v78, v79
	v_add_f32_e32 v76, v76, v78
	v_add_f32_e32 v78, v85, v87
	v_add_f32_e32 v85, v104, v105
	v_add_f32_e32 v78, v78, v85
	v_add_f32_e32 v76, v76, v78
	v_add_f32_e32 v85, 0, v76
	v_mul_f32_e32 v76, v77, v77
	v_mul_f32_e32 v77, v79, v79
	v_fma_mix_f32 v76, v106, v106, v76 op_sel_hi:[1,1,0]
	v_fma_mix_f32 v77, v84, v84, v77 op_sel_hi:[1,1,0]
	v_mul_f32_e32 v78, v105, v105
	v_add_f32_e32 v76, v76, v77
	v_mul_f32_e32 v77, v87, v87
	v_fma_mix_f32 v77, v86, v86, v77 op_sel_hi:[1,1,0]
	v_fma_mix_f32 v78, v108, v108, v78 op_sel_hi:[1,1,0]
	v_cvt_f32_f16_sdwa v79, v136 dst_sel:DWORD dst_unused:UNUSED_PAD src0_sel:WORD_1
	v_add_f32_e32 v77, v77, v78
	v_add_f32_e32 v84, v76, v77
	v_cvt_f32_f16_e32 v78, v136
	v_cvt_f32_f16_sdwa v77, v137 dst_sel:DWORD dst_unused:UNUSED_PAD src0_sel:WORD_1
	v_cvt_f32_f16_e32 v76, v137
	v_cvt_f32_f16_sdwa v86, v138 dst_sel:DWORD dst_unused:UNUSED_PAD src0_sel:WORD_1
	v_cvt_f32_f16_e32 v87, v138
	v_cvt_f32_f16_sdwa v104, v139 dst_sel:DWORD dst_unused:UNUSED_PAD src0_sel:WORD_1
	v_cvt_f32_f16_e32 v105, v139
	v_sub_f32_e32 v76, v76, v216
	v_sub_f32_e32 v77, v77, v216
	v_sub_f32_e32 v78, v78, v216
	v_sub_f32_e32 v79, v79, v216
	v_pk_add_f32 v[70:71], v[70:71], v[198:199]
	v_pk_add_f32 v[68:69], v[68:69], v[200:201]
	v_pk_mul_f32 v[78:79], v[216:217], v[78:79] op_sel:[1,0]
	v_pk_mul_f32 v[76:77], v[216:217], v[76:77] op_sel:[1,0]
	v_pk_fma_f32 v[68:69], v[78:79], v[80:81], v[68:69]
	v_pk_fma_f32 v[70:71], v[76:77], v[82:83], v[70:71]
	v_sub_f32_e32 v76, v105, v216
	v_sub_f32_e32 v77, v104, v216
	v_sub_f32_e32 v78, v87, v216
	v_sub_f32_e32 v79, v86, v216
	v_pk_add_f32 v[66:67], v[66:67], v[192:193]
	v_pk_add_f32 v[64:65], v[64:65], v[194:195]
	v_pk_mul_f32 v[78:79], v[216:217], v[78:79] op_sel:[1,0]
	v_pk_mul_f32 v[76:77], v[216:217], v[76:77] op_sel:[1,0]
	ds_bpermute_b32 v130, v237, v128
	v_pk_fma_f32 v[76:77], v[76:77], v[74:75], v[66:67]
	v_pk_fma_f32 v[66:67], v[78:79], v[72:73], v[64:65]
	v_cvt_f16_f32_e32 v78, v68
	v_cvt_f16_f32_e32 v79, v69
	v_cvt_pk_f16_f32 v64, v68, v69
	v_cvt_f16_f32_e32 v68, v70
	v_cvt_f16_f32_e32 v69, v71
	v_cvt_pk_f16_f32 v65, v70, v71
	v_cvt_f16_f32_e32 v71, v67
	v_cvt_f16_f32_e32 v87, v77
	v_cvt_f16_f32_e32 v70, v66
	v_cvt_f16_f32_e32 v86, v76
	v_cvt_f32_f16_e32 v105, v68
	v_cvt_f32_f16_e32 v69, v69
	v_cvt_f32_f16_e32 v71, v71
	v_cvt_f32_f16_e32 v104, v78
	v_cvt_f32_f16_e32 v79, v79
	v_cvt_f32_f16_e32 v87, v87
	v_cvt_f32_f16_e32 v106, v70
	v_cvt_f32_f16_e32 v107, v86
	v_add_f32_e32 v105, v105, v69
	v_mul_f32_e32 v69, v69, v69
	v_fma_mix_f32 v68, v68, v68, v69 op_sel_hi:[1,1,0]
	v_mul_f32_e32 v69, v71, v71
	v_add_f32_e32 v104, v104, v79
	v_mul_f32_e32 v79, v79, v79
	v_fma_mix_f32 v69, v70, v70, v69 op_sel_hi:[1,1,0]
	v_mul_f32_e32 v70, v87, v87
	v_add_f32_e32 v104, v104, v105
	v_add_f32_e32 v105, v106, v71
	v_add_f32_e32 v106, v107, v87
	v_fma_mix_f32 v78, v78, v78, v79 op_sel_hi:[1,1,0]
	v_fma_mix_f32 v70, v86, v86, v70 op_sel_hi:[1,1,0]
	v_add_f32_e32 v105, v105, v106
	v_add_f32_e32 v68, v78, v68
	v_add_f32_e32 v69, v69, v70
	v_add_f32_e32 v104, v104, v105
	v_add_f32_e32 v68, v68, v69
	v_add_f32_e32 v85, v85, v104
	v_add_f32_e32 v68, v84, v68
	ds_bpermute_b32 v69, v221, v85
	ds_bpermute_b32 v70, v221, v68
	v_cvt_pk_f16_f32 v66, v66, v67
	v_cvt_pk_f16_f32 v67, v76, v77
	ds_write_b128 v235, v[64:67] offset:64
	s_waitcnt lgkmcnt(2)
	v_add_f32_e32 v64, v85, v69
	s_waitcnt lgkmcnt(1)
	v_add_f32_e32 v65, v68, v70
	ds_bpermute_b32 v131, v237, v129
	ds_bpermute_b32 v66, v237, v64
	ds_bpermute_b32 v67, v237, v65
	ds_read_b128 v[104:107], v236
	ds_read_b128 v[108:111], v236 offset:1152
	v_add_f32_e32 v128, v128, v130
	s_waitcnt lgkmcnt(4)
	v_add_f32_e32 v129, v129, v131
	s_waitcnt lgkmcnt(3)
	v_add_f32_e32 v130, v64, v66
	s_waitcnt lgkmcnt(2)
	v_add_f32_e32 v131, v65, v67
	v_add_co_u32_e32 v64, vcc, s77, v214
	s_nop 1
	v_addc_co_u32_e32 v65, vcc, 0, v215, vcc
	global_load_dwordx4 v[84:87], v[64:65], off nt
	global_load_dwordx4 v[76:79], v[64:65], off offset:64 nt
	v_add_co_u32_e32 v64, vcc, s78, v214
	s_nop 1
	v_addc_co_u32_e32 v65, vcc, 0, v215, vcc
	global_load_dwordx4 v[68:71], v[64:65], off nt
	s_nop 0
	global_load_dwordx4 v[64:67], v[64:65], off offset:64 nt
	v_add_u32_e32 v132, 0xc000, v144
	buffer_store_dwordx4 v[96:99], v132, s[24:27], 0 offen nt
	s_nop 1
	v_add_u32_e32 v96, 0xf000, v144
	buffer_store_dwordx4 v[100:103], v96, s[24:27], 0 offen nt
	v_add_u32_e32 v96, 0x12000, v144
	global_store_dwordx2 v[140:141], v[128:129], off offset:3072
	s_waitcnt lgkmcnt(1)
	buffer_store_dwordx4 v[104:107], v96, s[24:27], 0 offen nt
	v_add_u32_e32 v96, 0x15000, v144
	s_waitcnt lgkmcnt(0)
	buffer_store_dwordx4 v[108:111], v96, s[24:27], 0 offen nt
	v_add_co_u32_e32 v96, vcc, s79, v140
	s_nop 1
	v_addc_co_u32_e32 v97, vcc, 0, v141, vcc
	global_store_dwordx2 v[96:97], v[130:131], off offset:512
	s_waitcnt vmcnt(19)
	v_cvt_f32_f16_sdwa v99, v124 dst_sel:DWORD dst_unused:UNUSED_PAD src0_sel:WORD_1
	v_cvt_f32_f16_e32 v98, v124
	v_cvt_f32_f16_sdwa v97, v125 dst_sel:DWORD dst_unused:UNUSED_PAD src0_sel:WORD_1
	v_cvt_f32_f16_e32 v96, v125
	v_cvt_f32_f16_sdwa v100, v126 dst_sel:DWORD dst_unused:UNUSED_PAD src0_sel:WORD_1
	v_cvt_f32_f16_e32 v101, v126
	v_cvt_f32_f16_sdwa v102, v127 dst_sel:DWORD dst_unused:UNUSED_PAD src0_sel:WORD_1
	v_cvt_f32_f16_e32 v103, v127
	v_sub_f32_e32 v96, v96, v212
	v_sub_f32_e32 v97, v97, v212
	v_sub_f32_e32 v98, v98, v212
	v_sub_f32_e32 v99, v99, v212
	v_pk_add_f32 v[62:63], v[62:63], v[206:207]
	v_pk_add_f32 v[60:61], v[60:61], v[208:209]
	v_pk_mul_f32 v[98:99], v[212:213], v[98:99] op_sel:[1,0]
	v_pk_mul_f32 v[96:97], v[212:213], v[96:97] op_sel:[1,0]
	v_pk_fma_f32 v[60:61], v[92:93], v[98:99], v[60:61]
	v_pk_fma_f32 v[62:63], v[94:95], v[96:97], v[62:63]
	v_sub_f32_e32 v96, v103, v212
	v_sub_f32_e32 v97, v102, v212
	v_sub_f32_e32 v98, v101, v212
	v_sub_f32_e32 v99, v100, v212
	v_pk_add_f32 v[58:59], v[58:59], v[202:203]
	v_pk_add_f32 v[56:57], v[56:57], v[204:205]
	v_pk_mul_f32 v[98:99], v[212:213], v[98:99] op_sel:[1,0]
	v_pk_mul_f32 v[96:97], v[212:213], v[96:97] op_sel:[1,0]
	v_pk_add_f32 v[54:55], v[54:55], v[198:199]
	v_pk_fma_f32 v[96:97], v[90:91], v[96:97], v[58:59]
	v_pk_fma_f32 v[58:59], v[88:89], v[98:99], v[56:57]
	v_cvt_f16_f32_e32 v98, v60
	v_cvt_f16_f32_e32 v99, v61
	v_cvt_pk_f16_f32 v56, v60, v61
	v_cvt_f16_f32_e32 v60, v62
	v_cvt_f16_f32_e32 v61, v63
	v_cvt_pk_f16_f32 v57, v62, v63
	v_cvt_f16_f32_e32 v62, v58
	v_cvt_f16_f32_e32 v63, v59
	v_cvt_f16_f32_e32 v100, v96
	v_cvt_f16_f32_e32 v101, v97
	v_cvt_pk_f16_f32 v58, v58, v59
	v_cvt_pk_f16_f32 v59, v96, v97
	ds_write_b128 v235, v[56:59]
	v_cvt_f32_f16_e32 v56, v98
	v_cvt_f32_f16_e32 v57, v99
	v_cvt_f32_f16_e32 v58, v60
	v_cvt_f32_f16_e32 v59, v61
	v_cvt_f32_f16_e32 v61, v62
	v_cvt_f32_f16_e32 v63, v63
	v_cvt_f32_f16_e32 v96, v100
	v_cvt_f32_f16_e32 v97, v101
	v_add_f32_e32 v56, v56, v57
	v_add_f32_e32 v58, v58, v59
	v_add_f32_e32 v56, v56, v58
	v_add_f32_e32 v58, v61, v63
	v_add_f32_e32 v61, v96, v97
	v_add_f32_e32 v58, v58, v61
	v_add_f32_e32 v56, v56, v58
	v_add_f32_e32 v61, 0, v56
	v_mul_f32_e32 v56, v57, v57
	v_mul_f32_e32 v57, v59, v59
	v_fma_mix_f32 v56, v98, v98, v56 op_sel_hi:[1,1,0]
	v_fma_mix_f32 v57, v60, v60, v57 op_sel_hi:[1,1,0]
	v_mul_f32_e32 v58, v97, v97
	v_add_f32_e32 v56, v56, v57
	v_mul_f32_e32 v57, v63, v63
	v_fma_mix_f32 v57, v62, v62, v57 op_sel_hi:[1,1,0]
	v_fma_mix_f32 v58, v100, v100, v58 op_sel_hi:[1,1,0]
	s_waitcnt vmcnt(18)
	v_cvt_f32_f16_sdwa v59, v120 dst_sel:DWORD dst_unused:UNUSED_PAD src0_sel:WORD_1
	v_add_f32_e32 v57, v57, v58
	v_add_f32_e32 v60, v56, v57
	v_cvt_f32_f16_e32 v58, v120
	v_cvt_f32_f16_sdwa v57, v121 dst_sel:DWORD dst_unused:UNUSED_PAD src0_sel:WORD_1
	v_cvt_f32_f16_e32 v56, v121
	v_cvt_f32_f16_sdwa v62, v122 dst_sel:DWORD dst_unused:UNUSED_PAD src0_sel:WORD_1
	v_cvt_f32_f16_e32 v63, v122
	v_cvt_f32_f16_sdwa v96, v123 dst_sel:DWORD dst_unused:UNUSED_PAD src0_sel:WORD_1
	v_cvt_f32_f16_e32 v97, v123
	v_sub_f32_e32 v56, v56, v212
	v_sub_f32_e32 v57, v57, v212
	v_sub_f32_e32 v58, v58, v212
	v_sub_f32_e32 v59, v59, v212
	v_pk_add_f32 v[52:53], v[52:53], v[200:201]
	v_pk_mul_f32 v[58:59], v[212:213], v[58:59] op_sel:[1,0]
	v_pk_mul_f32 v[56:57], v[212:213], v[56:57] op_sel:[1,0]
	v_pk_fma_f32 v[52:53], v[80:81], v[58:59], v[52:53]
	v_pk_fma_f32 v[54:55], v[82:83], v[56:57], v[54:55]
	v_sub_f32_e32 v56, v97, v212
	v_sub_f32_e32 v57, v96, v212
	v_sub_f32_e32 v58, v63, v212
	v_sub_f32_e32 v59, v62, v212
	v_pk_add_f32 v[50:51], v[50:51], v[192:193]
	v_pk_add_f32 v[48:49], v[48:49], v[194:195]
	v_pk_mul_f32 v[58:59], v[212:213], v[58:59] op_sel:[1,0]
	v_pk_mul_f32 v[56:57], v[212:213], v[56:57] op_sel:[1,0]
	s_waitcnt vmcnt(17)
	v_cvt_f32_f16_sdwa v98, v119 dst_sel:DWORD dst_unused:UNUSED_PAD src0_sel:WORD_1
	v_pk_fma_f32 v[56:57], v[74:75], v[56:57], v[50:51]
	v_pk_fma_f32 v[50:51], v[72:73], v[58:59], v[48:49]
	v_cvt_f16_f32_e32 v58, v52
	v_cvt_f16_f32_e32 v59, v53
	v_cvt_pk_f16_f32 v48, v52, v53
	v_cvt_f16_f32_e32 v52, v54
	v_cvt_f16_f32_e32 v53, v55
	v_cvt_pk_f16_f32 v49, v54, v55
	v_cvt_f16_f32_e32 v55, v51
	v_cvt_f16_f32_e32 v63, v57
	v_cvt_f16_f32_e32 v54, v50
	v_cvt_f16_f32_e32 v62, v56
	v_cvt_pk_f16_f32 v50, v50, v51
	v_cvt_pk_f16_f32 v51, v56, v57
	v_cvt_f32_f16_e32 v57, v59
	v_cvt_f32_f16_e32 v59, v52
	v_cvt_f32_f16_e32 v53, v53
	v_cvt_f32_f16_e32 v55, v55
	v_cvt_f32_f16_e32 v56, v58
	v_cvt_f32_f16_e32 v63, v63
	v_cvt_f32_f16_e32 v96, v54
	v_cvt_f32_f16_e32 v97, v62
	v_add_f32_e32 v59, v59, v53
	v_mul_f32_e32 v53, v53, v53
	v_fma_mix_f32 v52, v52, v52, v53 op_sel_hi:[1,1,0]
	v_mul_f32_e32 v53, v55, v55
	v_add_f32_e32 v56, v56, v57
	v_mul_f32_e32 v57, v57, v57
	v_fma_mix_f32 v53, v54, v54, v53 op_sel_hi:[1,1,0]
	v_mul_f32_e32 v54, v63, v63
	v_add_f32_e32 v56, v56, v59
	v_add_f32_e32 v59, v96, v55
	v_add_f32_e32 v96, v97, v63
	v_fma_mix_f32 v57, v58, v58, v57 op_sel_hi:[1,1,0]
	v_fma_mix_f32 v54, v62, v62, v54 op_sel_hi:[1,1,0]
	v_add_f32_e32 v59, v59, v96
	v_add_f32_e32 v52, v57, v52
	v_add_f32_e32 v53, v53, v54
	v_add_f32_e32 v56, v56, v59
	v_add_f32_e32 v52, v52, v53
	v_add_f32_e32 v56, v61, v56
	v_add_f32_e32 v57, v60, v52
	ds_bpermute_b32 v58, v221, v56
	ds_bpermute_b32 v59, v221, v57
	v_cvt_f32_f16_sdwa v96, v118 dst_sel:DWORD dst_unused:UNUSED_PAD src0_sel:WORD_1
	v_cvt_f32_f16_e32 v97, v118
	v_cvt_f32_f16_e32 v99, v119
	s_waitcnt lgkmcnt(1)
	v_add_f32_e32 v60, v56, v58
	s_waitcnt lgkmcnt(0)
	v_add_f32_e32 v61, v57, v59
	v_cvt_f32_f16_sdwa v59, v116 dst_sel:DWORD dst_unused:UNUSED_PAD src0_sel:WORD_1
	v_cvt_f32_f16_e32 v58, v116
	v_cvt_f32_f16_sdwa v57, v117 dst_sel:DWORD dst_unused:UNUSED_PAD src0_sel:WORD_1
	v_cvt_f32_f16_e32 v56, v117
	v_sub_f32_e32 v59, v59, v210
	v_sub_f32_e32 v58, v58, v210
	v_sub_f32_e32 v57, v57, v210
	v_sub_f32_e32 v56, v56, v210
	v_pk_add_f32 v[46:47], v[46:47], v[206:207]
	v_pk_add_f32 v[44:45], v[44:45], v[208:209]
	v_pk_mul_f32 v[58:59], v[210:211], v[58:59] op_sel:[1,0]
	v_pk_mul_f32 v[56:57], v[210:211], v[56:57] op_sel:[1,0]
	v_pk_fma_f32 v[44:45], v[92:93], v[58:59], v[44:45]
	v_pk_fma_f32 v[46:47], v[94:95], v[56:57], v[46:47]
	v_sub_f32_e32 v56, v99, v210
	v_sub_f32_e32 v57, v98, v210
	v_sub_f32_e32 v58, v97, v210
	v_sub_f32_e32 v59, v96, v210
	v_pk_add_f32 v[42:43], v[42:43], v[202:203]
	v_pk_add_f32 v[40:41], v[40:41], v[204:205]
	v_pk_mul_f32 v[58:59], v[210:211], v[58:59] op_sel:[1,0]
	v_pk_mul_f32 v[56:57], v[210:211], v[56:57] op_sel:[1,0]
	ds_write_b128 v235, v[48:51] offset:64
	v_pk_fma_f32 v[56:57], v[90:91], v[56:57], v[42:43]
	v_pk_fma_f32 v[42:43], v[88:89], v[58:59], v[40:41]
	v_cvt_f16_f32_e32 v58, v44
	v_cvt_f16_f32_e32 v59, v45
	v_cvt_pk_f16_f32 v40, v44, v45
	v_cvt_f16_f32_e32 v44, v46
	v_cvt_f16_f32_e32 v45, v47
	v_cvt_pk_f16_f32 v41, v46, v47
	v_cvt_f16_f32_e32 v46, v42
	v_cvt_f16_f32_e32 v47, v43
	v_cvt_f16_f32_e32 v96, v56
	v_cvt_f16_f32_e32 v97, v57
	v_cvt_pk_f16_f32 v42, v42, v43
	v_cvt_pk_f16_f32 v43, v56, v57
	ds_read_b128 v[48:51], v236
	ds_read_b128 v[52:55], v236 offset:1152
	ds_write_b128 v235, v[40:43]
	v_cvt_f32_f16_e32 v40, v58
	v_cvt_f32_f16_e32 v41, v59
	v_cvt_f32_f16_e32 v42, v44
	v_cvt_f32_f16_e32 v43, v45
	v_cvt_f32_f16_e32 v45, v46
	v_cvt_f32_f16_e32 v47, v47
	v_cvt_f32_f16_e32 v56, v96
	v_cvt_f32_f16_e32 v57, v97
	v_add_f32_e32 v40, v40, v41
	v_add_f32_e32 v42, v42, v43
	v_add_f32_e32 v40, v40, v42
	v_add_f32_e32 v42, v45, v47
	v_add_f32_e32 v45, v56, v57
	v_add_f32_e32 v42, v42, v45
	v_add_f32_e32 v40, v40, v42
	v_add_f32_e32 v45, 0, v40
	v_mul_f32_e32 v40, v41, v41
	v_mul_f32_e32 v41, v43, v43
	v_fma_mix_f32 v40, v58, v58, v40 op_sel_hi:[1,1,0]
	v_fma_mix_f32 v41, v44, v44, v41 op_sel_hi:[1,1,0]
	v_mul_f32_e32 v42, v57, v57
	v_add_f32_e32 v40, v40, v41
	v_mul_f32_e32 v41, v47, v47
	v_fma_mix_f32 v41, v46, v46, v41 op_sel_hi:[1,1,0]
	v_fma_mix_f32 v42, v96, v96, v42 op_sel_hi:[1,1,0]
	s_waitcnt vmcnt(16)
	v_cvt_f32_f16_sdwa v43, v112 dst_sel:DWORD dst_unused:UNUSED_PAD src0_sel:WORD_1
	v_add_f32_e32 v41, v41, v42
	v_add_f32_e32 v44, v40, v41
	v_cvt_f32_f16_e32 v42, v112
	v_cvt_f32_f16_sdwa v41, v113 dst_sel:DWORD dst_unused:UNUSED_PAD src0_sel:WORD_1
	v_cvt_f32_f16_e32 v40, v113
	v_cvt_f32_f16_sdwa v46, v114 dst_sel:DWORD dst_unused:UNUSED_PAD src0_sel:WORD_1
	v_cvt_f32_f16_e32 v47, v114
	v_cvt_f32_f16_sdwa v56, v115 dst_sel:DWORD dst_unused:UNUSED_PAD src0_sel:WORD_1
	v_cvt_f32_f16_e32 v57, v115
	v_sub_f32_e32 v40, v40, v210
	v_sub_f32_e32 v41, v41, v210
	v_sub_f32_e32 v42, v42, v210
	v_sub_f32_e32 v43, v43, v210
	v_pk_add_f32 v[38:39], v[38:39], v[198:199]
	v_pk_add_f32 v[36:37], v[36:37], v[200:201]
	v_pk_mul_f32 v[42:43], v[210:211], v[42:43] op_sel:[1,0]
	v_pk_mul_f32 v[40:41], v[210:211], v[40:41] op_sel:[1,0]
	v_pk_fma_f32 v[36:37], v[80:81], v[42:43], v[36:37]
	v_pk_fma_f32 v[38:39], v[82:83], v[40:41], v[38:39]
	v_sub_f32_e32 v40, v57, v210
	v_sub_f32_e32 v41, v56, v210
	v_sub_f32_e32 v42, v47, v210
	v_sub_f32_e32 v43, v46, v210
	v_pk_add_f32 v[34:35], v[34:35], v[192:193]
	v_pk_add_f32 v[32:33], v[32:33], v[194:195]
	v_pk_mul_f32 v[42:43], v[210:211], v[42:43] op_sel:[1,0]
	v_pk_mul_f32 v[40:41], v[210:211], v[40:41] op_sel:[1,0]
	ds_bpermute_b32 v62, v237, v60
	v_pk_fma_f32 v[40:41], v[74:75], v[40:41], v[34:35]
	v_pk_fma_f32 v[34:35], v[72:73], v[42:43], v[32:33]
	v_cvt_f16_f32_e32 v42, v36
	v_cvt_f16_f32_e32 v43, v37
	v_cvt_pk_f16_f32 v32, v36, v37
	v_cvt_f16_f32_e32 v36, v38
	v_cvt_f16_f32_e32 v37, v39
	v_cvt_pk_f16_f32 v33, v38, v39
	v_cvt_f16_f32_e32 v39, v35
	v_cvt_f16_f32_e32 v47, v41
	v_cvt_f16_f32_e32 v38, v34
	v_cvt_f16_f32_e32 v46, v40
	v_cvt_f32_f16_e32 v57, v36
	v_cvt_f32_f16_e32 v37, v37
	v_cvt_f32_f16_e32 v39, v39
	v_cvt_f32_f16_e32 v56, v42
	v_cvt_f32_f16_e32 v43, v43
	v_cvt_f32_f16_e32 v47, v47
	v_cvt_f32_f16_e32 v58, v38
	v_cvt_f32_f16_e32 v59, v46
	v_add_f32_e32 v57, v57, v37
	v_mul_f32_e32 v37, v37, v37
	v_fma_mix_f32 v36, v36, v36, v37 op_sel_hi:[1,1,0]
	v_mul_f32_e32 v37, v39, v39
	v_add_f32_e32 v56, v56, v43
	v_mul_f32_e32 v43, v43, v43
	v_fma_mix_f32 v37, v38, v38, v37 op_sel_hi:[1,1,0]
	v_mul_f32_e32 v38, v47, v47
	v_add_f32_e32 v56, v56, v57
	v_add_f32_e32 v57, v58, v39
	v_add_f32_e32 v58, v59, v47
	v_fma_mix_f32 v42, v42, v42, v43 op_sel_hi:[1,1,0]
	v_fma_mix_f32 v38, v46, v46, v38 op_sel_hi:[1,1,0]
	v_add_f32_e32 v57, v57, v58
	v_add_f32_e32 v36, v42, v36
	v_add_f32_e32 v37, v37, v38
	v_add_f32_e32 v56, v56, v57
	v_add_f32_e32 v36, v36, v37
	v_add_f32_e32 v45, v45, v56
	v_add_f32_e32 v36, v44, v36
	ds_bpermute_b32 v37, v221, v45
	ds_bpermute_b32 v38, v221, v36
	v_cvt_pk_f16_f32 v34, v34, v35
	v_cvt_pk_f16_f32 v35, v40, v41
	ds_write_b128 v235, v[32:35] offset:64
	s_waitcnt lgkmcnt(2)
	v_add_f32_e32 v32, v45, v37
	s_waitcnt lgkmcnt(1)
	v_add_f32_e32 v33, v36, v38
	ds_bpermute_b32 v63, v237, v61
	ds_bpermute_b32 v44, v237, v32
	ds_bpermute_b32 v45, v237, v33
	ds_read_b128 v[34:37], v236
	ds_read_b128 v[38:41], v236 offset:1152
	v_add_f32_e32 v42, v60, v62
	s_waitcnt lgkmcnt(4)
	v_add_f32_e32 v43, v61, v63
	s_waitcnt lgkmcnt(3)
	v_add_f32_e32 v44, v32, v44
	s_waitcnt lgkmcnt(2)
	v_add_f32_e32 v45, v33, v45
	v_add_u32_e32 v32, 0x30000, v144
	buffer_store_dwordx4 v[48:51], v32, s[24:27], 0 offen nt
	v_add_u32_e32 v32, 0x33000, v144
	buffer_store_dwordx4 v[52:55], v32, s[24:27], 0 offen nt
	v_add_co_u32_e32 v32, vcc, s76, v140
	s_nop 1
	v_addc_co_u32_e32 v33, vcc, 0, v141, vcc
	global_store_dwordx2 v[32:33], v[42:43], off
	v_add_u32_e32 v42, 0x36000, v144
	s_waitcnt lgkmcnt(1)
	buffer_store_dwordx4 v[34:37], v42, s[24:27], 0 offen nt
	s_nop 1
	v_add_u32_e32 v34, 0x39000, v144
	s_waitcnt lgkmcnt(0)
	buffer_store_dwordx4 v[38:41], v34, s[24:27], 0 offen nt
	global_store_dwordx2 v[32:33], v[44:45], off offset:1536
	s_waitcnt vmcnt(15)
	v_cvt_f32_f16_sdwa v37, v84 dst_sel:DWORD dst_unused:UNUSED_PAD src0_sel:WORD_1
	v_cvt_f32_f16_e32 v36, v84
	v_cvt_f32_f16_sdwa v35, v85 dst_sel:DWORD dst_unused:UNUSED_PAD src0_sel:WORD_1
	v_cvt_f32_f16_e32 v34, v85
	v_cvt_f32_f16_sdwa v38, v86 dst_sel:DWORD dst_unused:UNUSED_PAD src0_sel:WORD_1
	v_cvt_f32_f16_e32 v39, v86
	v_cvt_f32_f16_sdwa v40, v87 dst_sel:DWORD dst_unused:UNUSED_PAD src0_sel:WORD_1
	v_cvt_f32_f16_e32 v41, v87
	v_sub_f32_e32 v34, v34, v196
	v_sub_f32_e32 v35, v35, v196
	v_sub_f32_e32 v36, v36, v196
	v_sub_f32_e32 v37, v37, v196
	v_pk_add_f32 v[30:31], v[30:31], v[206:207]
	v_pk_add_f32 v[28:29], v[28:29], v[208:209]
	v_pk_mul_f32 v[36:37], v[196:197], v[36:37] op_sel:[1,0]
	v_pk_mul_f32 v[34:35], v[196:197], v[34:35] op_sel:[1,0]
	v_pk_fma_f32 v[28:29], v[92:93], v[36:37], v[28:29]
	v_pk_fma_f32 v[30:31], v[94:95], v[34:35], v[30:31]
	v_sub_f32_e32 v34, v41, v196
	v_sub_f32_e32 v35, v40, v196
	v_sub_f32_e32 v36, v39, v196
	v_sub_f32_e32 v37, v38, v196
	v_pk_add_f32 v[26:27], v[26:27], v[202:203]
	v_pk_add_f32 v[24:25], v[24:25], v[204:205]
	v_pk_mul_f32 v[36:37], v[196:197], v[36:37] op_sel:[1,0]
	v_pk_mul_f32 v[34:35], v[196:197], v[34:35] op_sel:[1,0]
	v_pk_add_f32 v[22:23], v[22:23], v[198:199]
	v_pk_fma_f32 v[34:35], v[90:91], v[34:35], v[26:27]
	v_pk_fma_f32 v[26:27], v[88:89], v[36:37], v[24:25]
	v_cvt_f16_f32_e32 v36, v28
	v_cvt_f16_f32_e32 v37, v29
	v_cvt_pk_f16_f32 v24, v28, v29
	v_cvt_f16_f32_e32 v28, v30
	v_cvt_f16_f32_e32 v29, v31
	v_cvt_pk_f16_f32 v25, v30, v31
	v_cvt_f16_f32_e32 v30, v26
	v_cvt_f16_f32_e32 v31, v27
	v_cvt_f16_f32_e32 v38, v34
	v_cvt_f16_f32_e32 v39, v35
	v_cvt_pk_f16_f32 v26, v26, v27
	v_cvt_pk_f16_f32 v27, v34, v35
	ds_write_b128 v235, v[24:27]
	v_cvt_f32_f16_e32 v24, v36
	v_cvt_f32_f16_e32 v25, v37
	v_cvt_f32_f16_e32 v26, v28
	v_cvt_f32_f16_e32 v27, v29
	v_cvt_f32_f16_e32 v29, v30
	v_cvt_f32_f16_e32 v31, v31
	v_cvt_f32_f16_e32 v34, v38
	v_cvt_f32_f16_e32 v35, v39
	v_add_f32_e32 v24, v24, v25
	v_add_f32_e32 v26, v26, v27
	v_add_f32_e32 v24, v24, v26
	v_add_f32_e32 v26, v29, v31
	v_add_f32_e32 v29, v34, v35
	v_add_f32_e32 v26, v26, v29
	v_add_f32_e32 v24, v24, v26
	v_add_f32_e32 v29, 0, v24
	v_mul_f32_e32 v24, v25, v25
	v_mul_f32_e32 v25, v27, v27
	v_fma_mix_f32 v24, v36, v36, v24 op_sel_hi:[1,1,0]
	v_fma_mix_f32 v25, v28, v28, v25 op_sel_hi:[1,1,0]
	v_mul_f32_e32 v26, v35, v35
	v_add_f32_e32 v24, v24, v25
	v_mul_f32_e32 v25, v31, v31
	v_fma_mix_f32 v25, v30, v30, v25 op_sel_hi:[1,1,0]
	v_fma_mix_f32 v26, v38, v38, v26 op_sel_hi:[1,1,0]
	s_waitcnt vmcnt(14)
	v_cvt_f32_f16_sdwa v27, v76 dst_sel:DWORD dst_unused:UNUSED_PAD src0_sel:WORD_1
	v_add_f32_e32 v25, v25, v26
	v_add_f32_e32 v28, v24, v25
	v_cvt_f32_f16_e32 v26, v76
	v_cvt_f32_f16_sdwa v25, v77 dst_sel:DWORD dst_unused:UNUSED_PAD src0_sel:WORD_1
	v_cvt_f32_f16_e32 v24, v77
	v_cvt_f32_f16_sdwa v30, v78 dst_sel:DWORD dst_unused:UNUSED_PAD src0_sel:WORD_1
	v_cvt_f32_f16_e32 v31, v78
	v_cvt_f32_f16_sdwa v34, v79 dst_sel:DWORD dst_unused:UNUSED_PAD src0_sel:WORD_1
	v_cvt_f32_f16_e32 v35, v79
	v_sub_f32_e32 v24, v24, v196
	v_sub_f32_e32 v25, v25, v196
	v_sub_f32_e32 v26, v26, v196
	v_sub_f32_e32 v27, v27, v196
	v_pk_add_f32 v[20:21], v[20:21], v[200:201]
	v_pk_mul_f32 v[26:27], v[196:197], v[26:27] op_sel:[1,0]
	v_pk_mul_f32 v[24:25], v[196:197], v[24:25] op_sel:[1,0]
	v_pk_fma_f32 v[20:21], v[80:81], v[26:27], v[20:21]
	v_pk_fma_f32 v[22:23], v[82:83], v[24:25], v[22:23]
	v_sub_f32_e32 v24, v35, v196
	v_sub_f32_e32 v25, v34, v196
	v_sub_f32_e32 v26, v31, v196
	v_sub_f32_e32 v27, v30, v196
	v_pk_add_f32 v[18:19], v[18:19], v[192:193]
	v_pk_add_f32 v[16:17], v[16:17], v[194:195]
	v_pk_mul_f32 v[26:27], v[196:197], v[26:27] op_sel:[1,0]
	v_pk_mul_f32 v[24:25], v[196:197], v[24:25] op_sel:[1,0]
	s_waitcnt vmcnt(13)
	v_cvt_f32_f16_sdwa v36, v71 dst_sel:DWORD dst_unused:UNUSED_PAD src0_sel:WORD_1
	v_pk_fma_f32 v[24:25], v[74:75], v[24:25], v[18:19]
	v_pk_fma_f32 v[18:19], v[72:73], v[26:27], v[16:17]
	v_cvt_f16_f32_e32 v26, v20
	v_cvt_f16_f32_e32 v27, v21
	v_cvt_pk_f16_f32 v16, v20, v21
	v_cvt_f16_f32_e32 v20, v22
	v_cvt_f16_f32_e32 v21, v23
	v_cvt_pk_f16_f32 v17, v22, v23
	v_cvt_f16_f32_e32 v23, v19
	v_cvt_f16_f32_e32 v31, v25
	v_cvt_f16_f32_e32 v22, v18
	v_cvt_f16_f32_e32 v30, v24
	v_cvt_pk_f16_f32 v18, v18, v19
	v_cvt_pk_f16_f32 v19, v24, v25
	v_cvt_f32_f16_e32 v25, v27
	v_cvt_f32_f16_e32 v27, v20
	v_cvt_f32_f16_e32 v21, v21
	v_cvt_f32_f16_e32 v23, v23
	v_cvt_f32_f16_e32 v24, v26
	v_cvt_f32_f16_e32 v31, v31
	v_cvt_f32_f16_e32 v34, v22
	v_cvt_f32_f16_e32 v35, v30
	v_add_f32_e32 v27, v27, v21
	v_mul_f32_e32 v21, v21, v21
	v_fma_mix_f32 v20, v20, v20, v21 op_sel_hi:[1,1,0]
	v_mul_f32_e32 v21, v23, v23
	v_add_f32_e32 v24, v24, v25
	v_mul_f32_e32 v25, v25, v25
	v_fma_mix_f32 v21, v22, v22, v21 op_sel_hi:[1,1,0]
	v_mul_f32_e32 v22, v31, v31
	v_add_f32_e32 v24, v24, v27
	v_add_f32_e32 v27, v34, v23
	v_add_f32_e32 v34, v35, v31
	v_fma_mix_f32 v25, v26, v26, v25 op_sel_hi:[1,1,0]
	v_fma_mix_f32 v22, v30, v30, v22 op_sel_hi:[1,1,0]
	v_add_f32_e32 v27, v27, v34
	v_add_f32_e32 v20, v25, v20
	v_add_f32_e32 v21, v21, v22
	v_add_f32_e32 v24, v24, v27
	v_add_f32_e32 v20, v20, v21
	v_add_f32_e32 v24, v29, v24
	v_add_f32_e32 v25, v28, v20
	ds_bpermute_b32 v26, v221, v24
	ds_bpermute_b32 v27, v221, v25
	v_cvt_f32_f16_sdwa v34, v70 dst_sel:DWORD dst_unused:UNUSED_PAD src0_sel:WORD_1
	v_cvt_f32_f16_e32 v35, v70
	v_cvt_f32_f16_e32 v37, v71
	s_waitcnt lgkmcnt(1)
	v_add_f32_e32 v28, v24, v26
	s_waitcnt lgkmcnt(0)
	v_add_f32_e32 v29, v25, v27
	v_cvt_f32_f16_sdwa v27, v68 dst_sel:DWORD dst_unused:UNUSED_PAD src0_sel:WORD_1
	v_cvt_f32_f16_e32 v26, v68
	v_cvt_f32_f16_sdwa v25, v69 dst_sel:DWORD dst_unused:UNUSED_PAD src0_sel:WORD_1
	v_cvt_f32_f16_e32 v24, v69
	v_sub_f32_e32 v27, v27, v190
	v_sub_f32_e32 v26, v26, v190
	v_sub_f32_e32 v25, v25, v190
	v_sub_f32_e32 v24, v24, v190
	v_pk_add_f32 v[14:15], v[14:15], v[206:207]
	v_pk_add_f32 v[12:13], v[12:13], v[208:209]
	v_pk_mul_f32 v[26:27], v[190:191], v[26:27] op_sel:[1,0]
	v_pk_mul_f32 v[24:25], v[190:191], v[24:25] op_sel:[1,0]
	v_pk_fma_f32 v[12:13], v[92:93], v[26:27], v[12:13]
	v_pk_fma_f32 v[14:15], v[94:95], v[24:25], v[14:15]
	v_sub_f32_e32 v24, v37, v190
	v_sub_f32_e32 v25, v36, v190
	v_sub_f32_e32 v26, v35, v190
	v_sub_f32_e32 v27, v34, v190
	v_pk_add_f32 v[10:11], v[10:11], v[202:203]
	v_pk_add_f32 v[8:9], v[8:9], v[204:205]
	v_pk_mul_f32 v[26:27], v[190:191], v[26:27] op_sel:[1,0]
	v_pk_mul_f32 v[24:25], v[190:191], v[24:25] op_sel:[1,0]
	ds_write_b128 v235, v[16:19] offset:64
	v_pk_fma_f32 v[24:25], v[90:91], v[24:25], v[10:11]
	v_pk_fma_f32 v[10:11], v[88:89], v[26:27], v[8:9]
	v_cvt_f16_f32_e32 v26, v12
	v_cvt_f16_f32_e32 v27, v13
	v_cvt_pk_f16_f32 v8, v12, v13
	v_cvt_f16_f32_e32 v12, v14
	v_cvt_f16_f32_e32 v13, v15
	v_cvt_pk_f16_f32 v9, v14, v15
	v_cvt_f16_f32_e32 v14, v10
	v_cvt_f16_f32_e32 v15, v11
	v_cvt_f16_f32_e32 v34, v24
	v_cvt_f16_f32_e32 v35, v25
	v_cvt_pk_f16_f32 v10, v10, v11
	v_cvt_pk_f16_f32 v11, v24, v25
	ds_read_b128 v[16:19], v236
	ds_read_b128 v[20:23], v236 offset:1152
	ds_write_b128 v235, v[8:11]
	v_cvt_f32_f16_e32 v8, v26
	v_cvt_f32_f16_e32 v9, v27
	v_cvt_f32_f16_e32 v10, v12
	v_cvt_f32_f16_e32 v11, v13
	v_cvt_f32_f16_e32 v13, v14
	v_cvt_f32_f16_e32 v15, v15
	v_cvt_f32_f16_e32 v24, v34
	v_cvt_f32_f16_e32 v25, v35
	v_add_f32_e32 v8, v8, v9
	v_add_f32_e32 v10, v10, v11
	v_add_f32_e32 v8, v8, v10
	v_add_f32_e32 v10, v13, v15
	v_add_f32_e32 v13, v24, v25
	v_add_f32_e32 v10, v10, v13
	v_add_f32_e32 v8, v8, v10
	v_add_f32_e32 v13, 0, v8
	v_mul_f32_e32 v8, v9, v9
	v_mul_f32_e32 v9, v11, v11
	v_fma_mix_f32 v8, v26, v26, v8 op_sel_hi:[1,1,0]
	v_fma_mix_f32 v9, v12, v12, v9 op_sel_hi:[1,1,0]
	v_mul_f32_e32 v10, v25, v25
	v_add_f32_e32 v8, v8, v9
	v_mul_f32_e32 v9, v15, v15
	v_fma_mix_f32 v9, v14, v14, v9 op_sel_hi:[1,1,0]
	v_fma_mix_f32 v10, v34, v34, v10 op_sel_hi:[1,1,0]
	s_waitcnt vmcnt(12)
	v_cvt_f32_f16_sdwa v11, v64 dst_sel:DWORD dst_unused:UNUSED_PAD src0_sel:WORD_1
	v_add_f32_e32 v9, v9, v10
	v_add_f32_e32 v12, v8, v9
	v_cvt_f32_f16_e32 v10, v64
	v_cvt_f32_f16_sdwa v9, v65 dst_sel:DWORD dst_unused:UNUSED_PAD src0_sel:WORD_1
	v_cvt_f32_f16_e32 v8, v65
	v_cvt_f32_f16_sdwa v14, v66 dst_sel:DWORD dst_unused:UNUSED_PAD src0_sel:WORD_1
	v_cvt_f32_f16_e32 v15, v66
	v_cvt_f32_f16_sdwa v24, v67 dst_sel:DWORD dst_unused:UNUSED_PAD src0_sel:WORD_1
	v_cvt_f32_f16_e32 v25, v67
	v_sub_f32_e32 v8, v8, v190
	v_sub_f32_e32 v9, v9, v190
	v_sub_f32_e32 v10, v10, v190
	v_sub_f32_e32 v11, v11, v190
	v_pk_add_f32 v[6:7], v[6:7], v[198:199]
	v_pk_add_f32 v[4:5], v[4:5], v[200:201]
	v_pk_mul_f32 v[10:11], v[190:191], v[10:11] op_sel:[1,0]
	v_pk_mul_f32 v[8:9], v[190:191], v[8:9] op_sel:[1,0]
	v_pk_fma_f32 v[4:5], v[80:81], v[10:11], v[4:5]
	v_pk_fma_f32 v[6:7], v[82:83], v[8:9], v[6:7]
	v_sub_f32_e32 v8, v25, v190
	v_sub_f32_e32 v9, v24, v190
	v_sub_f32_e32 v10, v15, v190
	v_sub_f32_e32 v11, v14, v190
	v_pk_add_f32 v[2:3], v[2:3], v[192:193]
	v_pk_add_f32 v[0:1], v[0:1], v[194:195]
	v_pk_mul_f32 v[10:11], v[190:191], v[10:11] op_sel:[1,0]
	v_pk_mul_f32 v[8:9], v[190:191], v[8:9] op_sel:[1,0]
	ds_bpermute_b32 v30, v237, v28
	v_pk_fma_f32 v[8:9], v[74:75], v[8:9], v[2:3]
	v_pk_fma_f32 v[2:3], v[72:73], v[10:11], v[0:1]
	v_cvt_f16_f32_e32 v10, v4
	v_cvt_f16_f32_e32 v11, v5
	v_cvt_pk_f16_f32 v0, v4, v5
	v_cvt_f16_f32_e32 v4, v6
	v_cvt_f16_f32_e32 v5, v7
	v_cvt_pk_f16_f32 v1, v6, v7
	v_cvt_f16_f32_e32 v7, v3
	v_cvt_f16_f32_e32 v15, v9
	v_cvt_f16_f32_e32 v6, v2
	v_cvt_f16_f32_e32 v14, v8
	v_cvt_f32_f16_e32 v25, v4
	v_cvt_f32_f16_e32 v5, v5
	v_cvt_f32_f16_e32 v7, v7
	v_cvt_f32_f16_e32 v24, v10
	v_cvt_f32_f16_e32 v11, v11
	v_cvt_f32_f16_e32 v15, v15
	v_cvt_f32_f16_e32 v26, v6
	v_cvt_f32_f16_e32 v27, v14
	v_add_f32_e32 v25, v25, v5
	v_mul_f32_e32 v5, v5, v5
	v_fma_mix_f32 v4, v4, v4, v5 op_sel_hi:[1,1,0]
	v_mul_f32_e32 v5, v7, v7
	v_add_f32_e32 v24, v24, v11
	v_mul_f32_e32 v11, v11, v11
	v_fma_mix_f32 v5, v6, v6, v5 op_sel_hi:[1,1,0]
	v_mul_f32_e32 v6, v15, v15
	v_add_f32_e32 v24, v24, v25
	v_add_f32_e32 v25, v26, v7
	v_add_f32_e32 v26, v27, v15
	v_fma_mix_f32 v10, v10, v10, v11 op_sel_hi:[1,1,0]
	v_fma_mix_f32 v6, v14, v14, v6 op_sel_hi:[1,1,0]
	v_add_f32_e32 v25, v25, v26
	v_add_f32_e32 v4, v10, v4
	v_add_f32_e32 v5, v5, v6
	v_add_f32_e32 v24, v24, v25
	v_add_f32_e32 v4, v4, v5
	v_add_f32_e32 v13, v13, v24
	v_add_f32_e32 v4, v12, v4
	ds_bpermute_b32 v5, v221, v13
	ds_bpermute_b32 v6, v221, v4
	v_cvt_pk_f16_f32 v2, v2, v3
	v_cvt_pk_f16_f32 v3, v8, v9
	ds_write_b128 v235, v[0:3] offset:64
	s_waitcnt lgkmcnt(2)
	v_add_f32_e32 v10, v13, v5
	s_waitcnt lgkmcnt(1)
	v_add_f32_e32 v11, v4, v6
	ds_bpermute_b32 v31, v237, v29
	ds_bpermute_b32 v12, v237, v10
	ds_bpermute_b32 v13, v237, v11
	ds_read_b128 v[0:3], v236
	ds_read_b128 v[4:7], v236 offset:1152
	v_add_f32_e32 v8, v28, v30
	s_waitcnt lgkmcnt(4)
	v_add_f32_e32 v9, v29, v31
	s_waitcnt lgkmcnt(3)
	v_add_f32_e32 v10, v10, v12
	s_waitcnt lgkmcnt(2)
	v_add_f32_e32 v11, v11, v13
	v_add_u32_e32 v12, 0x3c000, v144
	buffer_store_dwordx4 v[16:19], v12, s[24:27], 0 offen nt
	v_add_u32_e32 v12, 0x3f000, v144
	buffer_store_dwordx4 v[20:23], v12, s[24:27], 0 offen nt
	global_store_dwordx2 v[32:33], v[8:9], off offset:3072
	v_add_u32_e32 v8, 0x42000, v144
	s_waitcnt lgkmcnt(1)
	buffer_store_dwordx4 v[0:3], v8, s[24:27], 0 offen nt
	s_nop 1
	v_add_u32_e32 v0, 0x45000, v144
	s_waitcnt lgkmcnt(0)
	buffer_store_dwordx4 v[4:7], v0, s[24:27], 0 offen nt
	v_add_co_u32_e32 v0, vcc, 0x4000, v140
	s_nop 1
	v_addc_co_u32_e32 v1, vcc, 0, v141, vcc
	global_store_dwordx2 v[0:1], v[10:11], off offset:512
	s_mov_b32 s83, s81
	s_mov_b32 s84, s82
	s_mov_b64 s[40:41], s[0:1]
	s_mov_b64 s[38:39], s[8:9]
	s_mov_b64 vcc, s[6:7]
	s_cbranch_vccz .LBB8_12
	s_waitcnt vmcnt(0)
	s_cmpk_gt_u32 s44, 0xff
	s_cbranch_scc1 .LBB8_31
	s_barrier

.LBB8_32:
	s_endpgm
	s_endpgm
	s_endpgm
	.section	.rodata,"a",@progbits
	.p2align	6, 0x0
	.amdhsa_kernel _Z6k_gemmIN2pg6EpiResELi768EEvNS0_4GemmET_
		.amdhsa_group_segment_fixed_size 0
		.amdhsa_private_segment_fixed_size 0
		.amdhsa_kernarg_size 344
		.amdhsa_user_sgpr_count 2
		.amdhsa_user_sgpr_dispatch_ptr 0
		.amdhsa_user_sgpr_queue_ptr 0
		.amdhsa_user_sgpr_kernarg_segment_ptr 1
		.amdhsa_user_sgpr_dispatch_id 0
		.amdhsa_user_sgpr_kernarg_preload_length 0
		.amdhsa_user_sgpr_kernarg_preload_offset 0
		.amdhsa_user_sgpr_private_segment_size 0
		.amdhsa_uses_dynamic_stack 0
		.amdhsa_enable_private_segment 0
		.amdhsa_system_sgpr_workgroup_id_x 1
		.amdhsa_system_sgpr_workgroup_id_y 0
		.amdhsa_system_sgpr_workgroup_id_z 0
		.amdhsa_system_sgpr_workgroup_info 0
		.amdhsa_system_vgpr_workitem_id 0
		.amdhsa_next_free_vgpr 254
		.amdhsa_next_free_sgpr 96
		.amdhsa_accum_offset 256
		.amdhsa_reserve_vcc 1
		.amdhsa_float_round_mode_32 0
		.amdhsa_float_round_mode_16_64 0
		.amdhsa_float_denorm_mode_32 3
		.amdhsa_float_denorm_mode_16_64 3
		.amdhsa_dx10_clamp 1
		.amdhsa_ieee_mode 1
		.amdhsa_fp16_overflow 0
		.amdhsa_tg_split 0
		.amdhsa_exception_fp_ieee_invalid_op 0
		.amdhsa_exception_fp_denorm_src 0
		.amdhsa_exception_fp_ieee_div_zero 0
		.amdhsa_exception_fp_ieee_overflow 0
		.amdhsa_exception_fp_ieee_underflow 0
		.amdhsa_exception_fp_ieee_inexact 0
		.amdhsa_exception_int_div_zero 0
	.end_amdhsa_kernel

.LBB10_27:
	ds_read_b128 v[72:75], v231
	ds_read_b128 v[80:83], v231 offset:1024
	ds_read_b128 v[88:91], v231 offset:2048
	ds_read_b128 v[92:95], v231 offset:3072
	s_add_u32 s40, s38, 0xfff40080
	s_addc_u32 s41, s39, -1
	s_cmp_eq_u32 s87, 44
	s_cselect_b32 s43, s9, s41
	s_cselect_b32 s42, s8, s40
	s_cselect_b32 s41, s1, s86
	s_cselect_b32 s40, s0, s85
	v_lshl_add_u64 v[190:191], s[38:39], 0, v[184:185]
	s_add_i32 m0, s51, 0xc000
	ds_read_b128 v[136:139], v232
	ds_read_b128 v[148:151], v232 offset:1024
	ds_read_b128 v[152:155], v232 offset:2048
	ds_read_b128 v[156:159], v232 offset:3072
	ds_read_b128 v[160:163], v232 offset:4096
	ds_read_b128 v[164:167], v232 offset:5120
	ds_read_b128 v[168:171], v232 offset:6144
	ds_read_b128 v[172:175], v232 offset:7168
	global_load_lds_dwordx4 v[190:191], off
	v_lshl_add_u64 v[190:191], s[38:39], 0, v[186:187]
	s_add_i32 m0, s51, 0xe000
	s_nop 0
	global_load_lds_dwordx4 v[190:191], off
	s_waitcnt lgkmcnt(8)
	s_barrier
	s_waitcnt lgkmcnt(0)
	s_setprio 1
	s_waitcnt lgkmcnt(0)
	v_mfma_f32_16x16x32_f16 v[144:147], v[72:75], v[136:139], v[144:147]
	v_mfma_f32_16x16x32_f16 v[140:143], v[88:91], v[136:139], v[140:143]
	v_mfma_f32_16x16x32_f16 v[124:127], v[72:75], v[152:155], v[124:127]
	v_mfma_f32_16x16x32_f16 v[120:123], v[88:91], v[152:155], v[120:123]
	v_mfma_f32_16x16x32_f16 v[108:111], v[72:75], v[160:163], v[108:111]
	v_mfma_f32_16x16x32_f16 v[104:107], v[88:91], v[160:163], v[104:107]
	v_mfma_f32_16x16x32_f16 v[84:87], v[72:75], v[168:171], v[84:87]
	v_mfma_f32_16x16x32_f16 v[76:79], v[88:91], v[168:171], v[76:79]
	v_mfma_f32_16x16x32_f16 v[144:147], v[80:83], v[148:151], v[144:147]
	v_mfma_f32_16x16x32_f16 v[140:143], v[92:95], v[148:151], v[140:143]
	v_mfma_f32_16x16x32_f16 v[124:127], v[80:83], v[156:159], v[124:127]
	v_mfma_f32_16x16x32_f16 v[120:123], v[92:95], v[156:159], v[120:123]
	v_mfma_f32_16x16x32_f16 v[108:111], v[80:83], v[164:167], v[108:111]
	v_mfma_f32_16x16x32_f16 v[104:107], v[92:95], v[164:167], v[104:107]
	v_mfma_f32_16x16x32_f16 v[84:87], v[80:83], v[172:175], v[84:87]
	v_mfma_f32_16x16x32_f16 v[76:79], v[92:95], v[172:175], v[76:79]
	s_setprio 0
	s_barrier
	s_add_i32 s88, s69, s50
	v_lshl_add_u64 v[206:207], s[40:41], 0, v[178:179]
	s_mov_b32 m0, s88
	ds_read_b128 v[190:193], v233
	ds_read_b128 v[194:197], v233 offset:1024
	ds_read_b128 v[198:201], v233 offset:2048
	ds_read_b128 v[202:205], v233 offset:3072
	global_load_lds_dwordx4 v[206:207], off
	v_lshl_add_u64 v[208:209], s[40:41], 0, v[182:183]
	s_add_i32 m0, s88, 0x2000
	s_nop 0
	global_load_lds_dwordx4 v[208:209], off
	s_barrier
	s_waitcnt lgkmcnt(0)
	s_setprio 1
	s_waitcnt lgkmcnt(0)
	v_mfma_f32_16x16x32_f16 v[132:135], v[190:193], v[136:139], v[132:135]
	v_mfma_f32_16x16x32_f16 v[128:131], v[198:201], v[136:139], v[128:131]
	v_mfma_f32_16x16x32_f16 v[116:119], v[190:193], v[152:155], v[116:119]
	v_mfma_f32_16x16x32_f16 v[112:115], v[198:201], v[152:155], v[112:115]
	v_mfma_f32_16x16x32_f16 v[100:103], v[190:193], v[160:163], v[100:103]
	v_mfma_f32_16x16x32_f16 v[96:99], v[198:201], v[160:163], v[96:99]
	v_mfma_f32_16x16x32_f16 v[68:71], v[190:193], v[168:171], v[68:71]
	v_mfma_f32_16x16x32_f16 v[64:67], v[198:201], v[168:171], v[64:67]
	v_mfma_f32_16x16x32_f16 v[132:135], v[194:197], v[148:151], v[132:135]
	v_mfma_f32_16x16x32_f16 v[128:131], v[202:205], v[148:151], v[128:131]
	v_mfma_f32_16x16x32_f16 v[116:119], v[194:197], v[156:159], v[116:119]
	v_mfma_f32_16x16x32_f16 v[112:115], v[202:205], v[156:159], v[112:115]
	v_mfma_f32_16x16x32_f16 v[100:103], v[194:197], v[164:167], v[100:103]
	v_mfma_f32_16x16x32_f16 v[96:99], v[202:205], v[164:167], v[96:99]
	v_mfma_f32_16x16x32_f16 v[68:71], v[194:197], v[172:175], v[68:71]
	v_mfma_f32_16x16x32_f16 v[64:67], v[202:205], v[172:175], v[64:67]
	s_setprio 0
	s_mov_b32 m0, s51
	v_lshl_add_u64 v[210:211], s[42:43], 0, v[176:177]
	s_barrier
	ds_read_b128 v[136:139], v232 offset:16384
	ds_read_b128 v[148:151], v232 offset:17408
	ds_read_b128 v[152:155], v232 offset:18432
	ds_read_b128 v[156:159], v232 offset:19456
	ds_read_b128 v[160:163], v232 offset:20480
	ds_read_b128 v[164:167], v232 offset:21504
	ds_read_b128 v[168:171], v232 offset:22528
	ds_read_b128 v[172:175], v232 offset:23552
	global_load_lds_dwordx4 v[210:211], off
	v_lshl_add_u64 v[212:213], s[42:43], 0, v[180:181]
	s_mov_b32 m0, s52
	s_nop 0
	global_load_lds_dwordx4 v[212:213], off
	s_barrier
	s_waitcnt lgkmcnt(0)
	s_setprio 1
	s_waitcnt lgkmcnt(0)
	v_mfma_f32_16x16x32_f16 v[60:63], v[72:75], v[136:139], v[60:63]
	v_mfma_f32_16x16x32_f16 v[56:59], v[88:91], v[136:139], v[56:59]
	v_mfma_f32_16x16x32_f16 v[44:47], v[72:75], v[152:155], v[44:47]
	v_mfma_f32_16x16x32_f16 v[40:43], v[88:91], v[152:155], v[40:43]
	v_mfma_f32_16x16x32_f16 v[28:31], v[72:75], v[160:163], v[28:31]
	v_mfma_f32_16x16x32_f16 v[24:27], v[88:91], v[160:163], v[24:27]
	v_mfma_f32_16x16x32_f16 v[12:15], v[72:75], v[168:171], v[12:15]
	v_mfma_f32_16x16x32_f16 v[8:11], v[88:91], v[168:171], v[8:11]
	v_mfma_f32_16x16x32_f16 v[60:63], v[80:83], v[148:151], v[60:63]
	v_mfma_f32_16x16x32_f16 v[56:59], v[92:95], v[148:151], v[56:59]
	v_mfma_f32_16x16x32_f16 v[44:47], v[80:83], v[156:159], v[44:47]
	v_mfma_f32_16x16x32_f16 v[40:43], v[92:95], v[156:159], v[40:43]
	v_mfma_f32_16x16x32_f16 v[28:31], v[80:83], v[164:167], v[28:31]
	v_mfma_f32_16x16x32_f16 v[24:27], v[92:95], v[164:167], v[24:27]
	v_mfma_f32_16x16x32_f16 v[12:15], v[80:83], v[172:175], v[12:15]
	v_mfma_f32_16x16x32_f16 v[8:11], v[92:95], v[172:175], v[8:11]
	s_setprio 0
	s_barrier
	s_add_u32 s88, s40, 0x30000
	s_addc_u32 s89, s41, 0
	s_add_i32 s90, s70, s50
	v_lshl_add_u64 v[72:73], s[88:89], 0, v[178:179]
	s_mov_b32 m0, s90
	s_nop 0
	global_load_lds_dwordx4 v[72:73], off
	v_lshl_add_u64 v[72:73], s[88:89], 0, v[182:183]
	s_add_i32 m0, s90, 0x2000
	s_nop 0
	global_load_lds_dwordx4 v[72:73], off
	s_waitcnt vmcnt(6)
	s_barrier
	s_setprio 1
	v_mfma_f32_16x16x32_f16 v[52:55], v[190:193], v[136:139], v[52:55]
	v_mfma_f32_16x16x32_f16 v[48:51], v[198:201], v[136:139], v[48:51]
	v_mfma_f32_16x16x32_f16 v[36:39], v[190:193], v[152:155], v[36:39]
	v_mfma_f32_16x16x32_f16 v[32:35], v[198:201], v[152:155], v[32:35]
	v_mfma_f32_16x16x32_f16 v[20:23], v[190:193], v[160:163], v[20:23]
	v_mfma_f32_16x16x32_f16 v[16:19], v[198:201], v[160:163], v[16:19]
	v_mfma_f32_16x16x32_f16 v[4:7], v[190:193], v[168:171], v[4:7]
	v_mfma_f32_16x16x32_f16 v[0:3], v[198:201], v[168:171], v[0:3]
	v_mfma_f32_16x16x32_f16 v[52:55], v[194:197], v[148:151], v[52:55]
	v_mfma_f32_16x16x32_f16 v[48:51], v[202:205], v[148:151], v[48:51]
	v_mfma_f32_16x16x32_f16 v[36:39], v[194:197], v[156:159], v[36:39]
	v_mfma_f32_16x16x32_f16 v[32:35], v[202:205], v[156:159], v[32:35]
	v_mfma_f32_16x16x32_f16 v[20:23], v[194:197], v[164:167], v[20:23]
	v_mfma_f32_16x16x32_f16 v[16:19], v[202:205], v[164:167], v[16:19]
	v_mfma_f32_16x16x32_f16 v[4:7], v[194:197], v[172:175], v[4:7]
	v_mfma_f32_16x16x32_f16 v[0:3], v[202:205], v[172:175], v[0:3]
	s_setprio 0
	s_add_i32 s88, 0, 0x18000
	v_add_u32_e32 v92, s88, v228
	s_barrier
	ds_read_b128 v[72:75], v92
	ds_read_b128 v[80:83], v92 offset:1024
	ds_read_b128 v[88:91], v92 offset:2048
	ds_read_b128 v[92:95], v92 offset:3072
	s_add_u32 s42, s42, 0xc0000
	s_addc_u32 s43, s43, 0
	s_mov_b32 m0, s53
	v_lshl_add_u64 v[190:191], s[42:43], 0, v[176:177]
	ds_read_b128 v[136:139], v232 offset:32768
	ds_read_b128 v[148:151], v232 offset:33792
	ds_read_b128 v[152:155], v232 offset:34816
	ds_read_b128 v[156:159], v232 offset:35840
	ds_read_b128 v[160:163], v232 offset:36864
	ds_read_b128 v[164:167], v232 offset:37888
	ds_read_b128 v[168:171], v232 offset:38912
	ds_read_b128 v[172:175], v232 offset:39936
	global_load_lds_dwordx4 v[190:191], off
	v_lshl_add_u64 v[190:191], s[42:43], 0, v[180:181]
	s_mov_b32 m0, s54
	s_nop 0
	global_load_lds_dwordx4 v[190:191], off
	s_waitcnt lgkmcnt(8)
	s_barrier
	s_waitcnt lgkmcnt(0)
	s_setprio 1
	s_waitcnt lgkmcnt(0)
	v_mfma_f32_16x16x32_f16 v[144:147], v[72:75], v[136:139], v[144:147]
	v_mfma_f32_16x16x32_f16 v[140:143], v[88:91], v[136:139], v[140:143]
	v_mfma_f32_16x16x32_f16 v[124:127], v[72:75], v[152:155], v[124:127]
	v_mfma_f32_16x16x32_f16 v[120:123], v[88:91], v[152:155], v[120:123]
	v_mfma_f32_16x16x32_f16 v[108:111], v[72:75], v[160:163], v[108:111]
	v_mfma_f32_16x16x32_f16 v[104:107], v[88:91], v[160:163], v[104:107]
	v_mfma_f32_16x16x32_f16 v[84:87], v[72:75], v[168:171], v[84:87]
	v_mfma_f32_16x16x32_f16 v[76:79], v[88:91], v[168:171], v[76:79]
	v_mfma_f32_16x16x32_f16 v[144:147], v[80:83], v[148:151], v[144:147]
	v_mfma_f32_16x16x32_f16 v[140:143], v[92:95], v[148:151], v[140:143]
	v_mfma_f32_16x16x32_f16 v[124:127], v[80:83], v[156:159], v[124:127]
	v_mfma_f32_16x16x32_f16 v[120:123], v[92:95], v[156:159], v[120:123]
	v_mfma_f32_16x16x32_f16 v[108:111], v[80:83], v[164:167], v[108:111]
	v_mfma_f32_16x16x32_f16 v[104:107], v[92:95], v[164:167], v[104:107]
	v_mfma_f32_16x16x32_f16 v[84:87], v[80:83], v[172:175], v[84:87]
	v_mfma_f32_16x16x32_f16 v[76:79], v[92:95], v[172:175], v[76:79]
	s_setprio 0
	s_barrier
	s_add_i32 s42, 0, 0x1c000
	s_add_i32 s43, s88, s50
	v_add_u32_e32 v202, s42, v228
	v_lshl_add_u64 v[206:207], v[206:207], 0, s[36:37]
	s_mov_b32 m0, s43
	ds_read_b128 v[190:193], v202
	ds_read_b128 v[194:197], v202 offset:1024
	ds_read_b128 v[198:201], v202 offset:2048
	ds_read_b128 v[202:205], v202 offset:3072
	global_load_lds_dwordx4 v[206:207], off
	v_lshl_add_u64 v[206:207], v[208:209], 0, s[36:37]
	s_add_i32 m0, s43, 0x2000
	s_nop 0
	global_load_lds_dwordx4 v[206:207], off
	s_barrier
	s_waitcnt lgkmcnt(0)
	s_setprio 1
	s_waitcnt lgkmcnt(0)
	v_mfma_f32_16x16x32_f16 v[132:135], v[190:193], v[136:139], v[132:135]
	v_mfma_f32_16x16x32_f16 v[128:131], v[198:201], v[136:139], v[128:131]
	v_mfma_f32_16x16x32_f16 v[116:119], v[190:193], v[152:155], v[116:119]
	v_mfma_f32_16x16x32_f16 v[112:115], v[198:201], v[152:155], v[112:115]
	v_mfma_f32_16x16x32_f16 v[100:103], v[190:193], v[160:163], v[100:103]
	v_mfma_f32_16x16x32_f16 v[96:99], v[198:201], v[160:163], v[96:99]
	v_mfma_f32_16x16x32_f16 v[68:71], v[190:193], v[168:171], v[68:71]
	v_mfma_f32_16x16x32_f16 v[64:67], v[198:201], v[168:171], v[64:67]
	v_mfma_f32_16x16x32_f16 v[132:135], v[194:197], v[148:151], v[132:135]
	v_mfma_f32_16x16x32_f16 v[128:131], v[202:205], v[148:151], v[128:131]
	v_mfma_f32_16x16x32_f16 v[116:119], v[194:197], v[156:159], v[116:119]
	v_mfma_f32_16x16x32_f16 v[112:115], v[202:205], v[156:159], v[112:115]
	v_mfma_f32_16x16x32_f16 v[100:103], v[194:197], v[164:167], v[100:103]
	v_mfma_f32_16x16x32_f16 v[96:99], v[202:205], v[164:167], v[96:99]
	v_mfma_f32_16x16x32_f16 v[68:71], v[194:197], v[172:175], v[68:71]
	v_mfma_f32_16x16x32_f16 v[64:67], v[202:205], v[172:175], v[64:67]
	s_setprio 0
	s_mov_b32 m0, s58
	v_lshl_add_u64 v[206:207], v[210:211], 0, s[36:37]
	s_barrier
	ds_read_b128 v[136:139], v232 offset:49152
	ds_read_b128 v[148:151], v232 offset:50176
	ds_read_b128 v[152:155], v232 offset:51200
	ds_read_b128 v[156:159], v232 offset:52224
	ds_read_b128 v[160:163], v232 offset:53248
	ds_read_b128 v[164:167], v232 offset:54272
	ds_read_b128 v[168:171], v232 offset:55296
	ds_read_b128 v[172:175], v232 offset:56320
	global_load_lds_dwordx4 v[206:207], off
	v_lshl_add_u64 v[206:207], v[212:213], 0, s[36:37]
	s_mov_b32 m0, s59
	s_nop 0
	global_load_lds_dwordx4 v[206:207], off
	s_barrier
	s_waitcnt lgkmcnt(0)
	s_setprio 1
	s_waitcnt lgkmcnt(0)
	v_mfma_f32_16x16x32_f16 v[60:63], v[72:75], v[136:139], v[60:63]
	v_mfma_f32_16x16x32_f16 v[56:59], v[88:91], v[136:139], v[56:59]
	v_mfma_f32_16x16x32_f16 v[44:47], v[72:75], v[152:155], v[44:47]
	v_mfma_f32_16x16x32_f16 v[40:43], v[88:91], v[152:155], v[40:43]
	v_mfma_f32_16x16x32_f16 v[28:31], v[72:75], v[160:163], v[28:31]
	v_mfma_f32_16x16x32_f16 v[24:27], v[88:91], v[160:163], v[24:27]
	v_mfma_f32_16x16x32_f16 v[12:15], v[72:75], v[168:171], v[12:15]
	v_mfma_f32_16x16x32_f16 v[8:11], v[88:91], v[168:171], v[8:11]
	v_mfma_f32_16x16x32_f16 v[60:63], v[80:83], v[148:151], v[60:63]
	v_mfma_f32_16x16x32_f16 v[56:59], v[92:95], v[148:151], v[56:59]
	v_mfma_f32_16x16x32_f16 v[44:47], v[80:83], v[156:159], v[44:47]
	v_mfma_f32_16x16x32_f16 v[40:43], v[92:95], v[156:159], v[40:43]
	v_mfma_f32_16x16x32_f16 v[28:31], v[80:83], v[164:167], v[28:31]
	v_mfma_f32_16x16x32_f16 v[24:27], v[92:95], v[164:167], v[24:27]
	v_mfma_f32_16x16x32_f16 v[12:15], v[80:83], v[172:175], v[12:15]
	v_mfma_f32_16x16x32_f16 v[8:11], v[92:95], v[172:175], v[8:11]
	s_setprio 0
	s_barrier
	s_add_u32 s40, s40, 0x30080
	s_addc_u32 s41, s41, 0
	s_add_i32 s42, s42, s50
	v_lshl_add_u64 v[72:73], s[40:41], 0, v[178:179]
	s_mov_b32 m0, s42
	s_nop 0
	global_load_lds_dwordx4 v[72:73], off
	v_lshl_add_u64 v[72:73], s[40:41], 0, v[182:183]
	s_add_i32 m0, s42, 0x2000
	s_nop 0
	global_load_lds_dwordx4 v[72:73], off
	s_waitcnt vmcnt(6)
	s_barrier
	s_setprio 1
	v_mfma_f32_16x16x32_f16 v[52:55], v[190:193], v[136:139], v[52:55]
	v_mfma_f32_16x16x32_f16 v[48:51], v[198:201], v[136:139], v[48:51]
	v_mfma_f32_16x16x32_f16 v[36:39], v[190:193], v[152:155], v[36:39]
	v_mfma_f32_16x16x32_f16 v[32:35], v[198:201], v[152:155], v[32:35]
	v_mfma_f32_16x16x32_f16 v[20:23], v[190:193], v[160:163], v[20:23]
	v_mfma_f32_16x16x32_f16 v[16:19], v[198:201], v[160:163], v[16:19]
	v_mfma_f32_16x16x32_f16 v[4:7], v[190:193], v[168:171], v[4:7]
	v_mfma_f32_16x16x32_f16 v[0:3], v[198:201], v[168:171], v[0:3]
	v_mfma_f32_16x16x32_f16 v[52:55], v[194:197], v[148:151], v[52:55]
	v_mfma_f32_16x16x32_f16 v[48:51], v[202:205], v[148:151], v[48:51]
	v_mfma_f32_16x16x32_f16 v[36:39], v[194:197], v[156:159], v[36:39]
	v_mfma_f32_16x16x32_f16 v[32:35], v[202:205], v[156:159], v[32:35]
	v_mfma_f32_16x16x32_f16 v[20:23], v[194:197], v[164:167], v[20:23]
	v_mfma_f32_16x16x32_f16 v[16:19], v[202:205], v[164:167], v[16:19]
	v_mfma_f32_16x16x32_f16 v[4:7], v[194:197], v[172:175], v[4:7]
	v_mfma_f32_16x16x32_f16 v[0:3], v[202:205], v[172:175], v[0:3]
	s_setprio 0
	s_add_i32 s87, s87, 2
	s_add_u32 s38, s38, 0x100
	s_addc_u32 s39, s39, 0
	s_add_u32 s85, s85, 0x100
	s_addc_u32 s86, s86, 0
	s_cmp_gt_u32 s87, 45
	s_barrier
	s_cbranch_scc0 .LBB10_27
	s_lshl_b32 s38, s84, 8
	s_lshl_b32 s39, s83, 8
	s_add_i32 s38, s38, s57
	s_or_b32 s39, s39, s60
	v_or_b32_e32 v72, s39, v226
	v_or_b32_e32 v220, s38, v227
	v_mov_b64_e32 v[74:75], s[10:11]
	v_mad_i64_i32 v[74:75], s[40:41], v220, s71, v[74:75]
	v_ashrrev_i32_e32 v73, 31, v72
	v_lshl_add_u64 v[214:215], v[72:73], 1, v[74:75]
	v_add_co_u32_e32 v74, vcc, 0x6000, v214
	global_load_dwordx4 v[172:175], v[214:215], off nt
	global_load_dwordx4 v[168:171], v[214:215], off offset:64 nt
	v_addc_co_u32_e32 v75, vcc, 0, v215, vcc
	global_load_dwordx4 v[164:167], v[74:75], off nt
	global_load_dwordx4 v[160:163], v[74:75], off offset:64 nt
	v_add_co_u32_e32 v74, vcc, 0xc000, v214
	v_ashrrev_i32_e32 v221, 31, v220
	s_nop 0
	v_addc_co_u32_e32 v75, vcc, 0, v215, vcc
	global_load_dwordx4 v[156:159], v[74:75], off nt
	global_load_dwordx4 v[152:155], v[74:75], off offset:64 nt
	v_add_co_u32_e32 v74, vcc, s56, v214
	v_lshlrev_b64 v[72:73], 2, v[72:73]
	s_nop 0
	v_addc_co_u32_e32 v75, vcc, 0, v215, vcc
	global_load_dwordx4 v[148:151], v[74:75], off nt
	global_load_dwordx4 v[136:139], v[74:75], off offset:64 nt
	v_lshl_add_u64 v[74:75], v[220:221], 3, s[12:13]
	v_lshl_add_u64 v[238:239], s[14:15], 0, v[72:73]
	global_load_dwordx2 v[224:225], v[74:75], off
	global_load_dwordx2 v[222:223], v[74:75], off offset:128
	global_load_dwordx2 v[218:219], v[74:75], off offset:256
	global_load_dwordx2 v[216:217], v[74:75], off offset:384
	global_load_dwordx2 v[212:213], v[74:75], off offset:1024
	global_load_dwordx2 v[210:211], v[74:75], off offset:1152
	global_load_dwordx2 v[196:197], v[74:75], off offset:1280
	global_load_dwordx2 v[190:191], v[74:75], off offset:1408
	v_lshl_add_u64 v[242:243], s[16:17], 0, v[72:73]
	v_lshl_add_u64 v[246:247], s[18:19], 0, v[72:73]
	global_load_dwordx4 v[88:91], v[238:239], off offset:16
	global_load_dwordx4 v[92:95], v[238:239], off
	global_load_dwordx4 v[72:75], v[242:243], off offset:16
	global_load_dwordx4 v[80:83], v[242:243], off
	global_load_dwordx4 v[192:195], v[246:247], off offset:16
	global_load_dwordx4 v[198:201], v[246:247], off
	v_or_b32_e32 v221, s38, v229
	v_mul_lo_u32 v221, v221, s72
	v_and_b32_e32 v237, 64, v234
	v_add_u32_e32 v237, 64, v237
	s_lshl_b32 s38, s83, 2
	s_mov_b32 s92, 0x30000
	s_mov_b32 s93, 0
	s_mov_b32 s94, 0x6000
	s_mov_b32 s95, 0
	v_lshl_add_u64 v[250:251], v[214:215], 0, s[92:93]
	global_load_dword v252, v[250:251], off
	v_lshl_add_u64 v[250:251], v[250:251], 0, s[94:95]
	global_load_dword v252, v[250:251], off
	v_lshl_add_u64 v[250:251], v[250:251], 0, s[94:95]
	global_load_dword v252, v[250:251], off
	v_lshl_add_u64 v[250:251], v[250:251], 0, s[94:95]
	global_load_dword v252, v[250:251], off
	s_waitcnt vmcnt(0)
	v_pk_add_f32 v[202:203], v[74:75], v[194:195]
	v_pk_add_f32 v[206:207], v[82:83], v[200:201]
	v_pk_add_f32 v[208:209], v[80:81], v[198:199]
	v_pk_add_f32 v[204:205], v[72:73], v[192:193]
	global_load_dwordx4 v[72:75], v[238:239], off offset:144
	global_load_dwordx4 v[80:83], v[238:239], off offset:128
	s_nop 0
	global_load_dwordx4 v[238:241], v[242:243], off offset:144
	global_load_dwordx4 v[192:195], v[242:243], off offset:128
	s_nop 0
	global_load_dwordx4 v[242:245], v[246:247], off offset:144
	s_nop 0
	global_load_dwordx4 v[246:249], v[246:247], off offset:128
	v_pk_add_f32 v[146:147], v[146:147], v[206:207]
	v_pk_add_f32 v[144:145], v[144:145], v[208:209]
	v_pk_add_f32 v[142:143], v[142:143], v[202:203]
	v_pk_add_f32 v[140:141], v[140:141], v[204:205]
	v_pk_add_f32 v[126:127], v[126:127], v[206:207]
	v_pk_add_f32 v[124:125], v[124:125], v[208:209]
	v_pk_add_f32 v[122:123], v[122:123], v[202:203]
	v_pk_add_f32 v[120:121], v[120:121], v[204:205]
	s_waitcnt vmcnt(0)
	v_pk_add_f32 v[198:199], v[194:195], v[248:249]
	v_pk_add_f32 v[194:195], v[238:239], v[242:243]
	v_add_u32_e32 v238, s39, v221
	v_xor_b32_e32 v221, 16, v234
	v_cmp_lt_i32_e32 vcc, v221, v237
	v_xor_b32_e32 v239, 32, v234
	v_pk_add_f32 v[200:201], v[192:193], v[246:247]
	v_cndmask_b32_e32 v221, v234, v221, vcc
	v_cmp_lt_i32_e32 vcc, v239, v237
	v_pk_add_f32 v[192:193], v[240:241], v[244:245]
	v_cvt_f32_f16_e32 v240, v172
	v_cndmask_b32_e32 v237, v234, v239, vcc
	v_cvt_f32_f16_sdwa v239, v172 dst_sel:DWORD dst_unused:UNUSED_PAD src0_sel:WORD_1
	v_cvt_f32_f16_sdwa v241, v173 dst_sel:DWORD dst_unused:UNUSED_PAD src0_sel:WORD_1
	v_cvt_f32_f16_e32 v172, v173
	v_cvt_f32_f16_sdwa v242, v174 dst_sel:DWORD dst_unused:UNUSED_PAD src0_sel:WORD_1
	v_cvt_f32_f16_e32 v243, v174
	v_cvt_f32_f16_sdwa v244, v175 dst_sel:DWORD dst_unused:UNUSED_PAD src0_sel:WORD_1
	v_cvt_f32_f16_e32 v245, v175
	v_sub_f32_e32 v172, v172, v224
	v_sub_f32_e32 v173, v241, v224
	v_sub_f32_e32 v174, v240, v224
	v_sub_f32_e32 v175, v239, v224
	v_pk_mul_f32 v[174:175], v[224:225], v[174:175] op_sel:[1,0]
	v_pk_mul_f32 v[172:173], v[224:225], v[172:173] op_sel:[1,0]
	v_pk_fma_f32 v[144:145], v[174:175], v[92:93], v[144:145]
	v_pk_fma_f32 v[146:147], v[172:173], v[94:95], v[146:147]
	v_sub_f32_e32 v172, v245, v224
	v_sub_f32_e32 v173, v244, v224
	v_sub_f32_e32 v174, v243, v224
	v_sub_f32_e32 v175, v242, v224
	v_pk_mul_f32 v[174:175], v[224:225], v[174:175] op_sel:[1,0]
	v_pk_mul_f32 v[172:173], v[224:225], v[172:173] op_sel:[1,0]
	v_pk_add_f32 v[134:135], v[134:135], v[198:199]
	v_pk_fma_f32 v[172:173], v[172:173], v[90:91], v[142:143]
	v_pk_fma_f32 v[142:143], v[174:175], v[88:89], v[140:141]
	v_cvt_f16_f32_e32 v174, v144
	v_cvt_f16_f32_e32 v175, v145
	v_cvt_pk_f16_f32 v140, v144, v145
	v_cvt_f16_f32_e32 v144, v146
	v_cvt_f16_f32_e32 v145, v147
	v_cvt_pk_f16_f32 v141, v146, v147
	v_cvt_f16_f32_e32 v146, v142
	v_cvt_f16_f32_e32 v147, v143
	v_cvt_f16_f32_e32 v239, v172
	v_cvt_f16_f32_e32 v240, v173
	v_cvt_pk_f16_f32 v142, v142, v143
	v_cvt_pk_f16_f32 v143, v172, v173
	ds_write_b128 v235, v[140:143]
	v_cvt_f32_f16_e32 v140, v174
	v_cvt_f32_f16_e32 v141, v175
	v_cvt_f32_f16_e32 v142, v144
	v_cvt_f32_f16_e32 v143, v145
	v_cvt_f32_f16_e32 v145, v146
	v_cvt_f32_f16_e32 v147, v147
	v_cvt_f32_f16_e32 v172, v239
	v_cvt_f32_f16_e32 v173, v240
	v_add_f32_e32 v140, v140, v141
	v_add_f32_e32 v142, v142, v143
	v_add_f32_e32 v140, v140, v142
	v_add_f32_e32 v142, v145, v147
	v_add_f32_e32 v145, v172, v173
	v_add_f32_e32 v142, v142, v145
	v_add_f32_e32 v140, v140, v142
	v_add_f32_e32 v145, 0, v140
	v_mul_f32_e32 v140, v141, v141
	v_mul_f32_e32 v141, v143, v143
	v_fma_mix_f32 v140, v174, v174, v140 op_sel_hi:[1,1,0]
	v_fma_mix_f32 v141, v144, v144, v141 op_sel_hi:[1,1,0]
	v_mul_f32_e32 v142, v173, v173
	v_add_f32_e32 v140, v140, v141
	v_mul_f32_e32 v141, v147, v147
	v_fma_mix_f32 v141, v146, v146, v141 op_sel_hi:[1,1,0]
	v_fma_mix_f32 v142, v239, v239, v142 op_sel_hi:[1,1,0]
	v_cvt_f32_f16_sdwa v143, v168 dst_sel:DWORD dst_unused:UNUSED_PAD src0_sel:WORD_1
	v_add_f32_e32 v141, v141, v142
	v_add_f32_e32 v144, v140, v141
	v_cvt_f32_f16_e32 v142, v168
	v_cvt_f32_f16_sdwa v141, v169 dst_sel:DWORD dst_unused:UNUSED_PAD src0_sel:WORD_1
	v_cvt_f32_f16_e32 v140, v169
	v_cvt_f32_f16_sdwa v146, v170 dst_sel:DWORD dst_unused:UNUSED_PAD src0_sel:WORD_1
	v_cvt_f32_f16_e32 v147, v170
	v_cvt_f32_f16_sdwa v168, v171 dst_sel:DWORD dst_unused:UNUSED_PAD src0_sel:WORD_1
	v_cvt_f32_f16_e32 v169, v171
	v_sub_f32_e32 v140, v140, v224
	v_sub_f32_e32 v141, v141, v224
	v_sub_f32_e32 v142, v142, v224
	v_sub_f32_e32 v143, v143, v224
	v_pk_add_f32 v[132:133], v[132:133], v[200:201]
	v_pk_mul_f32 v[142:143], v[224:225], v[142:143] op_sel:[1,0]
	v_pk_mul_f32 v[140:141], v[224:225], v[140:141] op_sel:[1,0]
	v_pk_fma_f32 v[132:133], v[142:143], v[80:81], v[132:133]
	v_pk_fma_f32 v[134:135], v[140:141], v[82:83], v[134:135]
	v_sub_f32_e32 v140, v169, v224
	v_sub_f32_e32 v141, v168, v224
	v_sub_f32_e32 v142, v147, v224
	v_sub_f32_e32 v143, v146, v224
	v_pk_add_f32 v[130:131], v[130:131], v[192:193]
	v_pk_add_f32 v[128:129], v[128:129], v[194:195]
	v_pk_mul_f32 v[142:143], v[224:225], v[142:143] op_sel:[1,0]
	v_pk_mul_f32 v[140:141], v[224:225], v[140:141] op_sel:[1,0]
	v_lshlrev_b32_e32 v221, 2, v221
	v_pk_fma_f32 v[140:141], v[140:141], v[74:75], v[130:131]
	v_pk_fma_f32 v[130:131], v[142:143], v[72:73], v[128:129]
	v_cvt_f16_f32_e32 v142, v132
	v_cvt_f16_f32_e32 v143, v133
	v_cvt_pk_f16_f32 v128, v132, v133
	v_cvt_f16_f32_e32 v132, v134
	v_cvt_f16_f32_e32 v133, v135
	v_cvt_pk_f16_f32 v129, v134, v135
	v_cvt_f16_f32_e32 v134, v130
	v_cvt_f16_f32_e32 v135, v131
	v_cvt_f16_f32_e32 v146, v140
	v_cvt_f16_f32_e32 v147, v141
	v_cvt_pk_f16_f32 v130, v130, v131
	v_cvt_pk_f16_f32 v131, v140, v141
	ds_write_b128 v235, v[128:131] offset:64
	v_cvt_f32_f16_e32 v128, v142
	v_cvt_f32_f16_e32 v129, v143
	v_cvt_f32_f16_e32 v130, v132
	v_cvt_f32_f16_e32 v131, v133
	v_cvt_f32_f16_e32 v133, v134
	v_cvt_f32_f16_e32 v135, v135
	v_cvt_f32_f16_e32 v140, v146
	v_cvt_f32_f16_e32 v141, v147
	v_add_f32_e32 v128, v128, v129
	v_add_f32_e32 v130, v130, v131
	v_add_f32_e32 v128, v128, v130
	v_add_f32_e32 v130, v133, v135
	v_add_f32_e32 v133, v140, v141
	v_add_f32_e32 v130, v130, v133
	v_add_f32_e32 v128, v128, v130
	v_add_f32_e32 v140, v145, v128
	v_mul_f32_e32 v128, v129, v129
	v_mul_f32_e32 v129, v131, v131
	v_fma_mix_f32 v128, v142, v142, v128 op_sel_hi:[1,1,0]
	v_fma_mix_f32 v129, v132, v132, v129 op_sel_hi:[1,1,0]
	v_mul_f32_e32 v130, v141, v141
	v_add_f32_e32 v128, v128, v129
	v_mul_f32_e32 v129, v135, v135
	ds_bpermute_b32 v142, v221, v140
	v_fma_mix_f32 v129, v134, v134, v129 op_sel_hi:[1,1,0]
	v_fma_mix_f32 v130, v146, v146, v130 op_sel_hi:[1,1,0]
	v_lshlrev_b32_e32 v237, 2, v237
	v_add_f32_e32 v129, v129, v130
	v_add_f32_e32 v128, v128, v129
	v_add_f32_e32 v141, v144, v128
	s_waitcnt lgkmcnt(0)
	v_add_f32_e32 v140, v140, v142
	ds_bpermute_b32 v142, v221, v141
	v_cvt_f32_f16_sdwa v145, v164 dst_sel:DWORD dst_unused:UNUSED_PAD src0_sel:WORD_1
	v_cvt_f32_f16_e32 v144, v164
	v_cvt_f32_f16_sdwa v146, v166 dst_sel:DWORD dst_unused:UNUSED_PAD src0_sel:WORD_1
	v_cvt_f32_f16_e32 v147, v166
	s_waitcnt lgkmcnt(0)
	v_add_f32_e32 v141, v141, v142
	ds_bpermute_b32 v142, v237, v140
	v_cvt_f32_f16_sdwa v164, v167 dst_sel:DWORD dst_unused:UNUSED_PAD src0_sel:WORD_1
	v_sub_f32_e32 v144, v144, v222
	v_sub_f32_e32 v145, v145, v222
	v_pk_mul_f32 v[144:145], v[222:223], v[144:145] op_sel:[1,0]
	s_waitcnt lgkmcnt(0)
	v_add_f32_e32 v142, v140, v142
	ds_bpermute_b32 v140, v237, v141
	v_pk_fma_f32 v[124:125], v[144:145], v[92:93], v[124:125]
	v_sub_f32_e32 v144, v147, v222
	v_sub_f32_e32 v145, v146, v222
	v_pk_mul_f32 v[144:145], v[222:223], v[144:145] op_sel:[1,0]
	s_waitcnt lgkmcnt(0)
	v_add_f32_e32 v143, v141, v140
	v_cvt_f32_f16_sdwa v141, v165 dst_sel:DWORD dst_unused:UNUSED_PAD src0_sel:WORD_1
	v_cvt_f32_f16_e32 v140, v165
	v_cvt_f32_f16_e32 v165, v167
	ds_read_b128 v[132:135], v236
	ds_read_b128 v[128:131], v236 offset:1152
	v_sub_f32_e32 v141, v141, v222
	v_sub_f32_e32 v140, v140, v222
	v_pk_mul_f32 v[140:141], v[222:223], v[140:141] op_sel:[1,0]
	v_pk_add_f32 v[118:119], v[118:119], v[198:199]
	v_pk_fma_f32 v[126:127], v[140:141], v[94:95], v[126:127]
	v_sub_f32_e32 v140, v165, v222
	v_sub_f32_e32 v141, v164, v222
	v_pk_mul_f32 v[140:141], v[222:223], v[140:141] op_sel:[1,0]
	v_pk_add_f32 v[116:117], v[116:117], v[200:201]
	v_pk_fma_f32 v[140:141], v[140:141], v[90:91], v[122:123]
	v_pk_fma_f32 v[122:123], v[144:145], v[88:89], v[120:121]
	v_cvt_f16_f32_e32 v144, v124
	v_cvt_f16_f32_e32 v145, v125
	v_cvt_pk_f16_f32 v120, v124, v125
	v_cvt_f16_f32_e32 v124, v126
	v_cvt_f16_f32_e32 v125, v127
	v_cvt_pk_f16_f32 v121, v126, v127
	v_cvt_f16_f32_e32 v126, v122
	v_cvt_f16_f32_e32 v127, v123
	v_cvt_f16_f32_e32 v146, v140
	v_cvt_f16_f32_e32 v147, v141
	v_cvt_pk_f16_f32 v122, v122, v123
	v_cvt_pk_f16_f32 v123, v140, v141
	ds_write_b128 v235, v[120:123]
	v_cvt_f32_f16_e32 v120, v144
	v_cvt_f32_f16_e32 v121, v145
	v_cvt_f32_f16_e32 v122, v124
	v_cvt_f32_f16_e32 v123, v125
	v_cvt_f32_f16_e32 v125, v126
	v_cvt_f32_f16_e32 v127, v127
	v_cvt_f32_f16_e32 v140, v146
	v_cvt_f32_f16_e32 v141, v147
	v_add_f32_e32 v120, v120, v121
	v_add_f32_e32 v122, v122, v123
	v_add_f32_e32 v120, v120, v122
	v_add_f32_e32 v122, v125, v127
	v_add_f32_e32 v125, v140, v141
	v_add_f32_e32 v122, v122, v125
	v_add_f32_e32 v120, v120, v122
	v_add_f32_e32 v125, 0, v120
	v_mul_f32_e32 v120, v121, v121
	v_mul_f32_e32 v121, v123, v123
	v_fma_mix_f32 v120, v144, v144, v120 op_sel_hi:[1,1,0]
	v_fma_mix_f32 v121, v124, v124, v121 op_sel_hi:[1,1,0]
	v_mul_f32_e32 v122, v141, v141
	v_add_f32_e32 v120, v120, v121
	v_mul_f32_e32 v121, v127, v127
	v_fma_mix_f32 v121, v126, v126, v121 op_sel_hi:[1,1,0]
	v_fma_mix_f32 v122, v146, v146, v122 op_sel_hi:[1,1,0]
	v_cvt_f32_f16_sdwa v123, v160 dst_sel:DWORD dst_unused:UNUSED_PAD src0_sel:WORD_1
	v_add_f32_e32 v121, v121, v122
	v_add_f32_e32 v124, v120, v121
	v_cvt_f32_f16_e32 v122, v160
	v_cvt_f32_f16_sdwa v121, v161 dst_sel:DWORD dst_unused:UNUSED_PAD src0_sel:WORD_1
	v_cvt_f32_f16_e32 v120, v161
	v_cvt_f32_f16_sdwa v126, v162 dst_sel:DWORD dst_unused:UNUSED_PAD src0_sel:WORD_1
	v_cvt_f32_f16_e32 v127, v162
	v_cvt_f32_f16_sdwa v140, v163 dst_sel:DWORD dst_unused:UNUSED_PAD src0_sel:WORD_1
	v_cvt_f32_f16_e32 v141, v163
	v_sub_f32_e32 v120, v120, v222
	v_sub_f32_e32 v121, v121, v222
	v_sub_f32_e32 v122, v122, v222
	v_sub_f32_e32 v123, v123, v222
	v_pk_mul_f32 v[122:123], v[222:223], v[122:123] op_sel:[1,0]
	v_pk_mul_f32 v[120:121], v[222:223], v[120:121] op_sel:[1,0]
	v_pk_fma_f32 v[116:117], v[122:123], v[80:81], v[116:117]
	v_pk_fma_f32 v[118:119], v[120:121], v[82:83], v[118:119]
	v_sub_f32_e32 v120, v141, v222
	v_sub_f32_e32 v121, v140, v222
	v_sub_f32_e32 v122, v127, v222
	v_sub_f32_e32 v123, v126, v222
	v_pk_add_f32 v[114:115], v[114:115], v[192:193]
	v_pk_add_f32 v[112:113], v[112:113], v[194:195]
	v_pk_mul_f32 v[122:123], v[222:223], v[122:123] op_sel:[1,0]
	v_pk_mul_f32 v[120:121], v[222:223], v[120:121] op_sel:[1,0]
	s_ashr_i32 s39, s38, 31
	v_pk_fma_f32 v[120:121], v[120:121], v[74:75], v[114:115]
	v_pk_fma_f32 v[114:115], v[122:123], v[72:73], v[112:113]
	v_cvt_f16_f32_e32 v122, v116
	v_cvt_f16_f32_e32 v123, v117
	v_cvt_pk_f16_f32 v112, v116, v117
	v_cvt_f16_f32_e32 v116, v118
	v_cvt_f16_f32_e32 v117, v119
	v_cvt_pk_f16_f32 v113, v118, v119
	v_cvt_f16_f32_e32 v118, v114
	v_cvt_f16_f32_e32 v119, v115
	v_cvt_f16_f32_e32 v126, v120
	v_cvt_f16_f32_e32 v127, v121
	v_cvt_pk_f16_f32 v114, v114, v115
	v_cvt_pk_f16_f32 v115, v120, v121
	ds_write_b128 v235, v[112:115] offset:64
	v_cvt_f32_f16_e32 v112, v122
	v_cvt_f32_f16_e32 v113, v123
	v_cvt_f32_f16_e32 v114, v116
	v_cvt_f32_f16_e32 v115, v117
	v_cvt_f32_f16_e32 v117, v118
	v_cvt_f32_f16_e32 v119, v119
	v_cvt_f32_f16_e32 v120, v126
	v_cvt_f32_f16_e32 v121, v127
	v_add_f32_e32 v112, v112, v113
	v_add_f32_e32 v114, v114, v115
	v_add_f32_e32 v112, v112, v114
	v_add_f32_e32 v114, v117, v119
	v_add_f32_e32 v117, v120, v121
	v_add_f32_e32 v114, v114, v117
	v_add_f32_e32 v112, v112, v114
	v_mul_f32_e32 v113, v113, v113
	v_mul_f32_e32 v114, v115, v115
	v_fma_mix_f32 v113, v122, v122, v113 op_sel_hi:[1,1,0]
	v_fma_mix_f32 v114, v116, v116, v114 op_sel_hi:[1,1,0]
	v_mul_f32_e32 v115, v121, v121
	v_add_f32_e32 v113, v113, v114
	v_mul_f32_e32 v114, v119, v119
	v_fma_mix_f32 v114, v118, v118, v114 op_sel_hi:[1,1,0]
	v_fma_mix_f32 v115, v126, v126, v115 op_sel_hi:[1,1,0]
	v_add_f32_e32 v112, v125, v112
	v_add_f32_e32 v114, v114, v115
	v_add_f32_e32 v113, v113, v114
	ds_bpermute_b32 v114, v221, v112
	v_add_f32_e32 v113, v124, v113
	ds_read_b128 v[160:163], v236
	ds_read_b128 v[164:167], v236 offset:1152
	s_waitcnt lgkmcnt(2)
	v_add_f32_e32 v112, v112, v114
	ds_bpermute_b32 v114, v221, v113
	s_waitcnt lgkmcnt(0)
	v_add_f32_e32 v113, v113, v114
	ds_bpermute_b32 v114, v237, v112
	s_waitcnt lgkmcnt(0)
	v_add_f32_e32 v146, v112, v114
	ds_bpermute_b32 v112, v237, v113
	s_waitcnt lgkmcnt(0)
	v_add_f32_e32 v147, v113, v112
	v_mov_b64_e32 v[112:113], s[28:29]
	v_mad_i64_i32 v[112:113], s[40:41], v220, s73, v[112:113]
	v_lshl_add_u64 v[140:141], s[38:39], 3, v[112:113]
	v_add_co_u32_e32 v112, vcc, s74, v214
	v_lshl_or_b32 v144, v238, 1, v230
	s_nop 0
	v_addc_co_u32_e32 v113, vcc, 0, v215, vcc
	global_load_dwordx4 v[124:127], v[112:113], off nt
	global_load_dwordx4 v[120:123], v[112:113], off offset:64 nt
	v_add_co_u32_e32 v112, vcc, s75, v214
	v_lshl_add_u64 v[140:141], v[140:141], 0, s[34:35]
	s_nop 0
	v_addc_co_u32_e32 v113, vcc, 0, v215, vcc
	global_load_dwordx4 v[116:119], v[112:113], off nt
	s_nop 0
	global_load_dwordx4 v[112:115], v[112:113], off offset:64 nt
	s_nop 0
	buffer_store_dwordx4 v[132:135], v144, s[24:27], 0 offen nt
	s_nop 1
	v_add_u32_e32 v132, 0x3000, v144
	buffer_store_dwordx4 v[128:131], v132, s[24:27], 0 offen nt
	global_store_dwordx2 v[140:141], v[142:143], off
	s_nop 0
	v_add_u32_e32 v128, 0x6000, v144
	buffer_store_dwordx4 v[160:163], v128, s[24:27], 0 offen nt
	v_add_u32_e32 v128, 0x9000, v144
	buffer_store_dwordx4 v[164:167], v128, s[24:27], 0 offen nt
	global_store_dwordx2 v[140:141], v[146:147], off offset:1536
	v_cvt_f32_f16_sdwa v131, v156 dst_sel:DWORD dst_unused:UNUSED_PAD src0_sel:WORD_1
	v_cvt_f32_f16_e32 v130, v156
	v_cvt_f32_f16_sdwa v129, v157 dst_sel:DWORD dst_unused:UNUSED_PAD src0_sel:WORD_1
	v_cvt_f32_f16_e32 v128, v157
	v_cvt_f32_f16_sdwa v132, v158 dst_sel:DWORD dst_unused:UNUSED_PAD src0_sel:WORD_1
	v_cvt_f32_f16_e32 v133, v158
	v_cvt_f32_f16_sdwa v134, v159 dst_sel:DWORD dst_unused:UNUSED_PAD src0_sel:WORD_1
	v_cvt_f32_f16_e32 v135, v159
	v_sub_f32_e32 v128, v128, v218
	v_sub_f32_e32 v129, v129, v218
	v_sub_f32_e32 v130, v130, v218
	v_sub_f32_e32 v131, v131, v218
	v_pk_add_f32 v[110:111], v[110:111], v[206:207]
	v_pk_add_f32 v[108:109], v[108:109], v[208:209]
	v_pk_mul_f32 v[130:131], v[218:219], v[130:131] op_sel:[1,0]
	v_pk_mul_f32 v[128:129], v[218:219], v[128:129] op_sel:[1,0]
	v_pk_fma_f32 v[108:109], v[130:131], v[92:93], v[108:109]
	v_pk_fma_f32 v[110:111], v[128:129], v[94:95], v[110:111]
	v_sub_f32_e32 v128, v135, v218
	v_sub_f32_e32 v129, v134, v218
	v_sub_f32_e32 v130, v133, v218
	v_sub_f32_e32 v131, v132, v218
	v_pk_add_f32 v[106:107], v[106:107], v[202:203]
	v_pk_add_f32 v[104:105], v[104:105], v[204:205]
	v_pk_mul_f32 v[130:131], v[218:219], v[130:131] op_sel:[1,0]
	v_pk_mul_f32 v[128:129], v[218:219], v[128:129] op_sel:[1,0]
	v_pk_add_f32 v[102:103], v[102:103], v[198:199]
	v_pk_fma_f32 v[128:129], v[128:129], v[90:91], v[106:107]
	v_pk_fma_f32 v[106:107], v[130:131], v[88:89], v[104:105]
	v_cvt_f16_f32_e32 v130, v108
	v_cvt_f16_f32_e32 v131, v109
	v_cvt_pk_f16_f32 v104, v108, v109
	v_cvt_f16_f32_e32 v108, v110
	v_cvt_f16_f32_e32 v109, v111
	v_cvt_pk_f16_f32 v105, v110, v111
	v_cvt_f16_f32_e32 v110, v106
	v_cvt_f16_f32_e32 v111, v107
	v_cvt_f16_f32_e32 v132, v128
	v_cvt_f16_f32_e32 v133, v129
	v_cvt_pk_f16_f32 v106, v106, v107
	v_cvt_pk_f16_f32 v107, v128, v129
	ds_write_b128 v235, v[104:107]
	v_cvt_f32_f16_e32 v104, v130
	v_cvt_f32_f16_e32 v105, v131
	v_cvt_f32_f16_e32 v106, v108
	v_cvt_f32_f16_e32 v107, v109
	v_cvt_f32_f16_e32 v109, v110
	v_cvt_f32_f16_e32 v111, v111
	v_cvt_f32_f16_e32 v128, v132
	v_cvt_f32_f16_e32 v129, v133
	v_add_f32_e32 v104, v104, v105
	v_add_f32_e32 v106, v106, v107
	v_add_f32_e32 v104, v104, v106
	v_add_f32_e32 v106, v109, v111
	v_add_f32_e32 v109, v128, v129
	v_add_f32_e32 v106, v106, v109
	v_add_f32_e32 v104, v104, v106
	v_add_f32_e32 v109, 0, v104
	v_mul_f32_e32 v104, v105, v105
	v_mul_f32_e32 v105, v107, v107
	v_fma_mix_f32 v104, v130, v130, v104 op_sel_hi:[1,1,0]
	v_fma_mix_f32 v105, v108, v108, v105 op_sel_hi:[1,1,0]
	v_mul_f32_e32 v106, v129, v129
	v_add_f32_e32 v104, v104, v105
	v_mul_f32_e32 v105, v111, v111
	v_fma_mix_f32 v105, v110, v110, v105 op_sel_hi:[1,1,0]
	v_fma_mix_f32 v106, v132, v132, v106 op_sel_hi:[1,1,0]
	v_cvt_f32_f16_sdwa v107, v152 dst_sel:DWORD dst_unused:UNUSED_PAD src0_sel:WORD_1
	v_add_f32_e32 v105, v105, v106
	v_add_f32_e32 v108, v104, v105
	v_cvt_f32_f16_e32 v106, v152
	v_cvt_f32_f16_sdwa v105, v153 dst_sel:DWORD dst_unused:UNUSED_PAD src0_sel:WORD_1
	v_cvt_f32_f16_e32 v104, v153
	v_cvt_f32_f16_sdwa v110, v154 dst_sel:DWORD dst_unused:UNUSED_PAD src0_sel:WORD_1
	v_cvt_f32_f16_e32 v111, v154
	v_cvt_f32_f16_sdwa v128, v155 dst_sel:DWORD dst_unused:UNUSED_PAD src0_sel:WORD_1
	v_cvt_f32_f16_e32 v129, v155
	v_sub_f32_e32 v104, v104, v218
	v_sub_f32_e32 v105, v105, v218
	v_sub_f32_e32 v106, v106, v218
	v_sub_f32_e32 v107, v107, v218
	v_pk_add_f32 v[100:101], v[100:101], v[200:201]
	v_pk_mul_f32 v[106:107], v[218:219], v[106:107] op_sel:[1,0]
	v_pk_mul_f32 v[104:105], v[218:219], v[104:105] op_sel:[1,0]
	v_pk_fma_f32 v[100:101], v[106:107], v[80:81], v[100:101]
	v_pk_fma_f32 v[102:103], v[104:105], v[82:83], v[102:103]
	v_sub_f32_e32 v104, v129, v218
	v_sub_f32_e32 v105, v128, v218
	v_sub_f32_e32 v106, v111, v218
	v_sub_f32_e32 v107, v110, v218
	v_pk_add_f32 v[98:99], v[98:99], v[192:193]
	v_pk_add_f32 v[96:97], v[96:97], v[194:195]
	v_pk_mul_f32 v[106:107], v[218:219], v[106:107] op_sel:[1,0]
	v_pk_mul_f32 v[104:105], v[218:219], v[104:105] op_sel:[1,0]
	v_pk_add_f32 v[86:87], v[86:87], v[206:207]
	v_pk_fma_f32 v[104:105], v[104:105], v[74:75], v[98:99]
	v_pk_fma_f32 v[98:99], v[106:107], v[72:73], v[96:97]
	v_cvt_f16_f32_e32 v106, v100
	v_cvt_f16_f32_e32 v107, v101
	v_cvt_pk_f16_f32 v96, v100, v101
	v_cvt_f16_f32_e32 v100, v102
	v_cvt_f16_f32_e32 v101, v103
	v_cvt_pk_f16_f32 v97, v102, v103
	v_cvt_f16_f32_e32 v103, v99
	v_cvt_f16_f32_e32 v111, v105
	v_cvt_f16_f32_e32 v102, v98
	v_cvt_f16_f32_e32 v110, v104
	v_cvt_pk_f16_f32 v98, v98, v99
	v_cvt_pk_f16_f32 v99, v104, v105
	v_cvt_f32_f16_e32 v105, v107
	v_cvt_f32_f16_e32 v107, v100
	v_cvt_f32_f16_e32 v101, v101
	v_cvt_f32_f16_e32 v103, v103
	v_cvt_f32_f16_e32 v104, v106
	v_cvt_f32_f16_e32 v111, v111
	v_cvt_f32_f16_e32 v128, v102
	v_cvt_f32_f16_e32 v129, v110
	v_add_f32_e32 v107, v107, v101
	v_mul_f32_e32 v101, v101, v101
	v_fma_mix_f32 v100, v100, v100, v101 op_sel_hi:[1,1,0]
	v_mul_f32_e32 v101, v103, v103
	v_add_f32_e32 v104, v104, v105
	v_mul_f32_e32 v105, v105, v105
	v_fma_mix_f32 v101, v102, v102, v101 op_sel_hi:[1,1,0]
	v_mul_f32_e32 v102, v111, v111
	v_add_f32_e32 v104, v104, v107
	v_add_f32_e32 v107, v128, v103
	v_add_f32_e32 v128, v129, v111
	v_fma_mix_f32 v105, v106, v106, v105 op_sel_hi:[1,1,0]
	v_fma_mix_f32 v102, v110, v110, v102 op_sel_hi:[1,1,0]
	v_add_f32_e32 v107, v107, v128
	v_add_f32_e32 v100, v105, v100
	v_add_f32_e32 v101, v101, v102
	v_add_f32_e32 v104, v104, v107
	v_add_f32_e32 v100, v100, v101
	v_add_f32_e32 v104, v109, v104
	v_add_f32_e32 v105, v108, v100
	ds_bpermute_b32 v106, v221, v104
	ds_bpermute_b32 v107, v221, v105
	v_cvt_f32_f16_sdwa v108, v150 dst_sel:DWORD dst_unused:UNUSED_PAD src0_sel:WORD_1
	v_cvt_f32_f16_e32 v109, v150
	v_cvt_f32_f16_sdwa v110, v151 dst_sel:DWORD dst_unused:UNUSED_PAD src0_sel:WORD_1
	s_waitcnt lgkmcnt(1)
	v_add_f32_e32 v128, v104, v106
	s_waitcnt lgkmcnt(0)
	v_add_f32_e32 v129, v105, v107
	v_cvt_f32_f16_sdwa v107, v148 dst_sel:DWORD dst_unused:UNUSED_PAD src0_sel:WORD_1
	v_cvt_f32_f16_e32 v106, v148
	v_cvt_f32_f16_sdwa v105, v149 dst_sel:DWORD dst_unused:UNUSED_PAD src0_sel:WORD_1
	v_cvt_f32_f16_e32 v104, v149
	v_cvt_f32_f16_e32 v111, v151
	v_sub_f32_e32 v106, v106, v216
	v_sub_f32_e32 v105, v105, v216
	v_sub_f32_e32 v104, v104, v216
	v_sub_f32_e32 v107, v107, v216
	v_pk_add_f32 v[84:85], v[84:85], v[208:209]
	v_pk_mul_f32 v[106:107], v[216:217], v[106:107] op_sel:[1,0]
	v_pk_mul_f32 v[104:105], v[216:217], v[104:105] op_sel:[1,0]
	v_pk_fma_f32 v[84:85], v[106:107], v[92:93], v[84:85]
	v_pk_fma_f32 v[86:87], v[104:105], v[94:95], v[86:87]
	v_sub_f32_e32 v104, v111, v216
	v_sub_f32_e32 v105, v110, v216
	v_sub_f32_e32 v106, v109, v216
	v_sub_f32_e32 v107, v108, v216
	v_pk_add_f32 v[78:79], v[78:79], v[202:203]
	v_pk_add_f32 v[76:77], v[76:77], v[204:205]
	v_pk_mul_f32 v[106:107], v[216:217], v[106:107] op_sel:[1,0]
	v_pk_mul_f32 v[104:105], v[216:217], v[104:105] op_sel:[1,0]
	ds_write_b128 v235, v[96:99] offset:64
	v_pk_fma_f32 v[104:105], v[104:105], v[90:91], v[78:79]
	v_pk_fma_f32 v[78:79], v[106:107], v[88:89], v[76:77]
	v_cvt_f16_f32_e32 v106, v84
	v_cvt_f16_f32_e32 v107, v85
	v_cvt_pk_f16_f32 v76, v84, v85
	v_cvt_f16_f32_e32 v84, v86
	v_cvt_f16_f32_e32 v85, v87
	v_cvt_pk_f16_f32 v77, v86, v87
	v_cvt_f16_f32_e32 v86, v78
	v_cvt_f16_f32_e32 v87, v79
	v_cvt_f16_f32_e32 v108, v104
	v_cvt_f16_f32_e32 v109, v105
	v_cvt_pk_f16_f32 v78, v78, v79
	v_cvt_pk_f16_f32 v79, v104, v105
	ds_read_b128 v[96:99], v236
	ds_read_b128 v[100:103], v236 offset:1152
	ds_write_b128 v235, v[76:79]
	v_cvt_f32_f16_e32 v76, v106
	v_cvt_f32_f16_e32 v77, v107
	v_cvt_f32_f16_e32 v78, v84
	v_cvt_f32_f16_e32 v79, v85
	v_cvt_f32_f16_e32 v85, v86
	v_cvt_f32_f16_e32 v87, v87
	v_cvt_f32_f16_e32 v104, v108
	v_cvt_f32_f16_e32 v105, v109
	v_add_f32_e32 v76, v76, v77
	v_add_f32_e32 v78, v78, v79
	v_add_f32_e32 v76, v76, v78
	v_add_f32_e32 v78, v85, v87
	v_add_f32_e32 v85, v104, v105
	v_add_f32_e32 v78, v78, v85
	v_add_f32_e32 v76, v76, v78
	v_add_f32_e32 v85, 0, v76
	v_mul_f32_e32 v76, v77, v77
	v_mul_f32_e32 v77, v79, v79
	v_fma_mix_f32 v76, v106, v106, v76 op_sel_hi:[1,1,0]
	v_fma_mix_f32 v77, v84, v84, v77 op_sel_hi:[1,1,0]
	v_mul_f32_e32 v78, v105, v105
	v_add_f32_e32 v76, v76, v77
	v_mul_f32_e32 v77, v87, v87
	v_fma_mix_f32 v77, v86, v86, v77 op_sel_hi:[1,1,0]
	v_fma_mix_f32 v78, v108, v108, v78 op_sel_hi:[1,1,0]
	v_cvt_f32_f16_sdwa v79, v136 dst_sel:DWORD dst_unused:UNUSED_PAD src0_sel:WORD_1
	v_add_f32_e32 v77, v77, v78
	v_add_f32_e32 v84, v76, v77
	v_cvt_f32_f16_e32 v78, v136
	v_cvt_f32_f16_sdwa v77, v137 dst_sel:DWORD dst_unused:UNUSED_PAD src0_sel:WORD_1
	v_cvt_f32_f16_e32 v76, v137
	v_cvt_f32_f16_sdwa v86, v138 dst_sel:DWORD dst_unused:UNUSED_PAD src0_sel:WORD_1
	v_cvt_f32_f16_e32 v87, v138
	v_cvt_f32_f16_sdwa v104, v139 dst_sel:DWORD dst_unused:UNUSED_PAD src0_sel:WORD_1
	v_cvt_f32_f16_e32 v105, v139
	v_sub_f32_e32 v76, v76, v216
	v_sub_f32_e32 v77, v77, v216
	v_sub_f32_e32 v78, v78, v216
	v_sub_f32_e32 v79, v79, v216
	v_pk_add_f32 v[70:71], v[70:71], v[198:199]
	v_pk_add_f32 v[68:69], v[68:69], v[200:201]
	v_pk_mul_f32 v[78:79], v[216:217], v[78:79] op_sel:[1,0]
	v_pk_mul_f32 v[76:77], v[216:217], v[76:77] op_sel:[1,0]
	v_pk_fma_f32 v[68:69], v[78:79], v[80:81], v[68:69]
	v_pk_fma_f32 v[70:71], v[76:77], v[82:83], v[70:71]
	v_sub_f32_e32 v76, v105, v216
	v_sub_f32_e32 v77, v104, v216
	v_sub_f32_e32 v78, v87, v216
	v_sub_f32_e32 v79, v86, v216
	v_pk_add_f32 v[66:67], v[66:67], v[192:193]
	v_pk_add_f32 v[64:65], v[64:65], v[194:195]
	v_pk_mul_f32 v[78:79], v[216:217], v[78:79] op_sel:[1,0]
	v_pk_mul_f32 v[76:77], v[216:217], v[76:77] op_sel:[1,0]
	ds_bpermute_b32 v130, v237, v128
	v_pk_fma_f32 v[76:77], v[76:77], v[74:75], v[66:67]
	v_pk_fma_f32 v[66:67], v[78:79], v[72:73], v[64:65]
	v_cvt_f16_f32_e32 v78, v68
	v_cvt_f16_f32_e32 v79, v69
	v_cvt_pk_f16_f32 v64, v68, v69
	v_cvt_f16_f32_e32 v68, v70
	v_cvt_f16_f32_e32 v69, v71
	v_cvt_pk_f16_f32 v65, v70, v71
	v_cvt_f16_f32_e32 v71, v67
	v_cvt_f16_f32_e32 v87, v77
	v_cvt_f16_f32_e32 v70, v66
	v_cvt_f16_f32_e32 v86, v76
	v_cvt_f32_f16_e32 v105, v68
	v_cvt_f32_f16_e32 v69, v69
	v_cvt_f32_f16_e32 v71, v71
	v_cvt_f32_f16_e32 v104, v78
	v_cvt_f32_f16_e32 v79, v79
	v_cvt_f32_f16_e32 v87, v87
	v_cvt_f32_f16_e32 v106, v70
	v_cvt_f32_f16_e32 v107, v86
	v_add_f32_e32 v105, v105, v69
	v_mul_f32_e32 v69, v69, v69
	v_fma_mix_f32 v68, v68, v68, v69 op_sel_hi:[1,1,0]
	v_mul_f32_e32 v69, v71, v71
	v_add_f32_e32 v104, v104, v79
	v_mul_f32_e32 v79, v79, v79
	v_fma_mix_f32 v69, v70, v70, v69 op_sel_hi:[1,1,0]
	v_mul_f32_e32 v70, v87, v87
	v_add_f32_e32 v104, v104, v105
	v_add_f32_e32 v105, v106, v71
	v_add_f32_e32 v106, v107, v87
	v_fma_mix_f32 v78, v78, v78, v79 op_sel_hi:[1,1,0]
	v_fma_mix_f32 v70, v86, v86, v70 op_sel_hi:[1,1,0]
	v_add_f32_e32 v105, v105, v106
	v_add_f32_e32 v68, v78, v68
	v_add_f32_e32 v69, v69, v70
	v_add_f32_e32 v104, v104, v105
	v_add_f32_e32 v68, v68, v69
	v_add_f32_e32 v85, v85, v104
	v_add_f32_e32 v68, v84, v68
	ds_bpermute_b32 v69, v221, v85
	ds_bpermute_b32 v70, v221, v68
	v_cvt_pk_f16_f32 v66, v66, v67
	v_cvt_pk_f16_f32 v67, v76, v77
	ds_write_b128 v235, v[64:67] offset:64
	s_waitcnt lgkmcnt(2)
	v_add_f32_e32 v64, v85, v69
	s_waitcnt lgkmcnt(1)
	v_add_f32_e32 v65, v68, v70
	ds_bpermute_b32 v131, v237, v129
	ds_bpermute_b32 v66, v237, v64
	ds_bpermute_b32 v67, v237, v65
	ds_read_b128 v[104:107], v236
	ds_read_b128 v[108:111], v236 offset:1152
	v_add_f32_e32 v128, v128, v130
	s_waitcnt lgkmcnt(4)
	v_add_f32_e32 v129, v129, v131
	s_waitcnt lgkmcnt(3)
	v_add_f32_e32 v130, v64, v66
	s_waitcnt lgkmcnt(2)
	v_add_f32_e32 v131, v65, v67
	v_add_co_u32_e32 v64, vcc, s77, v214
	s_nop 1
	v_addc_co_u32_e32 v65, vcc, 0, v215, vcc
	global_load_dwordx4 v[84:87], v[64:65], off nt
	global_load_dwordx4 v[76:79], v[64:65], off offset:64 nt
	v_add_co_u32_e32 v64, vcc, s78, v214
	s_nop 1
	v_addc_co_u32_e32 v65, vcc, 0, v215, vcc
	global_load_dwordx4 v[68:71], v[64:65], off nt
	s_nop 0
	global_load_dwordx4 v[64:67], v[64:65], off offset:64 nt
	v_add_u32_e32 v132, 0xc000, v144
	buffer_store_dwordx4 v[96:99], v132, s[24:27], 0 offen nt
	s_nop 1
	v_add_u32_e32 v96, 0xf000, v144
	buffer_store_dwordx4 v[100:103], v96, s[24:27], 0 offen nt
	v_add_u32_e32 v96, 0x12000, v144
	global_store_dwordx2 v[140:141], v[128:129], off offset:3072
	s_waitcnt lgkmcnt(1)
	buffer_store_dwordx4 v[104:107], v96, s[24:27], 0 offen nt
	v_add_u32_e32 v96, 0x15000, v144
	s_waitcnt lgkmcnt(0)
	buffer_store_dwordx4 v[108:111], v96, s[24:27], 0 offen nt
	v_add_co_u32_e32 v96, vcc, s79, v140
	s_nop 1
	v_addc_co_u32_e32 v97, vcc, 0, v141, vcc
	global_store_dwordx2 v[96:97], v[130:131], off offset:512
	s_waitcnt vmcnt(19)
	v_cvt_f32_f16_sdwa v99, v124 dst_sel:DWORD dst_unused:UNUSED_PAD src0_sel:WORD_1
	v_cvt_f32_f16_e32 v98, v124
	v_cvt_f32_f16_sdwa v97, v125 dst_sel:DWORD dst_unused:UNUSED_PAD src0_sel:WORD_1
	v_cvt_f32_f16_e32 v96, v125
	v_cvt_f32_f16_sdwa v100, v126 dst_sel:DWORD dst_unused:UNUSED_PAD src0_sel:WORD_1
	v_cvt_f32_f16_e32 v101, v126
	v_cvt_f32_f16_sdwa v102, v127 dst_sel:DWORD dst_unused:UNUSED_PAD src0_sel:WORD_1
	v_cvt_f32_f16_e32 v103, v127
	v_sub_f32_e32 v96, v96, v212
	v_sub_f32_e32 v97, v97, v212
	v_sub_f32_e32 v98, v98, v212
	v_sub_f32_e32 v99, v99, v212
	v_pk_add_f32 v[62:63], v[62:63], v[206:207]
	v_pk_add_f32 v[60:61], v[60:61], v[208:209]
	v_pk_mul_f32 v[98:99], v[212:213], v[98:99] op_sel:[1,0]
	v_pk_mul_f32 v[96:97], v[212:213], v[96:97] op_sel:[1,0]
	v_pk_fma_f32 v[60:61], v[92:93], v[98:99], v[60:61]
	v_pk_fma_f32 v[62:63], v[94:95], v[96:97], v[62:63]
	v_sub_f32_e32 v96, v103, v212
	v_sub_f32_e32 v97, v102, v212
	v_sub_f32_e32 v98, v101, v212
	v_sub_f32_e32 v99, v100, v212
	v_pk_add_f32 v[58:59], v[58:59], v[202:203]
	v_pk_add_f32 v[56:57], v[56:57], v[204:205]
	v_pk_mul_f32 v[98:99], v[212:213], v[98:99] op_sel:[1,0]
	v_pk_mul_f32 v[96:97], v[212:213], v[96:97] op_sel:[1,0]
	v_pk_add_f32 v[54:55], v[54:55], v[198:199]
	v_pk_fma_f32 v[96:97], v[90:91], v[96:97], v[58:59]
	v_pk_fma_f32 v[58:59], v[88:89], v[98:99], v[56:57]
	v_cvt_f16_f32_e32 v98, v60
	v_cvt_f16_f32_e32 v99, v61
	v_cvt_pk_f16_f32 v56, v60, v61
	v_cvt_f16_f32_e32 v60, v62
	v_cvt_f16_f32_e32 v61, v63
	v_cvt_pk_f16_f32 v57, v62, v63
	v_cvt_f16_f32_e32 v62, v58
	v_cvt_f16_f32_e32 v63, v59
	v_cvt_f16_f32_e32 v100, v96
	v_cvt_f16_f32_e32 v101, v97
	v_cvt_pk_f16_f32 v58, v58, v59
	v_cvt_pk_f16_f32 v59, v96, v97
	ds_write_b128 v235, v[56:59]
	v_cvt_f32_f16_e32 v56, v98
	v_cvt_f32_f16_e32 v57, v99
	v_cvt_f32_f16_e32 v58, v60
	v_cvt_f32_f16_e32 v59, v61
	v_cvt_f32_f16_e32 v61, v62
	v_cvt_f32_f16_e32 v63, v63
	v_cvt_f32_f16_e32 v96, v100
	v_cvt_f32_f16_e32 v97, v101
	v_add_f32_e32 v56, v56, v57
	v_add_f32_e32 v58, v58, v59
	v_add_f32_e32 v56, v56, v58
	v_add_f32_e32 v58, v61, v63
	v_add_f32_e32 v61, v96, v97
	v_add_f32_e32 v58, v58, v61
	v_add_f32_e32 v56, v56, v58
	v_add_f32_e32 v61, 0, v56
	v_mul_f32_e32 v56, v57, v57
	v_mul_f32_e32 v57, v59, v59
	v_fma_mix_f32 v56, v98, v98, v56 op_sel_hi:[1,1,0]
	v_fma_mix_f32 v57, v60, v60, v57 op_sel_hi:[1,1,0]
	v_mul_f32_e32 v58, v97, v97
	v_add_f32_e32 v56, v56, v57
	v_mul_f32_e32 v57, v63, v63
	v_fma_mix_f32 v57, v62, v62, v57 op_sel_hi:[1,1,0]
	v_fma_mix_f32 v58, v100, v100, v58 op_sel_hi:[1,1,0]
	s_waitcnt vmcnt(18)
	v_cvt_f32_f16_sdwa v59, v120 dst_sel:DWORD dst_unused:UNUSED_PAD src0_sel:WORD_1
	v_add_f32_e32 v57, v57, v58
	v_add_f32_e32 v60, v56, v57
	v_cvt_f32_f16_e32 v58, v120
	v_cvt_f32_f16_sdwa v57, v121 dst_sel:DWORD dst_unused:UNUSED_PAD src0_sel:WORD_1
	v_cvt_f32_f16_e32 v56, v121
	v_cvt_f32_f16_sdwa v62, v122 dst_sel:DWORD dst_unused:UNUSED_PAD src0_sel:WORD_1
	v_cvt_f32_f16_e32 v63, v122
	v_cvt_f32_f16_sdwa v96, v123 dst_sel:DWORD dst_unused:UNUSED_PAD src0_sel:WORD_1
	v_cvt_f32_f16_e32 v97, v123
	v_sub_f32_e32 v56, v56, v212
	v_sub_f32_e32 v57, v57, v212
	v_sub_f32_e32 v58, v58, v212
	v_sub_f32_e32 v59, v59, v212
	v_pk_add_f32 v[52:53], v[52:53], v[200:201]
	v_pk_mul_f32 v[58:59], v[212:213], v[58:59] op_sel:[1,0]
	v_pk_mul_f32 v[56:57], v[212:213], v[56:57] op_sel:[1,0]
	v_pk_fma_f32 v[52:53], v[80:81], v[58:59], v[52:53]
	v_pk_fma_f32 v[54:55], v[82:83], v[56:57], v[54:55]
	v_sub_f32_e32 v56, v97, v212
	v_sub_f32_e32 v57, v96, v212
	v_sub_f32_e32 v58, v63, v212
	v_sub_f32_e32 v59, v62, v212
	v_pk_add_f32 v[50:51], v[50:51], v[192:193]
	v_pk_add_f32 v[48:49], v[48:49], v[194:195]
	v_pk_mul_f32 v[58:59], v[212:213], v[58:59] op_sel:[1,0]
	v_pk_mul_f32 v[56:57], v[212:213], v[56:57] op_sel:[1,0]
	s_waitcnt vmcnt(17)
	v_cvt_f32_f16_sdwa v98, v119 dst_sel:DWORD dst_unused:UNUSED_PAD src0_sel:WORD_1
	v_pk_fma_f32 v[56:57], v[74:75], v[56:57], v[50:51]
	v_pk_fma_f32 v[50:51], v[72:73], v[58:59], v[48:49]
	v_cvt_f16_f32_e32 v58, v52
	v_cvt_f16_f32_e32 v59, v53
	v_cvt_pk_f16_f32 v48, v52, v53
	v_cvt_f16_f32_e32 v52, v54
	v_cvt_f16_f32_e32 v53, v55
	v_cvt_pk_f16_f32 v49, v54, v55
	v_cvt_f16_f32_e32 v55, v51
	v_cvt_f16_f32_e32 v63, v57
	v_cvt_f16_f32_e32 v54, v50
	v_cvt_f16_f32_e32 v62, v56
	v_cvt_pk_f16_f32 v50, v50, v51
	v_cvt_pk_f16_f32 v51, v56, v57
	v_cvt_f32_f16_e32 v57, v59
	v_cvt_f32_f16_e32 v59, v52
	v_cvt_f32_f16_e32 v53, v53
	v_cvt_f32_f16_e32 v55, v55
	v_cvt_f32_f16_e32 v56, v58
	v_cvt_f32_f16_e32 v63, v63
	v_cvt_f32_f16_e32 v96, v54
	v_cvt_f32_f16_e32 v97, v62
	v_add_f32_e32 v59, v59, v53
	v_mul_f32_e32 v53, v53, v53
	v_fma_mix_f32 v52, v52, v52, v53 op_sel_hi:[1,1,0]
	v_mul_f32_e32 v53, v55, v55
	v_add_f32_e32 v56, v56, v57
	v_mul_f32_e32 v57, v57, v57
	v_fma_mix_f32 v53, v54, v54, v53 op_sel_hi:[1,1,0]
	v_mul_f32_e32 v54, v63, v63
	v_add_f32_e32 v56, v56, v59
	v_add_f32_e32 v59, v96, v55
	v_add_f32_e32 v96, v97, v63
	v_fma_mix_f32 v57, v58, v58, v57 op_sel_hi:[1,1,0]
	v_fma_mix_f32 v54, v62, v62, v54 op_sel_hi:[1,1,0]
	v_add_f32_e32 v59, v59, v96
	v_add_f32_e32 v52, v57, v52
	v_add_f32_e32 v53, v53, v54
	v_add_f32_e32 v56, v56, v59
	v_add_f32_e32 v52, v52, v53
	v_add_f32_e32 v56, v61, v56
	v_add_f32_e32 v57, v60, v52
	ds_bpermute_b32 v58, v221, v56
	ds_bpermute_b32 v59, v221, v57
	v_cvt_f32_f16_sdwa v96, v118 dst_sel:DWORD dst_unused:UNUSED_PAD src0_sel:WORD_1
	v_cvt_f32_f16_e32 v97, v118
	v_cvt_f32_f16_e32 v99, v119
	s_waitcnt lgkmcnt(1)
	v_add_f32_e32 v60, v56, v58
	s_waitcnt lgkmcnt(0)
	v_add_f32_e32 v61, v57, v59
	v_cvt_f32_f16_sdwa v59, v116 dst_sel:DWORD dst_unused:UNUSED_PAD src0_sel:WORD_1
	v_cvt_f32_f16_e32 v58, v116
	v_cvt_f32_f16_sdwa v57, v117 dst_sel:DWORD dst_unused:UNUSED_PAD src0_sel:WORD_1
	v_cvt_f32_f16_e32 v56, v117
	v_sub_f32_e32 v59, v59, v210
	v_sub_f32_e32 v58, v58, v210
	v_sub_f32_e32 v57, v57, v210
	v_sub_f32_e32 v56, v56, v210
	v_pk_add_f32 v[46:47], v[46:47], v[206:207]
	v_pk_add_f32 v[44:45], v[44:45], v[208:209]
	v_pk_mul_f32 v[58:59], v[210:211], v[58:59] op_sel:[1,0]
	v_pk_mul_f32 v[56:57], v[210:211], v[56:57] op_sel:[1,0]
	v_pk_fma_f32 v[44:45], v[92:93], v[58:59], v[44:45]
	v_pk_fma_f32 v[46:47], v[94:95], v[56:57], v[46:47]
	v_sub_f32_e32 v56, v99, v210
	v_sub_f32_e32 v57, v98, v210
	v_sub_f32_e32 v58, v97, v210
	v_sub_f32_e32 v59, v96, v210
	v_pk_add_f32 v[42:43], v[42:43], v[202:203]
	v_pk_add_f32 v[40:41], v[40:41], v[204:205]
	v_pk_mul_f32 v[58:59], v[210:211], v[58:59] op_sel:[1,0]
	v_pk_mul_f32 v[56:57], v[210:211], v[56:57] op_sel:[1,0]
	ds_write_b128 v235, v[48:51] offset:64
	v_pk_fma_f32 v[56:57], v[90:91], v[56:57], v[42:43]
	v_pk_fma_f32 v[42:43], v[88:89], v[58:59], v[40:41]
	v_cvt_f16_f32_e32 v58, v44
	v_cvt_f16_f32_e32 v59, v45
	v_cvt_pk_f16_f32 v40, v44, v45
	v_cvt_f16_f32_e32 v44, v46
	v_cvt_f16_f32_e32 v45, v47
	v_cvt_pk_f16_f32 v41, v46, v47
	v_cvt_f16_f32_e32 v46, v42
	v_cvt_f16_f32_e32 v47, v43
	v_cvt_f16_f32_e32 v96, v56
	v_cvt_f16_f32_e32 v97, v57
	v_cvt_pk_f16_f32 v42, v42, v43
	v_cvt_pk_f16_f32 v43, v56, v57
	ds_read_b128 v[48:51], v236
	ds_read_b128 v[52:55], v236 offset:1152
	ds_write_b128 v235, v[40:43]
	v_cvt_f32_f16_e32 v40, v58
	v_cvt_f32_f16_e32 v41, v59
	v_cvt_f32_f16_e32 v42, v44
	v_cvt_f32_f16_e32 v43, v45
	v_cvt_f32_f16_e32 v45, v46
	v_cvt_f32_f16_e32 v47, v47
	v_cvt_f32_f16_e32 v56, v96
	v_cvt_f32_f16_e32 v57, v97
	v_add_f32_e32 v40, v40, v41
	v_add_f32_e32 v42, v42, v43
	v_add_f32_e32 v40, v40, v42
	v_add_f32_e32 v42, v45, v47
	v_add_f32_e32 v45, v56, v57
	v_add_f32_e32 v42, v42, v45
	v_add_f32_e32 v40, v40, v42
	v_add_f32_e32 v45, 0, v40
	v_mul_f32_e32 v40, v41, v41
	v_mul_f32_e32 v41, v43, v43
	v_fma_mix_f32 v40, v58, v58, v40 op_sel_hi:[1,1,0]
	v_fma_mix_f32 v41, v44, v44, v41 op_sel_hi:[1,1,0]
	v_mul_f32_e32 v42, v57, v57
	v_add_f32_e32 v40, v40, v41
	v_mul_f32_e32 v41, v47, v47
	v_fma_mix_f32 v41, v46, v46, v41 op_sel_hi:[1,1,0]
	v_fma_mix_f32 v42, v96, v96, v42 op_sel_hi:[1,1,0]
	s_waitcnt vmcnt(16)
	v_cvt_f32_f16_sdwa v43, v112 dst_sel:DWORD dst_unused:UNUSED_PAD src0_sel:WORD_1
	v_add_f32_e32 v41, v41, v42
	v_add_f32_e32 v44, v40, v41
	v_cvt_f32_f16_e32 v42, v112
	v_cvt_f32_f16_sdwa v41, v113 dst_sel:DWORD dst_unused:UNUSED_PAD src0_sel:WORD_1
	v_cvt_f32_f16_e32 v40, v113
	v_cvt_f32_f16_sdwa v46, v114 dst_sel:DWORD dst_unused:UNUSED_PAD src0_sel:WORD_1
	v_cvt_f32_f16_e32 v47, v114
	v_cvt_f32_f16_sdwa v56, v115 dst_sel:DWORD dst_unused:UNUSED_PAD src0_sel:WORD_1
	v_cvt_f32_f16_e32 v57, v115
	v_sub_f32_e32 v40, v40, v210
	v_sub_f32_e32 v41, v41, v210
	v_sub_f32_e32 v42, v42, v210
	v_sub_f32_e32 v43, v43, v210
	v_pk_add_f32 v[38:39], v[38:39], v[198:199]
	v_pk_add_f32 v[36:37], v[36:37], v[200:201]
	v_pk_mul_f32 v[42:43], v[210:211], v[42:43] op_sel:[1,0]
	v_pk_mul_f32 v[40:41], v[210:211], v[40:41] op_sel:[1,0]
	v_pk_fma_f32 v[36:37], v[80:81], v[42:43], v[36:37]
	v_pk_fma_f32 v[38:39], v[82:83], v[40:41], v[38:39]
	v_sub_f32_e32 v40, v57, v210
	v_sub_f32_e32 v41, v56, v210
	v_sub_f32_e32 v42, v47, v210
	v_sub_f32_e32 v43, v46, v210
	v_pk_add_f32 v[34:35], v[34:35], v[192:193]
	v_pk_add_f32 v[32:33], v[32:33], v[194:195]
	v_pk_mul_f32 v[42:43], v[210:211], v[42:43] op_sel:[1,0]
	v_pk_mul_f32 v[40:41], v[210:211], v[40:41] op_sel:[1,0]
	ds_bpermute_b32 v62, v237, v60
	v_pk_fma_f32 v[40:41], v[74:75], v[40:41], v[34:35]
	v_pk_fma_f32 v[34:35], v[72:73], v[42:43], v[32:33]
	v_cvt_f16_f32_e32 v42, v36
	v_cvt_f16_f32_e32 v43, v37
	v_cvt_pk_f16_f32 v32, v36, v37
	v_cvt_f16_f32_e32 v36, v38
	v_cvt_f16_f32_e32 v37, v39
	v_cvt_pk_f16_f32 v33, v38, v39
	v_cvt_f16_f32_e32 v39, v35
	v_cvt_f16_f32_e32 v47, v41
	v_cvt_f16_f32_e32 v38, v34
	v_cvt_f16_f32_e32 v46, v40
	v_cvt_f32_f16_e32 v57, v36
	v_cvt_f32_f16_e32 v37, v37
	v_cvt_f32_f16_e32 v39, v39
	v_cvt_f32_f16_e32 v56, v42
	v_cvt_f32_f16_e32 v43, v43
	v_cvt_f32_f16_e32 v47, v47
	v_cvt_f32_f16_e32 v58, v38
	v_cvt_f32_f16_e32 v59, v46
	v_add_f32_e32 v57, v57, v37
	v_mul_f32_e32 v37, v37, v37
	v_fma_mix_f32 v36, v36, v36, v37 op_sel_hi:[1,1,0]
	v_mul_f32_e32 v37, v39, v39
	v_add_f32_e32 v56, v56, v43
	v_mul_f32_e32 v43, v43, v43
	v_fma_mix_f32 v37, v38, v38, v37 op_sel_hi:[1,1,0]
	v_mul_f32_e32 v38, v47, v47
	v_add_f32_e32 v56, v56, v57
	v_add_f32_e32 v57, v58, v39
	v_add_f32_e32 v58, v59, v47
	v_fma_mix_f32 v42, v42, v42, v43 op_sel_hi:[1,1,0]
	v_fma_mix_f32 v38, v46, v46, v38 op_sel_hi:[1,1,0]
	v_add_f32_e32 v57, v57, v58
	v_add_f32_e32 v36, v42, v36
	v_add_f32_e32 v37, v37, v38
	v_add_f32_e32 v56, v56, v57
	v_add_f32_e32 v36, v36, v37
	v_add_f32_e32 v45, v45, v56
	v_add_f32_e32 v36, v44, v36
	ds_bpermute_b32 v37, v221, v45
	ds_bpermute_b32 v38, v221, v36
	v_cvt_pk_f16_f32 v34, v34, v35
	v_cvt_pk_f16_f32 v35, v40, v41
	ds_write_b128 v235, v[32:35] offset:64
	s_waitcnt lgkmcnt(2)
	v_add_f32_e32 v32, v45, v37
	s_waitcnt lgkmcnt(1)
	v_add_f32_e32 v33, v36, v38
	ds_bpermute_b32 v63, v237, v61
	ds_bpermute_b32 v44, v237, v32
	ds_bpermute_b32 v45, v237, v33
	ds_read_b128 v[34:37], v236
	ds_read_b128 v[38:41], v236 offset:1152
	v_add_f32_e32 v42, v60, v62
	s_waitcnt lgkmcnt(4)
	v_add_f32_e32 v43, v61, v63
	s_waitcnt lgkmcnt(3)
	v_add_f32_e32 v44, v32, v44
	s_waitcnt lgkmcnt(2)
	v_add_f32_e32 v45, v33, v45
	v_add_u32_e32 v32, 0x30000, v144
	buffer_store_dwordx4 v[48:51], v32, s[24:27], 0 offen nt
	v_add_u32_e32 v32, 0x33000, v144
	buffer_store_dwordx4 v[52:55], v32, s[24:27], 0 offen nt
	v_add_co_u32_e32 v32, vcc, s76, v140
	s_nop 1
	v_addc_co_u32_e32 v33, vcc, 0, v141, vcc
	global_store_dwordx2 v[32:33], v[42:43], off
	v_add_u32_e32 v42, 0x36000, v144
	s_waitcnt lgkmcnt(1)
	buffer_store_dwordx4 v[34:37], v42, s[24:27], 0 offen nt
	s_nop 1
	v_add_u32_e32 v34, 0x39000, v144
	s_waitcnt lgkmcnt(0)
	buffer_store_dwordx4 v[38:41], v34, s[24:27], 0 offen nt
	global_store_dwordx2 v[32:33], v[44:45], off offset:1536
	s_waitcnt vmcnt(15)
	v_cvt_f32_f16_sdwa v37, v84 dst_sel:DWORD dst_unused:UNUSED_PAD src0_sel:WORD_1
	v_cvt_f32_f16_e32 v36, v84
	v_cvt_f32_f16_sdwa v35, v85 dst_sel:DWORD dst_unused:UNUSED_PAD src0_sel:WORD_1
	v_cvt_f32_f16_e32 v34, v85
	v_cvt_f32_f16_sdwa v38, v86 dst_sel:DWORD dst_unused:UNUSED_PAD src0_sel:WORD_1
	v_cvt_f32_f16_e32 v39, v86
	v_cvt_f32_f16_sdwa v40, v87 dst_sel:DWORD dst_unused:UNUSED_PAD src0_sel:WORD_1
	v_cvt_f32_f16_e32 v41, v87
	v_sub_f32_e32 v34, v34, v196
	v_sub_f32_e32 v35, v35, v196
	v_sub_f32_e32 v36, v36, v196
	v_sub_f32_e32 v37, v37, v196
	v_pk_add_f32 v[30:31], v[30:31], v[206:207]
	v_pk_add_f32 v[28:29], v[28:29], v[208:209]
	v_pk_mul_f32 v[36:37], v[196:197], v[36:37] op_sel:[1,0]
	v_pk_mul_f32 v[34:35], v[196:197], v[34:35] op_sel:[1,0]
	v_pk_fma_f32 v[28:29], v[92:93], v[36:37], v[28:29]
	v_pk_fma_f32 v[30:31], v[94:95], v[34:35], v[30:31]
	v_sub_f32_e32 v34, v41, v196
	v_sub_f32_e32 v35, v40, v196
	v_sub_f32_e32 v36, v39, v196
	v_sub_f32_e32 v37, v38, v196
	v_pk_add_f32 v[26:27], v[26:27], v[202:203]
	v_pk_add_f32 v[24:25], v[24:25], v[204:205]
	v_pk_mul_f32 v[36:37], v[196:197], v[36:37] op_sel:[1,0]
	v_pk_mul_f32 v[34:35], v[196:197], v[34:35] op_sel:[1,0]
	v_pk_add_f32 v[22:23], v[22:23], v[198:199]
	v_pk_fma_f32 v[34:35], v[90:91], v[34:35], v[26:27]
	v_pk_fma_f32 v[26:27], v[88:89], v[36:37], v[24:25]
	v_cvt_f16_f32_e32 v36, v28
	v_cvt_f16_f32_e32 v37, v29
	v_cvt_pk_f16_f32 v24, v28, v29
	v_cvt_f16_f32_e32 v28, v30
	v_cvt_f16_f32_e32 v29, v31
	v_cvt_pk_f16_f32 v25, v30, v31
	v_cvt_f16_f32_e32 v30, v26
	v_cvt_f16_f32_e32 v31, v27
	v_cvt_f16_f32_e32 v38, v34
	v_cvt_f16_f32_e32 v39, v35
	v_cvt_pk_f16_f32 v26, v26, v27
	v_cvt_pk_f16_f32 v27, v34, v35
	ds_write_b128 v235, v[24:27]
	v_cvt_f32_f16_e32 v24, v36
	v_cvt_f32_f16_e32 v25, v37
	v_cvt_f32_f16_e32 v26, v28
	v_cvt_f32_f16_e32 v27, v29
	v_cvt_f32_f16_e32 v29, v30
	v_cvt_f32_f16_e32 v31, v31
	v_cvt_f32_f16_e32 v34, v38
	v_cvt_f32_f16_e32 v35, v39
	v_add_f32_e32 v24, v24, v25
	v_add_f32_e32 v26, v26, v27
	v_add_f32_e32 v24, v24, v26
	v_add_f32_e32 v26, v29, v31
	v_add_f32_e32 v29, v34, v35
	v_add_f32_e32 v26, v26, v29
	v_add_f32_e32 v24, v24, v26
	v_add_f32_e32 v29, 0, v24
	v_mul_f32_e32 v24, v25, v25
	v_mul_f32_e32 v25, v27, v27
	v_fma_mix_f32 v24, v36, v36, v24 op_sel_hi:[1,1,0]
	v_fma_mix_f32 v25, v28, v28, v25 op_sel_hi:[1,1,0]
	v_mul_f32_e32 v26, v35, v35
	v_add_f32_e32 v24, v24, v25
	v_mul_f32_e32 v25, v31, v31
	v_fma_mix_f32 v25, v30, v30, v25 op_sel_hi:[1,1,0]
	v_fma_mix_f32 v26, v38, v38, v26 op_sel_hi:[1,1,0]
	s_waitcnt vmcnt(14)
	v_cvt_f32_f16_sdwa v27, v76 dst_sel:DWORD dst_unused:UNUSED_PAD src0_sel:WORD_1
	v_add_f32_e32 v25, v25, v26
	v_add_f32_e32 v28, v24, v25
	v_cvt_f32_f16_e32 v26, v76
	v_cvt_f32_f16_sdwa v25, v77 dst_sel:DWORD dst_unused:UNUSED_PAD src0_sel:WORD_1
	v_cvt_f32_f16_e32 v24, v77
	v_cvt_f32_f16_sdwa v30, v78 dst_sel:DWORD dst_unused:UNUSED_PAD src0_sel:WORD_1
	v_cvt_f32_f16_e32 v31, v78
	v_cvt_f32_f16_sdwa v34, v79 dst_sel:DWORD dst_unused:UNUSED_PAD src0_sel:WORD_1
	v_cvt_f32_f16_e32 v35, v79
	v_sub_f32_e32 v24, v24, v196
	v_sub_f32_e32 v25, v25, v196
	v_sub_f32_e32 v26, v26, v196
	v_sub_f32_e32 v27, v27, v196
	v_pk_add_f32 v[20:21], v[20:21], v[200:201]
	v_pk_mul_f32 v[26:27], v[196:197], v[26:27] op_sel:[1,0]
	v_pk_mul_f32 v[24:25], v[196:197], v[24:25] op_sel:[1,0]
	v_pk_fma_f32 v[20:21], v[80:81], v[26:27], v[20:21]
	v_pk_fma_f32 v[22:23], v[82:83], v[24:25], v[22:23]
	v_sub_f32_e32 v24, v35, v196
	v_sub_f32_e32 v25, v34, v196
	v_sub_f32_e32 v26, v31, v196
	v_sub_f32_e32 v27, v30, v196
	v_pk_add_f32 v[18:19], v[18:19], v[192:193]
	v_pk_add_f32 v[16:17], v[16:17], v[194:195]
	v_pk_mul_f32 v[26:27], v[196:197], v[26:27] op_sel:[1,0]
	v_pk_mul_f32 v[24:25], v[196:197], v[24:25] op_sel:[1,0]
	s_waitcnt vmcnt(13)
	v_cvt_f32_f16_sdwa v36, v71 dst_sel:DWORD dst_unused:UNUSED_PAD src0_sel:WORD_1
	v_pk_fma_f32 v[24:25], v[74:75], v[24:25], v[18:19]
	v_pk_fma_f32 v[18:19], v[72:73], v[26:27], v[16:17]
	v_cvt_f16_f32_e32 v26, v20
	v_cvt_f16_f32_e32 v27, v21
	v_cvt_pk_f16_f32 v16, v20, v21
	v_cvt_f16_f32_e32 v20, v22
	v_cvt_f16_f32_e32 v21, v23
	v_cvt_pk_f16_f32 v17, v22, v23
	v_cvt_f16_f32_e32 v23, v19
	v_cvt_f16_f32_e32 v31, v25
	v_cvt_f16_f32_e32 v22, v18
	v_cvt_f16_f32_e32 v30, v24
	v_cvt_pk_f16_f32 v18, v18, v19
	v_cvt_pk_f16_f32 v19, v24, v25
	v_cvt_f32_f16_e32 v25, v27
	v_cvt_f32_f16_e32 v27, v20
	v_cvt_f32_f16_e32 v21, v21
	v_cvt_f32_f16_e32 v23, v23
	v_cvt_f32_f16_e32 v24, v26
	v_cvt_f32_f16_e32 v31, v31
	v_cvt_f32_f16_e32 v34, v22
	v_cvt_f32_f16_e32 v35, v30
	v_add_f32_e32 v27, v27, v21
	v_mul_f32_e32 v21, v21, v21
	v_fma_mix_f32 v20, v20, v20, v21 op_sel_hi:[1,1,0]
	v_mul_f32_e32 v21, v23, v23
	v_add_f32_e32 v24, v24, v25
	v_mul_f32_e32 v25, v25, v25
	v_fma_mix_f32 v21, v22, v22, v21 op_sel_hi:[1,1,0]
	v_mul_f32_e32 v22, v31, v31
	v_add_f32_e32 v24, v24, v27
	v_add_f32_e32 v27, v34, v23
	v_add_f32_e32 v34, v35, v31
	v_fma_mix_f32 v25, v26, v26, v25 op_sel_hi:[1,1,0]
	v_fma_mix_f32 v22, v30, v30, v22 op_sel_hi:[1,1,0]
	v_add_f32_e32 v27, v27, v34
	v_add_f32_e32 v20, v25, v20
	v_add_f32_e32 v21, v21, v22
	v_add_f32_e32 v24, v24, v27
	v_add_f32_e32 v20, v20, v21
	v_add_f32_e32 v24, v29, v24
	v_add_f32_e32 v25, v28, v20
	ds_bpermute_b32 v26, v221, v24
	ds_bpermute_b32 v27, v221, v25
	v_cvt_f32_f16_sdwa v34, v70 dst_sel:DWORD dst_unused:UNUSED_PAD src0_sel:WORD_1
	v_cvt_f32_f16_e32 v35, v70
	v_cvt_f32_f16_e32 v37, v71
	s_waitcnt lgkmcnt(1)
	v_add_f32_e32 v28, v24, v26
	s_waitcnt lgkmcnt(0)
	v_add_f32_e32 v29, v25, v27
	v_cvt_f32_f16_sdwa v27, v68 dst_sel:DWORD dst_unused:UNUSED_PAD src0_sel:WORD_1
	v_cvt_f32_f16_e32 v26, v68
	v_cvt_f32_f16_sdwa v25, v69 dst_sel:DWORD dst_unused:UNUSED_PAD src0_sel:WORD_1
	v_cvt_f32_f16_e32 v24, v69
	v_sub_f32_e32 v27, v27, v190
	v_sub_f32_e32 v26, v26, v190
	v_sub_f32_e32 v25, v25, v190
	v_sub_f32_e32 v24, v24, v190
	v_pk_add_f32 v[14:15], v[14:15], v[206:207]
	v_pk_add_f32 v[12:13], v[12:13], v[208:209]
	v_pk_mul_f32 v[26:27], v[190:191], v[26:27] op_sel:[1,0]
	v_pk_mul_f32 v[24:25], v[190:191], v[24:25] op_sel:[1,0]
	v_pk_fma_f32 v[12:13], v[92:93], v[26:27], v[12:13]
	v_pk_fma_f32 v[14:15], v[94:95], v[24:25], v[14:15]
	v_sub_f32_e32 v24, v37, v190
	v_sub_f32_e32 v25, v36, v190
	v_sub_f32_e32 v26, v35, v190
	v_sub_f32_e32 v27, v34, v190
	v_pk_add_f32 v[10:11], v[10:11], v[202:203]
	v_pk_add_f32 v[8:9], v[8:9], v[204:205]
	v_pk_mul_f32 v[26:27], v[190:191], v[26:27] op_sel:[1,0]
	v_pk_mul_f32 v[24:25], v[190:191], v[24:25] op_sel:[1,0]
	ds_write_b128 v235, v[16:19] offset:64
	v_pk_fma_f32 v[24:25], v[90:91], v[24:25], v[10:11]
	v_pk_fma_f32 v[10:11], v[88:89], v[26:27], v[8:9]
	v_cvt_f16_f32_e32 v26, v12
	v_cvt_f16_f32_e32 v27, v13
	v_cvt_pk_f16_f32 v8, v12, v13
	v_cvt_f16_f32_e32 v12, v14
	v_cvt_f16_f32_e32 v13, v15
	v_cvt_pk_f16_f32 v9, v14, v15
	v_cvt_f16_f32_e32 v14, v10
	v_cvt_f16_f32_e32 v15, v11
	v_cvt_f16_f32_e32 v34, v24
	v_cvt_f16_f32_e32 v35, v25
	v_cvt_pk_f16_f32 v10, v10, v11
	v_cvt_pk_f16_f32 v11, v24, v25
	ds_read_b128 v[16:19], v236
	ds_read_b128 v[20:23], v236 offset:1152
	ds_write_b128 v235, v[8:11]
	v_cvt_f32_f16_e32 v8, v26
	v_cvt_f32_f16_e32 v9, v27
	v_cvt_f32_f16_e32 v10, v12
	v_cvt_f32_f16_e32 v11, v13
	v_cvt_f32_f16_e32 v13, v14
	v_cvt_f32_f16_e32 v15, v15
	v_cvt_f32_f16_e32 v24, v34
	v_cvt_f32_f16_e32 v25, v35
	v_add_f32_e32 v8, v8, v9
	v_add_f32_e32 v10, v10, v11
	v_add_f32_e32 v8, v8, v10
	v_add_f32_e32 v10, v13, v15
	v_add_f32_e32 v13, v24, v25
	v_add_f32_e32 v10, v10, v13
	v_add_f32_e32 v8, v8, v10
	v_add_f32_e32 v13, 0, v8
	v_mul_f32_e32 v8, v9, v9
	v_mul_f32_e32 v9, v11, v11
	v_fma_mix_f32 v8, v26, v26, v8 op_sel_hi:[1,1,0]
	v_fma_mix_f32 v9, v12, v12, v9 op_sel_hi:[1,1,0]
	v_mul_f32_e32 v10, v25, v25
	v_add_f32_e32 v8, v8, v9
	v_mul_f32_e32 v9, v15, v15
	v_fma_mix_f32 v9, v14, v14, v9 op_sel_hi:[1,1,0]
	v_fma_mix_f32 v10, v34, v34, v10 op_sel_hi:[1,1,0]
	s_waitcnt vmcnt(12)
	v_cvt_f32_f16_sdwa v11, v64 dst_sel:DWORD dst_unused:UNUSED_PAD src0_sel:WORD_1
	v_add_f32_e32 v9, v9, v10
	v_add_f32_e32 v12, v8, v9
	v_cvt_f32_f16_e32 v10, v64
	v_cvt_f32_f16_sdwa v9, v65 dst_sel:DWORD dst_unused:UNUSED_PAD src0_sel:WORD_1
	v_cvt_f32_f16_e32 v8, v65
	v_cvt_f32_f16_sdwa v14, v66 dst_sel:DWORD dst_unused:UNUSED_PAD src0_sel:WORD_1
	v_cvt_f32_f16_e32 v15, v66
	v_cvt_f32_f16_sdwa v24, v67 dst_sel:DWORD dst_unused:UNUSED_PAD src0_sel:WORD_1
	v_cvt_f32_f16_e32 v25, v67
	v_sub_f32_e32 v8, v8, v190
	v_sub_f32_e32 v9, v9, v190
	v_sub_f32_e32 v10, v10, v190
	v_sub_f32_e32 v11, v11, v190
	v_pk_add_f32 v[6:7], v[6:7], v[198:199]
	v_pk_add_f32 v[4:5], v[4:5], v[200:201]
	v_pk_mul_f32 v[10:11], v[190:191], v[10:11] op_sel:[1,0]
	v_pk_mul_f32 v[8:9], v[190:191], v[8:9] op_sel:[1,0]
	v_pk_fma_f32 v[4:5], v[80:81], v[10:11], v[4:5]
	v_pk_fma_f32 v[6:7], v[82:83], v[8:9], v[6:7]
	v_sub_f32_e32 v8, v25, v190
	v_sub_f32_e32 v9, v24, v190
	v_sub_f32_e32 v10, v15, v190
	v_sub_f32_e32 v11, v14, v190
	v_pk_add_f32 v[2:3], v[2:3], v[192:193]
	v_pk_add_f32 v[0:1], v[0:1], v[194:195]
	v_pk_mul_f32 v[10:11], v[190:191], v[10:11] op_sel:[1,0]
	v_pk_mul_f32 v[8:9], v[190:191], v[8:9] op_sel:[1,0]
	ds_bpermute_b32 v30, v237, v28
	v_pk_fma_f32 v[8:9], v[74:75], v[8:9], v[2:3]
	v_pk_fma_f32 v[2:3], v[72:73], v[10:11], v[0:1]
	v_cvt_f16_f32_e32 v10, v4
	v_cvt_f16_f32_e32 v11, v5
	v_cvt_pk_f16_f32 v0, v4, v5
	v_cvt_f16_f32_e32 v4, v6
	v_cvt_f16_f32_e32 v5, v7
	v_cvt_pk_f16_f32 v1, v6, v7
	v_cvt_f16_f32_e32 v7, v3
	v_cvt_f16_f32_e32 v15, v9
	v_cvt_f16_f32_e32 v6, v2
	v_cvt_f16_f32_e32 v14, v8
	v_cvt_f32_f16_e32 v25, v4
	v_cvt_f32_f16_e32 v5, v5
	v_cvt_f32_f16_e32 v7, v7
	v_cvt_f32_f16_e32 v24, v10
	v_cvt_f32_f16_e32 v11, v11
	v_cvt_f32_f16_e32 v15, v15
	v_cvt_f32_f16_e32 v26, v6
	v_cvt_f32_f16_e32 v27, v14
	v_add_f32_e32 v25, v25, v5
	v_mul_f32_e32 v5, v5, v5
	v_fma_mix_f32 v4, v4, v4, v5 op_sel_hi:[1,1,0]
	v_mul_f32_e32 v5, v7, v7
	v_add_f32_e32 v24, v24, v11
	v_mul_f32_e32 v11, v11, v11
	v_fma_mix_f32 v5, v6, v6, v5 op_sel_hi:[1,1,0]
	v_mul_f32_e32 v6, v15, v15
	v_add_f32_e32 v24, v24, v25
	v_add_f32_e32 v25, v26, v7
	v_add_f32_e32 v26, v27, v15
	v_fma_mix_f32 v10, v10, v10, v11 op_sel_hi:[1,1,0]
	v_fma_mix_f32 v6, v14, v14, v6 op_sel_hi:[1,1,0]
	v_add_f32_e32 v25, v25, v26
	v_add_f32_e32 v4, v10, v4
	v_add_f32_e32 v5, v5, v6
	v_add_f32_e32 v24, v24, v25
	v_add_f32_e32 v4, v4, v5
	v_add_f32_e32 v13, v13, v24
	v_add_f32_e32 v4, v12, v4
	ds_bpermute_b32 v5, v221, v13
	ds_bpermute_b32 v6, v221, v4
	v_cvt_pk_f16_f32 v2, v2, v3
	v_cvt_pk_f16_f32 v3, v8, v9
	ds_write_b128 v235, v[0:3] offset:64
	s_waitcnt lgkmcnt(2)
	v_add_f32_e32 v10, v13, v5
	s_waitcnt lgkmcnt(1)
	v_add_f32_e32 v11, v4, v6
	ds_bpermute_b32 v31, v237, v29
	ds_bpermute_b32 v12, v237, v10
	ds_bpermute_b32 v13, v237, v11
	ds_read_b128 v[0:3], v236
	ds_read_b128 v[4:7], v236 offset:1152
	v_add_f32_e32 v8, v28, v30
	s_waitcnt lgkmcnt(4)
	v_add_f32_e32 v9, v29, v31
	s_waitcnt lgkmcnt(3)
	v_add_f32_e32 v10, v10, v12
	s_waitcnt lgkmcnt(2)
	v_add_f32_e32 v11, v11, v13
	v_add_u32_e32 v12, 0x3c000, v144
	buffer_store_dwordx4 v[16:19], v12, s[24:27], 0 offen nt
	v_add_u32_e32 v12, 0x3f000, v144
	buffer_store_dwordx4 v[20:23], v12, s[24:27], 0 offen nt
	global_store_dwordx2 v[32:33], v[8:9], off offset:3072
	v_add_u32_e32 v8, 0x42000, v144
	s_waitcnt lgkmcnt(1)
	buffer_store_dwordx4 v[0:3], v8, s[24:27], 0 offen nt
	s_nop 1
	v_add_u32_e32 v0, 0x45000, v144
	s_waitcnt lgkmcnt(0)
	buffer_store_dwordx4 v[4:7], v0, s[24:27], 0 offen nt
	v_add_co_u32_e32 v0, vcc, 0x4000, v140
	s_nop 1
	v_addc_co_u32_e32 v1, vcc, 0, v141, vcc
	global_store_dwordx2 v[0:1], v[10:11], off offset:512
	s_mov_b32 s83, s81
	s_mov_b32 s84, s82
	s_mov_b64 s[40:41], s[0:1]
	s_mov_b64 s[38:39], s[8:9]
	s_mov_b64 vcc, s[6:7]
	s_cbranch_vccz .LBB10_12
	s_waitcnt vmcnt(0)
	s_cmpk_gt_u32 s44, 0xff
	s_cbranch_scc1 .LBB10_31
	s_barrier

.LBB10_32:
	s_endpgm
	s_endpgm
	s_endpgm
	.section	.rodata,"a",@progbits
	.p2align	6, 0x0
	.amdhsa_kernel _Z6k_gemmIN2pg6EpiResELi3072EEvNS0_4GemmET_
		.amdhsa_group_segment_fixed_size 0
		.amdhsa_private_segment_fixed_size 0
		.amdhsa_kernarg_size 344
		.amdhsa_user_sgpr_count 2
		.amdhsa_user_sgpr_dispatch_ptr 0
		.amdhsa_user_sgpr_queue_ptr 0
		.amdhsa_user_sgpr_kernarg_segment_ptr 1
		.amdhsa_user_sgpr_dispatch_id 0
		.amdhsa_user_sgpr_kernarg_preload_length 0
		.amdhsa_user_sgpr_kernarg_preload_offset 0
		.amdhsa_user_sgpr_private_segment_size 0
		.amdhsa_uses_dynamic_stack 0
		.amdhsa_enable_private_segment 0
		.amdhsa_system_sgpr_workgroup_id_x 1
		.amdhsa_system_sgpr_workgroup_id_y 0
		.amdhsa_system_sgpr_workgroup_id_z 0
		.amdhsa_system_sgpr_workgroup_info 0
		.amdhsa_system_vgpr_workitem_id 0
		.amdhsa_next_free_vgpr 254
		.amdhsa_next_free_sgpr 96
		.amdhsa_accum_offset 256
		.amdhsa_reserve_vcc 1
		.amdhsa_float_round_mode_32 0
		.amdhsa_float_round_mode_16_64 0
		.amdhsa_float_denorm_mode_32 3
		.amdhsa_float_denorm_mode_16_64 3
		.amdhsa_dx10_clamp 1
		.amdhsa_ieee_mode 1
		.amdhsa_fp16_overflow 0
		.amdhsa_tg_split 0
		.amdhsa_exception_fp_ieee_invalid_op 0
		.amdhsa_exception_fp_denorm_src 0
		.amdhsa_exception_fp_ieee_div_zero 0
		.amdhsa_exception_fp_ieee_overflow 0
		.amdhsa_exception_fp_ieee_underflow 0
		.amdhsa_exception_fp_ieee_inexact 0
		.amdhsa_exception_int_div_zero 0
	.end_amdhsa_kernel

amdhsa.kernels:
  - .agpr_count:     16
    .args:
      - .actual_access:  read_only
        .address_space:  global
        .offset:         0
        .size:           8
        .value_kind:     global_buffer
      - .actual_access:  read_only
        .address_space:  global
        .offset:         8
        .size:           8
        .value_kind:     global_buffer
      - .actual_access:  write_only
        .address_space:  global
        .offset:         16
        .size:           8
        .value_kind:     global_buffer
    .group_segment_fixed_size: 45056
    .kernarg_segment_align: 8
    .kernarg_segment_size: 24
    .language:       OpenCL C
    .language_version:
      - 2
      - 0
    .max_flat_workgroup_size: 256
    .name:           _Z6k_attnPKDF16_PKfPDF16_
    .private_segment_fixed_size: 0
    .sgpr_count:     16
    .sgpr_spill_count: 0
    .symbol:         _Z6k_attnPKDF16_PKfPDF16_.kd
    .uniform_work_group_size: 1
    .uses_dynamic_stack: false
    .vgpr_count:     84
    .vgpr_spill_count: 0
    .wavefront_size: 64
  - .agpr_count:     0
    .args:
      - .actual_access:  read_only
        .address_space:  global
        .offset:         0
        .size:           8
        .value_kind:     global_buffer
      - .actual_access:  read_only
        .address_space:  global
        .offset:         8
        .size:           8
        .value_kind:     global_buffer
      - .actual_access:  write_only
        .address_space:  global
        .offset:         16
        .size:           8
        .value_kind:     global_buffer
      - .actual_access:  write_only
        .address_space:  global
        .offset:         24
        .size:           8
        .value_kind:     global_buffer
      - .actual_access:  write_only
        .address_space:  global
        .offset:         32
        .size:           8
        .value_kind:     global_buffer
      - .actual_access:  write_only
        .address_space:  global
        .offset:         40
        .size:           8
        .value_kind:     global_buffer
    .group_segment_fixed_size: 0
    .kernarg_segment_align: 8
    .kernarg_segment_size: 48
    .language:       OpenCL C
    .language_version:
      - 2
      - 0
    .max_flat_workgroup_size: 256
    .name:           _Z11k_prep_miscPKiPKfPfPDv2_fS3_S3_
    .private_segment_fixed_size: 0
    .sgpr_count:     16
    .sgpr_spill_count: 0
    .symbol:         _Z11k_prep_miscPKiPKfPfPDv2_fS3_S3_.kd
    .uniform_work_group_size: 1
    .uses_dynamic_stack: false
    .vgpr_count:     6
    .vgpr_spill_count: 0
    .wavefront_size: 64
  - .agpr_count:     0
    .args:
      - .actual_access:  read_only
        .address_space:  global
        .offset:         0
        .size:           8
        .value_kind:     global_buffer
      - .actual_access:  write_only
        .address_space:  global
        .offset:         8
        .size:           8
        .value_kind:     global_buffer
    .group_segment_fixed_size: 0
    .kernarg_segment_align: 8
    .kernarg_segment_size: 16
    .language:       OpenCL C
    .language_version:
      - 2
      - 0
    .max_flat_workgroup_size: 256
    .name:           _Z7k_cvt_xPKfPDF16_
    .private_segment_fixed_size: 0
    .sgpr_count:     14
    .sgpr_spill_count: 0
    .symbol:         _Z7k_cvt_xPKfPDF16_.kd
    .uniform_work_group_size: 1
    .uses_dynamic_stack: false
    .vgpr_count:     12
    .vgpr_spill_count: 0
    .wavefront_size: 64
  - .agpr_count:     0
    .args:
      - .offset:         0
        .size:           176
        .value_kind:     by_value
    .group_segment_fixed_size: 9216
    .kernarg_segment_align: 8
    .kernarg_segment_size: 176
    .language:       OpenCL C
    .language_version:
      - 2
      - 0
    .max_flat_workgroup_size: 256
    .name:           _Z8k_wtrans8PrepArgs
    .private_segment_fixed_size: 0
    .sgpr_count:     44
    .sgpr_spill_count: 0
    .symbol:         _Z8k_wtrans8PrepArgs.kd
    .uniform_work_group_size: 1
    .uses_dynamic_stack: false
    .vgpr_count:     18
    .vgpr_spill_count: 0
    .wavefront_size: 64
  - .agpr_count:     0
    .args:
      - .offset:         0
        .size:           176
        .value_kind:     by_value
      - .actual_access:  read_only
        .address_space:  global
        .offset:         176
        .size:           8
        .value_kind:     global_buffer
      - .actual_access:  read_only
        .address_space:  global
        .offset:         184
        .size:           8
        .value_kind:     global_buffer
    .group_segment_fixed_size: 2048
    .kernarg_segment_align: 8
    .kernarg_segment_size: 192
    .language:       OpenCL C
    .language_version:
      - 2
      - 0
    .max_flat_workgroup_size: 256
    .name:           _Z8k_colvec8PrepArgsPKfS1_
    .private_segment_fixed_size: 0
    .sgpr_count:     38
    .sgpr_spill_count: 0
    .symbol:         _Z8k_colvec8PrepArgsPKfS1_.kd
    .uniform_work_group_size: 1
    .uses_dynamic_stack: false
    .vgpr_count:     114
    .vgpr_spill_count: 0
    .wavefront_size: 64
  - .agpr_count:     0
    .args:
      - .actual_access:  read_only
        .address_space:  global
        .offset:         0
        .size:           8
        .value_kind:     global_buffer
      - .actual_access:  write_only
        .address_space:  global
        .offset:         8
        .size:           8
        .value_kind:     global_buffer
    .group_segment_fixed_size: 0
    .kernarg_segment_align: 8
    .kernarg_segment_size: 16
    .language:       OpenCL C
    .language_version:
      - 2
      - 0
    .max_flat_workgroup_size: 256
    .name:           _Z9k_rowstatPKDv2_fPS_
    .private_segment_fixed_size: 0
    .sgpr_count:     14
    .sgpr_spill_count: 0
    .symbol:         _Z9k_rowstatPKDv2_fPS_.kd
    .uniform_work_group_size: 1
    .uses_dynamic_stack: false
    .vgpr_count:     28
    .vgpr_spill_count: 0
    .wavefront_size: 64
  - .agpr_count:     0
    .args:
      - .actual_access:  read_only
        .address_space:  global
        .offset:         0
        .size:           8
        .value_kind:     global_buffer
      - .actual_access:  read_only
        .address_space:  global
        .offset:         8
        .size:           8
        .value_kind:     global_buffer
      - .actual_access:  read_only
        .address_space:  global
        .offset:         16
        .size:           8
        .value_kind:     global_buffer
      - .actual_access:  read_only
        .address_space:  global
        .offset:         24
        .size:           8
        .value_kind:     global_buffer
      - .actual_access:  write_only
        .address_space:  global
        .offset:         32
        .size:           8
        .value_kind:     global_buffer
    .group_segment_fixed_size: 0
    .kernarg_segment_align: 8
    .kernarg_segment_size: 40
    .language:       OpenCL C
    .language_version:
      - 2
      - 0
    .max_flat_workgroup_size: 256
    .name:           _Z10k_final_lnPKDF16_PKDv2_fPKfS5_Pf
    .private_segment_fixed_size: 0
    .sgpr_count:     19
    .sgpr_spill_count: 0
    .symbol:         _Z10k_final_lnPKDF16_PKDv2_fPKfS5_Pf.kd
    .uniform_work_group_size: 1
    .uses_dynamic_stack: false
    .vgpr_count:     19
    .vgpr_spill_count: 0
    .wavefront_size: 64
  - .agpr_count:     0
    .args:
      - .offset:         0
        .size:           32
        .value_kind:     by_value
      - .offset:         32
        .size:           32
        .value_kind:     by_value
      - .offset:         64
        .size:           4
        .value_kind:     hidden_block_count_x
      - .offset:         68
        .size:           4
        .value_kind:     hidden_block_count_y
      - .offset:         72
        .size:           4
        .value_kind:     hidden_block_count_z
      - .offset:         76
        .size:           2
        .value_kind:     hidden_group_size_x
      - .offset:         78
        .size:           2
        .value_kind:     hidden_group_size_y
      - .offset:         80
        .size:           2
        .value_kind:     hidden_group_size_z
      - .offset:         82
        .size:           2
        .value_kind:     hidden_remainder_x
      - .offset:         84
        .size:           2
        .value_kind:     hidden_remainder_y
      - .offset:         86
        .size:           2
        .value_kind:     hidden_remainder_z
      - .offset:         104
        .size:           8
        .value_kind:     hidden_global_offset_x
      - .offset:         112
        .size:           8
        .value_kind:     hidden_global_offset_y
      - .offset:         120
        .size:           8
        .value_kind:     hidden_global_offset_z
      - .offset:         128
        .size:           2
        .value_kind:     hidden_grid_dims
      - .offset:         184
        .size:           4
        .value_kind:     hidden_dynamic_lds_size
    .group_segment_fixed_size: 0
    .kernarg_segment_align: 8
    .kernarg_segment_size: 320
    .language:       OpenCL C
    .language_version:
      - 2
      - 0
    .max_flat_workgroup_size: 512
    .name:           _Z6k_gemmIN2pg6EpiLinILi0EEELi768EEvNS0_4GemmET_
    .private_segment_fixed_size: 0
    .sgpr_count:     83
    .sgpr_spill_count: 0
    .symbol:         _Z6k_gemmIN2pg6EpiLinILi0EEELi768EEvNS0_4GemmET_.kd
    .uniform_work_group_size: 1
    .uses_dynamic_stack: false
    .vgpr_count:     254
    .vgpr_spill_count: 0
    .wavefront_size: 64
  - .agpr_count:     0
    .args:
      - .offset:         0
        .size:           32
        .value_kind:     by_value
      - .offset:         32
        .size:           56
        .value_kind:     by_value
      - .offset:         88
        .size:           4
        .value_kind:     hidden_block_count_x
      - .offset:         92
        .size:           4
        .value_kind:     hidden_block_count_y
      - .offset:         96
        .size:           4
        .value_kind:     hidden_block_count_z
      - .offset:         100
        .size:           2
        .value_kind:     hidden_group_size_x
      - .offset:         102
        .size:           2
        .value_kind:     hidden_group_size_y
      - .offset:         104
        .size:           2
        .value_kind:     hidden_group_size_z
      - .offset:         106
        .size:           2
        .value_kind:     hidden_remainder_x
      - .offset:         108
        .size:           2
        .value_kind:     hidden_remainder_y
      - .offset:         110
        .size:           2
        .value_kind:     hidden_remainder_z
      - .offset:         128
        .size:           8
        .value_kind:     hidden_global_offset_x
      - .offset:         136
        .size:           8
        .value_kind:     hidden_global_offset_y
      - .offset:         144
        .size:           8
        .value_kind:     hidden_global_offset_z
      - .offset:         152
        .size:           2
        .value_kind:     hidden_grid_dims
      - .offset:         208
        .size:           4
        .value_kind:     hidden_dynamic_lds_size
    .group_segment_fixed_size: 0
    .kernarg_segment_align: 8
    .kernarg_segment_size: 344
    .language:       OpenCL C
    .language_version:
      - 2
      - 0
    .max_flat_workgroup_size: 512
    .name:           _Z6k_gemmIN2pg6EpiResELi768EEvNS0_4GemmET_
    .private_segment_fixed_size: 0
    .sgpr_count:     102
    .sgpr_spill_count: 0
    .symbol:         _Z6k_gemmIN2pg6EpiResELi768EEvNS0_4GemmET_.kd
    .uniform_work_group_size: 1
    .uses_dynamic_stack: false
    .vgpr_count:     254
    .vgpr_spill_count: 0
    .wavefront_size: 64
  - .agpr_count:     0
    .args:
      - .offset:         0
        .size:           32
        .value_kind:     by_value
      - .offset:         32
        .size:           32
        .value_kind:     by_value
      - .offset:         64
        .size:           4
        .value_kind:     hidden_block_count_x
      - .offset:         68
        .size:           4
        .value_kind:     hidden_block_count_y
      - .offset:         72
        .size:           4
        .value_kind:     hidden_block_count_z
      - .offset:         76
        .size:           2
        .value_kind:     hidden_group_size_x
      - .offset:         78
        .size:           2
        .value_kind:     hidden_group_size_y
      - .offset:         80
        .size:           2
        .value_kind:     hidden_group_size_z
      - .offset:         82
        .size:           2
        .value_kind:     hidden_remainder_x
      - .offset:         84
        .size:           2
        .value_kind:     hidden_remainder_y
      - .offset:         86
        .size:           2
        .value_kind:     hidden_remainder_z
      - .offset:         104
        .size:           8
        .value_kind:     hidden_global_offset_x
      - .offset:         112
        .size:           8
        .value_kind:     hidden_global_offset_y
      - .offset:         120
        .size:           8
        .value_kind:     hidden_global_offset_z
      - .offset:         128
        .size:           2
        .value_kind:     hidden_grid_dims
      - .offset:         184
        .size:           4
        .value_kind:     hidden_dynamic_lds_size
    .group_segment_fixed_size: 0
    .kernarg_segment_align: 8
    .kernarg_segment_size: 320
    .language:       OpenCL C
    .language_version:
      - 2
      - 0
    .max_flat_workgroup_size: 512
    .name:           _Z6k_gemmIN2pg6EpiLinILi1EEELi768EEvNS0_4GemmET_
    .private_segment_fixed_size: 0
    .sgpr_count:     83
    .sgpr_spill_count: 0
    .symbol:         _Z6k_gemmIN2pg6EpiLinILi1EEELi768EEvNS0_4GemmET_.kd
    .uniform_work_group_size: 1
    .uses_dynamic_stack: false
    .vgpr_count:     254
    .vgpr_spill_count: 0
    .wavefront_size: 64
  - .agpr_count:     0
    .args:
      - .offset:         0
        .size:           32
        .value_kind:     by_value
      - .offset:         32
        .size:           56
        .value_kind:     by_value
      - .offset:         88
        .size:           4
        .value_kind:     hidden_block_count_x
      - .offset:         92
        .size:           4
        .value_kind:     hidden_block_count_y
      - .offset:         96
        .size:           4
        .value_kind:     hidden_block_count_z
      - .offset:         100
        .size:           2
        .value_kind:     hidden_group_size_x
      - .offset:         102
        .size:           2
        .value_kind:     hidden_group_size_y
      - .offset:         104
        .size:           2
        .value_kind:     hidden_group_size_z
      - .offset:         106
        .size:           2
        .value_kind:     hidden_remainder_x
      - .offset:         108
        .size:           2
        .value_kind:     hidden_remainder_y
      - .offset:         110
        .size:           2
        .value_kind:     hidden_remainder_z
      - .offset:         128
        .size:           8
        .value_kind:     hidden_global_offset_x
      - .offset:         136
        .size:           8
        .value_kind:     hidden_global_offset_y
      - .offset:         144
        .size:           8
        .value_kind:     hidden_global_offset_z
      - .offset:         152
        .size:           2
        .value_kind:     hidden_grid_dims
      - .offset:         208
        .size:           4
        .value_kind:     hidden_dynamic_lds_size
    .group_segment_fixed_size: 0
    .kernarg_segment_align: 8
    .kernarg_segment_size: 344
    .language:       OpenCL C
    .language_version:
      - 2
      - 0
    .max_flat_workgroup_size: 512
    .name:           _Z6k_gemmIN2pg6EpiResELi3072EEvNS0_4GemmET_
    .private_segment_fixed_size: 0
    .sgpr_count:     102
    .sgpr_spill_count: 0
    .symbol:         _Z6k_gemmIN2pg6EpiResELi3072EEvNS0_4GemmET_.kd
    .uniform_work_group_size: 1
    .uses_dynamic_stack: false
    .vgpr_count:     254
    .vgpr_spill_count: 0
    .wavefront_size: 64
